# GEMM K-loops: per-segment s_setprio toggling replaced by one static priority raise for the trailing half
# speedup vs baseline: 1.0009x; 1.0009x over previous
; #define PG8_STAGE(bufoff, gbase, voff) do { _Pragma("unroll") for (int _i = 0; _i < 2; ++_i) \
;         __builtin_amdgcn_global_load_lds((const unsigned*)((const char*)(gbase) + (voff)[_i]), (PG8_LAS unsigned*)(lds + (bufoff) + ldsw + _i * 8192), 16, 0, 0); } while (0)
; #define PG8_LDA(dst, b, h) do { _Pragma("unroll") for (int m = 0; m < 4; ++m) _Pragma("unroll") for (int k = 0; k < 2; ++k) dst[m][k] = *(const PG8_LAS bf16x8*)(lds + PG8_SA(b, h) + aoff + m * 2048 + k * 1024); } while (0)
; #define PG8_LDB(dst, b, h) do { _Pragma("unroll") for (int n = 0; n < 2; ++n) _Pragma("unroll") for (int k = 0; k < 2; ++k) dst[n][k] = *(const PG8_LAS bf16x8*)(lds + PG8_SB(b, h) + boff + n * 2048 + k * 1024); } while (0)
; #define PG8_MMA(ai, bj, At, Bt) do { __builtin_amdgcn_s_setprio(1); _Pragma("unroll") for (int m = 0; m < 4; ++m) _Pragma("unroll") for (int n = 0; n < 2; ++n) _Pragma("unroll") for (int k = 0; k < 2; ++k) \
;         acc[ai][bj][m][n] = __builtin_amdgcn_mfma_f32_16x16x32_bf16(Bt[n][k], At[m][k], acc[ai][bj][m][n], 0, 0, 0); __builtin_amdgcn_s_setprio(0); } while (0)
; #define PG8_BAR __builtin_amdgcn_s_barrier()
; template <class Epi, class Sched, bool ALIGN_EPI = false, bool SP2 = false>
; __device__ __forceinline__ void gemm_phase(PG8_LAS unsigned char* lds, const Gemm g, const Sched& S, const Epi& E, const int tid) {
;     ...
;         for (int t = 0; t < nt; t += 2) {
;             const bool last = (t == nt - 2);
;             const char* a1 = cA + (size_t)(t + 1) * kstep;
;             const char* a2 = last ? nA : cA + (size_t)(t + 2) * kstep; const char* b2 = last ? nB : cB + (size_t)(t + 2) * kstep;
;             const char* a3 = a2 + kstep; const char* b3 = b2 + kstep;
;             if (last && has_next) S.a_ready(nxt);
;             if constexpr (SP2) {
;             PG8_LDB(B0, 0, 0); PG8_LDB(B1, 0, 1); PG8_SCHED; PG8_LDA(At, 0, 0); PG8_STAGE(PG8_SA(1, 1), a1 + hstep, voffA);
;             PG8_WAIT_V(8); PG8_WAIT_L(0); PG8_BAR; PG8_MMA(0, 0, At, B0); PG8_MMA(0, 1, At, B1); PG8_BAR; PG8_SCHED;
;     ...
; #pragma unroll
;         for (int a = 0; a < 2; ++a)
; #pragma unroll
;             for (int b = 0; b < 2; ++b)
; #pragma unroll
;                 for (int m = 0; m < 4; ++m)
; #pragma unroll
;                     for (int n = 0; n < 2; ++n) acc[a][b][m][n] = (f32x4){0.f, 0.f, 0.f, 0.f};
;         cur = nxt; cA = nA; cB = nB; ++ui; nt = cur.nt;
.LBB0_756:
	s_ashr_i32 s75, s74, 31
	s_lshl_b64 s[10:11], s[74:75], 20
	s_add_u32 s78, s59, s10
	s_addc_u32 s79, s31, s11
	s_and_b64 s[10:11], s[76:77], exec
	s_cselect_b32 s1, s79, s41
	s_cselect_b32 s2, s78, s40
	s_ashr_i32 s73, s72, 31
	s_lshl_b64 s[10:11], s[72:73], 20
	s_add_u32 s80, s48, s10
	s_addc_u32 s81, s27, s11
	s_and_b64 s[10:11], s[76:77], exec
	s_cselect_b32 s5, s81, s7
	s_cselect_b32 s10, s80, s6
	s_add_u32 s40, s40, 0x80080
	s_addc_u32 s41, s41, 0
	s_add_u32 s11, s6, 0x100
	s_waitcnt vmcnt(0)
	v_mov_b32_e32 v2, 0
	s_addc_u32 s12, s7, 0
	s_mov_b32 s13, -2
	v_mov_b32_e32 v3, v2
	v_mov_b32_e32 v4, v2
	v_mov_b32_e32 v5, v2
	v_mov_b32_e32 v6, v2
	v_mov_b32_e32 v7, v2
	v_mov_b32_e32 v8, v2
	v_mov_b32_e32 v9, v2
	v_mov_b32_e32 v10, v2
	v_mov_b32_e32 v11, v2
	v_mov_b32_e32 v12, v2
	v_mov_b32_e32 v13, v2
	v_mov_b32_e32 v18, v2
	v_mov_b32_e32 v19, v2
	v_mov_b32_e32 v20, v2
	v_mov_b32_e32 v21, v2
	v_mov_b32_e32 v26, v2
	v_mov_b32_e32 v27, v2
	v_mov_b32_e32 v28, v2
	v_mov_b32_e32 v29, v2
	v_mov_b32_e32 v34, v2
	v_mov_b32_e32 v35, v2
	v_mov_b32_e32 v36, v2
	v_mov_b32_e32 v37, v2
	v_mov_b32_e32 v42, v2
	v_mov_b32_e32 v43, v2
	v_mov_b32_e32 v44, v2
	v_mov_b32_e32 v45, v2
	v_mov_b32_e32 v50, v2
	v_mov_b32_e32 v51, v2
	v_mov_b32_e32 v52, v2
	v_mov_b32_e32 v53, v2
	v_mov_b32_e32 v14, v2
	v_mov_b32_e32 v15, v2
	v_mov_b32_e32 v16, v2
	v_mov_b32_e32 v17, v2
	v_mov_b32_e32 v22, v2
	v_mov_b32_e32 v23, v2
	v_mov_b32_e32 v24, v2
	v_mov_b32_e32 v25, v2
	v_mov_b32_e32 v30, v2
	v_mov_b32_e32 v31, v2
	v_mov_b32_e32 v32, v2
	v_mov_b32_e32 v33, v2
	v_mov_b32_e32 v38, v2
	v_mov_b32_e32 v39, v2
	v_mov_b32_e32 v40, v2
	v_mov_b32_e32 v41, v2
	v_mov_b32_e32 v46, v2
	v_mov_b32_e32 v47, v2
	v_mov_b32_e32 v48, v2
	v_mov_b32_e32 v49, v2
	v_mov_b32_e32 v54, v2
	v_mov_b32_e32 v55, v2
	v_mov_b32_e32 v56, v2
	v_mov_b32_e32 v57, v2
	v_mov_b32_e32 v58, v2
	v_mov_b32_e32 v59, v2
	v_mov_b32_e32 v60, v2
	v_mov_b32_e32 v61, v2
	v_mov_b32_e32 v62, v2
	v_mov_b32_e32 v63, v2
	v_mov_b32_e32 v64, v2
	v_mov_b32_e32 v65, v2
	v_mov_b32_e32 v66, v2
	v_mov_b32_e32 v67, v2
	v_mov_b32_e32 v68, v2
	v_mov_b32_e32 v69, v2
	v_mov_b32_e32 v70, v2
	v_mov_b32_e32 v71, v2
	v_mov_b32_e32 v72, v2
	v_mov_b32_e32 v73, v2
	v_mov_b32_e32 v74, v2
	v_mov_b32_e32 v75, v2
	v_mov_b32_e32 v76, v2
	v_mov_b32_e32 v77, v2
	v_mov_b32_e32 v82, v2
	v_mov_b32_e32 v83, v2
	v_mov_b32_e32 v84, v2
	v_mov_b32_e32 v85, v2
	v_mov_b32_e32 v90, v2
	v_mov_b32_e32 v91, v2
	v_mov_b32_e32 v92, v2
	v_mov_b32_e32 v93, v2
	v_mov_b32_e32 v98, v2
	v_mov_b32_e32 v99, v2
	v_mov_b32_e32 v100, v2
	v_mov_b32_e32 v101, v2
	v_mov_b32_e32 v106, v2
	v_mov_b32_e32 v107, v2
	v_mov_b32_e32 v108, v2
	v_mov_b32_e32 v109, v2
	v_mov_b32_e32 v114, v2
	v_mov_b32_e32 v115, v2
	v_mov_b32_e32 v116, v2
	v_mov_b32_e32 v117, v2
	v_mov_b32_e32 v78, v2
	v_mov_b32_e32 v79, v2
	v_mov_b32_e32 v80, v2
	v_mov_b32_e32 v81, v2
	v_mov_b32_e32 v86, v2
	v_mov_b32_e32 v87, v2
	v_mov_b32_e32 v88, v2
	v_mov_b32_e32 v89, v2
	v_mov_b32_e32 v94, v2
	v_mov_b32_e32 v95, v2
	v_mov_b32_e32 v96, v2
	v_mov_b32_e32 v97, v2
	v_mov_b32_e32 v102, v2
	v_mov_b32_e32 v103, v2
	v_mov_b32_e32 v104, v2
	v_mov_b32_e32 v105, v2
	v_mov_b32_e32 v110, v2
	v_mov_b32_e32 v111, v2
	v_mov_b32_e32 v112, v2
	v_mov_b32_e32 v113, v2
	v_mov_b32_e32 v118, v2
	v_mov_b32_e32 v119, v2
	v_mov_b32_e32 v120, v2
	v_mov_b32_e32 v121, v2
	v_mov_b32_e32 v122, v2
	v_mov_b32_e32 v123, v2
	v_mov_b32_e32 v124, v2
	v_mov_b32_e32 v125, v2
	v_mov_b32_e32 v126, v2
	v_mov_b32_e32 v127, v2
	v_mov_b32_e32 v128, v2
	v_mov_b32_e32 v129, v2
	s_cmp_eq_u64 s[70:71], 0
	s_cbranch_scc0 .Lsp_skip_757
	s_setprio 1
.Lsp_skip_757:
.LBB0_757:
	s_add_u32 s6, s40, 0xfff80080
	s_addc_u32 s7, s41, -1
	s_add_i32 s15, 0, 0x10000
	s_cmp_eq_u32 s13, 28
	s_cselect_b32 s69, s1, s7
	s_cselect_b32 s68, s2, s6
	v_add_u32_e32 v131, s15, v152
	s_cselect_b32 s7, s5, s12
	s_cselect_b32 s6, s10, s11
	s_add_i32 s16, 0, 0x14000
	ds_read_b128 v[164:167], v131
	ds_read_b128 v[168:171], v131 offset:1024
	ds_read_b128 v[172:175], v131 offset:2048
	ds_read_b128 v[176:179], v131 offset:3072
	v_add_u32_e32 v131, s16, v152
	ds_read_b128 v[180:183], v131
	ds_read_b128 v[184:187], v131 offset:1024
	ds_read_b128 v[188:191], v131 offset:2048
	ds_read_b128 v[192:195], v131 offset:3072
	v_lshl_add_u64 v[132:133], s[40:41], 0, v[144:145]
	s_add_i32 m0, s46, 0xc000
	ds_read_b128 v[198:201], v163
	ds_read_b128 v[202:205], v163 offset:1024
	ds_read_b128 v[206:209], v163 offset:2048
	ds_read_b128 v[210:213], v163 offset:3072
	ds_read_b128 v[214:217], v163 offset:4096
	ds_read_b128 v[218:221], v163 offset:5120
	ds_read_b128 v[222:225], v163 offset:6144
	ds_read_b128 v[226:229], v163 offset:7168
	global_load_lds_dwordx4 v[132:133], off
	v_lshl_add_u64 v[132:133], s[40:41], 0, v[146:147]
	s_add_i32 m0, s46, 0xe000
	s_nop 0
	global_load_lds_dwordx4 v[132:133], off
	s_waitcnt vmcnt(8)
	s_waitcnt lgkmcnt(0)
	s_barrier
; #define PG8_STAGE(bufoff, gbase, voff) do { _Pragma("unroll") for (int _i = 0; _i < 2; ++_i) \
;         __builtin_amdgcn_global_load_lds((const unsigned*)((const char*)(gbase) + (voff)[_i]), (PG8_LAS unsigned*)(lds + (bufoff) + ldsw + _i * 8192), 16, 0, 0); } while (0)
; #define PG8_LDA(dst, b, h) do { _Pragma("unroll") for (int m = 0; m < 4; ++m) _Pragma("unroll") for (int k = 0; k < 2; ++k) dst[m][k] = *(const PG8_LAS bf16x8*)(lds + PG8_SA(b, h) + aoff + m * 2048 + k * 1024); } while (0)
; #define PG8_LDB(dst, b, h) do { _Pragma("unroll") for (int n = 0; n < 2; ++n) _Pragma("unroll") for (int k = 0; k < 2; ++k) dst[n][k] = *(const PG8_LAS bf16x8*)(lds + PG8_SB(b, h) + boff + n * 2048 + k * 1024); } while (0)
; #define PG8_MMA(ai, bj, At, Bt) do { __builtin_amdgcn_s_setprio(1); _Pragma("unroll") for (int m = 0; m < 4; ++m) _Pragma("unroll") for (int n = 0; n < 2; ++n) _Pragma("unroll") for (int k = 0; k < 2; ++k) \
;         acc[ai][bj][m][n] = __builtin_amdgcn_mfma_f32_16x16x32_bf16(Bt[n][k], At[m][k], acc[ai][bj][m][n], 0, 0, 0); __builtin_amdgcn_s_setprio(0); } while (0)
; #define PG8_WAIT_V(n) asm volatile("s_waitcnt vmcnt(" #n ")" ::: "memory")
; #define PG8_WAIT_L(n) asm volatile("s_waitcnt lgkmcnt(" #n ")" ::: "memory")
; #define PG8_BAR __builtin_amdgcn_s_barrier()
; #define PG8_SCHED __builtin_amdgcn_sched_barrier(0)
; #define PG8_STAGE(bufoff, gbase, voff) do { _Pragma("unroll") for (int _i = 0; _i < 2; ++_i) \
;         __builtin_amdgcn_global_load_lds((const unsigned*)((const char*)(gbase) + (voff)[_i]), (PG8_LAS unsigned*)(lds + (bufoff) + ldsw + _i * 8192), 16, 0, 0); } while (0)
; #define PG8_BAR __builtin_amdgcn_s_barrier()
; template <class Epi, class Sched, bool ALIGN_EPI = false, bool SP2 = false>
; __device__ __forceinline__ void gemm_phase(PG8_LAS unsigned char* lds, const Gemm g, const Sched& S, const Epi& E, const int tid) {
;     ...
;             PG8_LDB(B0, 0, 0); PG8_LDB(B1, 0, 1); PG8_SCHED; PG8_LDA(At, 0, 0); PG8_STAGE(PG8_SA(1, 1), a1 + hstep, voffA);
;             PG8_WAIT_V(8); PG8_WAIT_L(0); PG8_BAR; PG8_MMA(0, 0, At, B0); PG8_MMA(0, 1, At, B1); PG8_BAR; PG8_SCHED;
;             PG8_LDA(At, 0, 1); PG8_STAGE(PG8_SB(0, 0), b2, voffB); PG8_STAGE(PG8_SB(0, 1), b2 + hstep, voffB); PG8_STAGE(PG8_SA(0, 0), a2, voffA);
;             PG8_WAIT_V(8); PG8_WAIT_L(0); PG8_BAR; PG8_MMA(1, 0, At, B0); PG8_MMA(1, 1, At, B1); PG8_BAR; PG8_SCHED;
	s_waitcnt lgkmcnt(0)
	v_mfma_f32_16x16x32_bf16 v[126:129], v[164:167], v[198:201], v[126:129]
	v_mfma_f32_16x16x32_bf16 v[122:125], v[172:175], v[198:201], v[122:125]
	v_mfma_f32_16x16x32_bf16 v[118:121], v[164:167], v[206:209], v[118:121]
	v_mfma_f32_16x16x32_bf16 v[110:113], v[172:175], v[206:209], v[110:113]
	v_mfma_f32_16x16x32_bf16 v[102:105], v[164:167], v[214:217], v[102:105]
	v_mfma_f32_16x16x32_bf16 v[94:97], v[172:175], v[214:217], v[94:97]
	v_mfma_f32_16x16x32_bf16 v[86:89], v[164:167], v[222:225], v[86:89]
	v_mfma_f32_16x16x32_bf16 v[78:81], v[172:175], v[222:225], v[78:81]
	v_mfma_f32_16x16x32_bf16 v[126:129], v[168:171], v[202:205], v[126:129]
	v_mfma_f32_16x16x32_bf16 v[122:125], v[176:179], v[202:205], v[122:125]
	v_mfma_f32_16x16x32_bf16 v[118:121], v[168:171], v[210:213], v[118:121]
	v_mfma_f32_16x16x32_bf16 v[110:113], v[176:179], v[210:213], v[110:113]
	v_mfma_f32_16x16x32_bf16 v[102:105], v[168:171], v[218:221], v[102:105]
	v_mfma_f32_16x16x32_bf16 v[94:97], v[176:179], v[218:221], v[94:97]
	v_mfma_f32_16x16x32_bf16 v[86:89], v[168:171], v[226:229], v[86:89]
	v_mfma_f32_16x16x32_bf16 v[78:81], v[176:179], v[226:229], v[78:81]
	v_mfma_f32_16x16x32_bf16 v[114:117], v[180:183], v[198:201], v[114:117]
	v_mfma_f32_16x16x32_bf16 v[106:109], v[188:191], v[198:201], v[106:109]
	v_mfma_f32_16x16x32_bf16 v[98:101], v[180:183], v[206:209], v[98:101]
	v_mfma_f32_16x16x32_bf16 v[90:93], v[188:191], v[206:209], v[90:93]
	v_mfma_f32_16x16x32_bf16 v[82:85], v[180:183], v[214:217], v[82:85]
	v_mfma_f32_16x16x32_bf16 v[74:77], v[188:191], v[214:217], v[74:77]
	v_mfma_f32_16x16x32_bf16 v[70:73], v[180:183], v[222:225], v[70:73]
	v_mfma_f32_16x16x32_bf16 v[66:69], v[188:191], v[222:225], v[66:69]
	v_mfma_f32_16x16x32_bf16 v[114:117], v[184:187], v[202:205], v[114:117]
	v_mfma_f32_16x16x32_bf16 v[106:109], v[192:195], v[202:205], v[106:109]
	v_mfma_f32_16x16x32_bf16 v[98:101], v[184:187], v[210:213], v[98:101]
	v_mfma_f32_16x16x32_bf16 v[90:93], v[192:195], v[210:213], v[90:93]
	v_mfma_f32_16x16x32_bf16 v[82:85], v[184:187], v[218:221], v[82:85]
	v_mfma_f32_16x16x32_bf16 v[74:77], v[192:195], v[218:221], v[74:77]
	v_mfma_f32_16x16x32_bf16 v[70:73], v[184:187], v[226:229], v[70:73]
	v_mfma_f32_16x16x32_bf16 v[66:69], v[192:195], v[226:229], v[66:69]
	s_barrier
	s_add_i32 s15, s15, s49
	v_lshl_add_u64 v[132:133], s[6:7], 0, v[136:137]
	s_mov_b32 m0, s15
	ds_read_b128 v[198:201], v163 offset:16384
	ds_read_b128 v[202:205], v163 offset:17408
	ds_read_b128 v[206:209], v163 offset:18432
	ds_read_b128 v[210:213], v163 offset:19456
	ds_read_b128 v[214:217], v163 offset:20480
	ds_read_b128 v[218:221], v163 offset:21504
	ds_read_b128 v[222:225], v163 offset:22528
	ds_read_b128 v[226:229], v163 offset:23552
	global_load_lds_dwordx4 v[132:133], off
	s_add_i32 m0, s15, 0x2000
	s_add_u32 s18, s6, 0x80000
	v_lshl_add_u64 v[148:149], s[6:7], 0, v[140:141]
	s_addc_u32 s19, s7, 0
	s_add_i32 s15, s16, s49
	global_load_lds_dwordx4 v[148:149], off
	v_lshl_add_u64 v[230:231], s[18:19], 0, v[136:137]
	s_mov_b32 m0, s15
	v_lshl_add_u64 v[242:243], s[68:69], 0, v[138:139]
	global_load_lds_dwordx4 v[230:231], off
	v_lshl_add_u64 v[230:231], s[18:19], 0, v[140:141]
	s_add_i32 m0, s15, 0x2000
	s_nop 0
	global_load_lds_dwordx4 v[230:231], off
	v_lshl_add_u64 v[230:231], s[68:69], 0, v[134:135]
	s_mov_b32 m0, s46
	s_nop 0
	global_load_lds_dwordx4 v[230:231], off
	s_mov_b32 m0, s47
	s_nop 0
	global_load_lds_dwordx4 v[242:243], off
	s_waitcnt vmcnt(8)
	s_waitcnt lgkmcnt(0)
	s_barrier
	s_waitcnt lgkmcnt(0)
	v_mfma_f32_16x16x32_bf16 v[62:65], v[164:167], v[198:201], v[62:65]
	v_mfma_f32_16x16x32_bf16 v[58:61], v[172:175], v[198:201], v[58:61]
	v_mfma_f32_16x16x32_bf16 v[54:57], v[164:167], v[206:209], v[54:57]
	v_mfma_f32_16x16x32_bf16 v[46:49], v[172:175], v[206:209], v[46:49]
	v_mfma_f32_16x16x32_bf16 v[38:41], v[164:167], v[214:217], v[38:41]
	v_mfma_f32_16x16x32_bf16 v[30:33], v[172:175], v[214:217], v[30:33]
	v_mfma_f32_16x16x32_bf16 v[22:25], v[164:167], v[222:225], v[22:25]
	v_mfma_f32_16x16x32_bf16 v[14:17], v[172:175], v[222:225], v[14:17]
	v_mfma_f32_16x16x32_bf16 v[62:65], v[168:171], v[202:205], v[62:65]
	v_mfma_f32_16x16x32_bf16 v[58:61], v[176:179], v[202:205], v[58:61]
	v_mfma_f32_16x16x32_bf16 v[54:57], v[168:171], v[210:213], v[54:57]
	v_mfma_f32_16x16x32_bf16 v[46:49], v[176:179], v[210:213], v[46:49]
	v_mfma_f32_16x16x32_bf16 v[38:41], v[168:171], v[218:221], v[38:41]
	v_mfma_f32_16x16x32_bf16 v[30:33], v[176:179], v[218:221], v[30:33]
	v_mfma_f32_16x16x32_bf16 v[22:25], v[168:171], v[226:229], v[22:25]
	v_mfma_f32_16x16x32_bf16 v[14:17], v[176:179], v[226:229], v[14:17]
	v_mfma_f32_16x16x32_bf16 v[50:53], v[180:183], v[198:201], v[50:53]
	v_mfma_f32_16x16x32_bf16 v[42:45], v[188:191], v[198:201], v[42:45]
	v_mfma_f32_16x16x32_bf16 v[34:37], v[180:183], v[206:209], v[34:37]
	v_mfma_f32_16x16x32_bf16 v[26:29], v[188:191], v[206:209], v[26:29]
	v_mfma_f32_16x16x32_bf16 v[18:21], v[180:183], v[214:217], v[18:21]
	v_mfma_f32_16x16x32_bf16 v[10:13], v[188:191], v[214:217], v[10:13]
	v_mfma_f32_16x16x32_bf16 v[6:9], v[180:183], v[222:225], v[6:9]
	v_mfma_f32_16x16x32_bf16 v[2:5], v[188:191], v[222:225], v[2:5]
	v_mfma_f32_16x16x32_bf16 v[50:53], v[184:187], v[202:205], v[50:53]
	v_mfma_f32_16x16x32_bf16 v[42:45], v[192:195], v[202:205], v[42:45]
	v_mfma_f32_16x16x32_bf16 v[34:37], v[184:187], v[210:213], v[34:37]
	v_mfma_f32_16x16x32_bf16 v[26:29], v[192:195], v[210:213], v[26:29]
	v_mfma_f32_16x16x32_bf16 v[18:21], v[184:187], v[218:221], v[18:21]
	v_mfma_f32_16x16x32_bf16 v[10:13], v[192:195], v[218:221], v[10:13]
	v_mfma_f32_16x16x32_bf16 v[6:9], v[184:187], v[226:229], v[6:9]
	v_mfma_f32_16x16x32_bf16 v[2:5], v[192:195], v[226:229], v[2:5]
	s_barrier
; #define PG8_STAGE(bufoff, gbase, voff) do { _Pragma("unroll") for (int _i = 0; _i < 2; ++_i) \
;         __builtin_amdgcn_global_load_lds((const unsigned*)((const char*)(gbase) + (voff)[_i]), (PG8_LAS unsigned*)(lds + (bufoff) + ldsw + _i * 8192), 16, 0, 0); } while (0)
; #define PG8_LDA(dst, b, h) do { _Pragma("unroll") for (int m = 0; m < 4; ++m) _Pragma("unroll") for (int k = 0; k < 2; ++k) dst[m][k] = *(const PG8_LAS bf16x8*)(lds + PG8_SA(b, h) + aoff + m * 2048 + k * 1024); } while (0)
; #define PG8_LDB(dst, b, h) do { _Pragma("unroll") for (int n = 0; n < 2; ++n) _Pragma("unroll") for (int k = 0; k < 2; ++k) dst[n][k] = *(const PG8_LAS bf16x8*)(lds + PG8_SB(b, h) + boff + n * 2048 + k * 1024); } while (0)
; #define PG8_MMA(ai, bj, At, Bt) do { __builtin_amdgcn_s_setprio(1); _Pragma("unroll") for (int m = 0; m < 4; ++m) _Pragma("unroll") for (int n = 0; n < 2; ++n) _Pragma("unroll") for (int k = 0; k < 2; ++k) \
;         acc[ai][bj][m][n] = __builtin_amdgcn_mfma_f32_16x16x32_bf16(Bt[n][k], At[m][k], acc[ai][bj][m][n], 0, 0, 0); __builtin_amdgcn_s_setprio(0); } while (0)
; #define PG8_WAIT_V(n) asm volatile("s_waitcnt vmcnt(" #n ")" ::: "memory")
; #define PG8_WAIT_L(n) asm volatile("s_waitcnt lgkmcnt(" #n ")" ::: "memory")
; #define PG8_BAR __builtin_amdgcn_s_barrier()
; #define PG8_SCHED __builtin_amdgcn_sched_barrier(0)
; #define PG8_STAGE(bufoff, gbase, voff) do { _Pragma("unroll") for (int _i = 0; _i < 2; ++_i) \
;         __builtin_amdgcn_global_load_lds((const unsigned*)((const char*)(gbase) + (voff)[_i]), (PG8_LAS unsigned*)(lds + (bufoff) + ldsw + _i * 8192), 16, 0, 0); } while (0)
; #define PG8_LDA(dst, b, h) do { _Pragma("unroll") for (int mb = 0; mb < 2; ++mb) _Pragma("unroll") for (int s = 0; s < 2; ++s) \
;         dst[mb][s] = cat8(*(const PG8_LAS bf16x8*)(lds + PG8_SA(b, h) + aoffk[s][0] + mb * 4096), *(const PG8_LAS bf16x8*)(lds + PG8_SA(b, h) + aoffk[s][1] + mb * 4096)); } while (0)
; template <class Epi, class Sched, bool ALIGN_EPI = false, bool SP2 = false>
; __device__ __forceinline__ void gemm_phase(PG8_LAS unsigned char* lds, const Gemm g, const Sched& S, const Epi& E, const int tid) {
;     ...
;             PG8_LDB(B0, 1, 0); PG8_LDB(B1, 1, 1); PG8_SCHED; PG8_LDA(At, 1, 0); PG8_STAGE(PG8_SA(0, 1), a2 + hstep, voffA);
;             PG8_WAIT_V(8); PG8_WAIT_L(0); PG8_BAR; PG8_MMA(0, 0, At, B0); PG8_MMA(0, 1, At, B1); PG8_BAR; PG8_SCHED;
	s_add_i32 s15, 0, 0x18000
	v_add_u32_e32 v131, s15, v152
	s_add_i32 s16, 0, 0x1c000
	ds_read_b128 v[164:167], v131
	ds_read_b128 v[168:171], v131 offset:1024
	ds_read_b128 v[172:175], v131 offset:2048
	ds_read_b128 v[176:179], v131 offset:3072
	v_add_u32_e32 v131, s16, v152
	ds_read_b128 v[180:183], v131
	ds_read_b128 v[184:187], v131 offset:1024
	ds_read_b128 v[188:191], v131 offset:2048
	ds_read_b128 v[192:195], v131 offset:3072
	s_add_u32 s18, s68, 0x80000
	s_addc_u32 s19, s69, 0
	s_mov_b32 m0, s44
	v_lshl_add_u64 v[244:245], s[18:19], 0, v[134:135]
	ds_read_b128 v[198:201], v163 offset:32768
	ds_read_b128 v[202:205], v163 offset:33792
	ds_read_b128 v[206:209], v163 offset:34816
	ds_read_b128 v[210:213], v163 offset:35840
	ds_read_b128 v[214:217], v163 offset:36864
	ds_read_b128 v[218:221], v163 offset:37888
	ds_read_b128 v[222:225], v163 offset:38912
	ds_read_b128 v[226:229], v163 offset:39936
	global_load_lds_dwordx4 v[244:245], off
	v_lshl_add_u64 v[244:245], s[18:19], 0, v[138:139]
	s_mov_b32 m0, s45
	s_nop 0
	global_load_lds_dwordx4 v[244:245], off
	s_waitcnt vmcnt(8)
	s_waitcnt lgkmcnt(0)
	s_barrier
	s_waitcnt lgkmcnt(0)
	v_mfma_f32_16x16x32_bf16 v[126:129], v[164:167], v[198:201], v[126:129]
	v_mfma_f32_16x16x32_bf16 v[122:125], v[172:175], v[198:201], v[122:125]
	v_mfma_f32_16x16x32_bf16 v[118:121], v[164:167], v[206:209], v[118:121]
	v_mfma_f32_16x16x32_bf16 v[110:113], v[172:175], v[206:209], v[110:113]
	v_mfma_f32_16x16x32_bf16 v[102:105], v[164:167], v[214:217], v[102:105]
	v_mfma_f32_16x16x32_bf16 v[94:97], v[172:175], v[214:217], v[94:97]
	v_mfma_f32_16x16x32_bf16 v[86:89], v[164:167], v[222:225], v[86:89]
	v_mfma_f32_16x16x32_bf16 v[78:81], v[172:175], v[222:225], v[78:81]
	v_mfma_f32_16x16x32_bf16 v[126:129], v[168:171], v[202:205], v[126:129]
	v_mfma_f32_16x16x32_bf16 v[122:125], v[176:179], v[202:205], v[122:125]
	v_mfma_f32_16x16x32_bf16 v[118:121], v[168:171], v[210:213], v[118:121]
	v_mfma_f32_16x16x32_bf16 v[110:113], v[176:179], v[210:213], v[110:113]
	v_mfma_f32_16x16x32_bf16 v[102:105], v[168:171], v[218:221], v[102:105]
	v_mfma_f32_16x16x32_bf16 v[94:97], v[176:179], v[218:221], v[94:97]
	v_mfma_f32_16x16x32_bf16 v[86:89], v[168:171], v[226:229], v[86:89]
	v_mfma_f32_16x16x32_bf16 v[78:81], v[176:179], v[226:229], v[78:81]
	v_mfma_f32_16x16x32_bf16 v[114:117], v[180:183], v[198:201], v[114:117]
	v_mfma_f32_16x16x32_bf16 v[106:109], v[188:191], v[198:201], v[106:109]
	v_mfma_f32_16x16x32_bf16 v[98:101], v[180:183], v[206:209], v[98:101]
	v_mfma_f32_16x16x32_bf16 v[90:93], v[188:191], v[206:209], v[90:93]
	v_mfma_f32_16x16x32_bf16 v[82:85], v[180:183], v[214:217], v[82:85]
	v_mfma_f32_16x16x32_bf16 v[74:77], v[188:191], v[214:217], v[74:77]
	v_mfma_f32_16x16x32_bf16 v[70:73], v[180:183], v[222:225], v[70:73]
	v_mfma_f32_16x16x32_bf16 v[66:69], v[188:191], v[222:225], v[66:69]
	v_mfma_f32_16x16x32_bf16 v[114:117], v[184:187], v[202:205], v[114:117]
	v_mfma_f32_16x16x32_bf16 v[106:109], v[192:195], v[202:205], v[106:109]
	v_mfma_f32_16x16x32_bf16 v[98:101], v[184:187], v[210:213], v[98:101]
	v_mfma_f32_16x16x32_bf16 v[90:93], v[192:195], v[210:213], v[90:93]
	v_mfma_f32_16x16x32_bf16 v[82:85], v[184:187], v[218:221], v[82:85]
	v_mfma_f32_16x16x32_bf16 v[74:77], v[192:195], v[218:221], v[74:77]
	v_mfma_f32_16x16x32_bf16 v[70:73], v[184:187], v[226:229], v[70:73]
	v_mfma_f32_16x16x32_bf16 v[66:69], v[192:195], v[226:229], v[66:69]
	s_barrier
; #define PG8_STAGE(bufoff, gbase, voff) do { _Pragma("unroll") for (int _i = 0; _i < 2; ++_i) \
;         __builtin_amdgcn_global_load_lds((const unsigned*)((const char*)(gbase) + (voff)[_i]), (PG8_LAS unsigned*)(lds + (bufoff) + ldsw + _i * 8192), 16, 0, 0); } while (0)
; #define PG8_LDA(dst, b, h) do { _Pragma("unroll") for (int m = 0; m < 4; ++m) _Pragma("unroll") for (int k = 0; k < 2; ++k) dst[m][k] = *(const PG8_LAS bf16x8*)(lds + PG8_SA(b, h) + aoff + m * 2048 + k * 1024); } while (0)
; #define PG8_MMA(ai, bj, At, Bt) do { __builtin_amdgcn_s_setprio(1); _Pragma("unroll") for (int m = 0; m < 4; ++m) _Pragma("unroll") for (int n = 0; n < 2; ++n) _Pragma("unroll") for (int k = 0; k < 2; ++k) \
;         acc[ai][bj][m][n] = __builtin_amdgcn_mfma_f32_16x16x32_bf16(Bt[n][k], At[m][k], acc[ai][bj][m][n], 0, 0, 0); __builtin_amdgcn_s_setprio(0); } while (0)
; #define PG8_WAIT_V(n) asm volatile("s_waitcnt vmcnt(" #n ")" ::: "memory")
; #define PG8_WAIT_L(n) asm volatile("s_waitcnt lgkmcnt(" #n ")" ::: "memory")
; #define PG8_BAR __builtin_amdgcn_s_barrier()
; #define PG8_SCHED __builtin_amdgcn_sched_barrier(0)
; #define PG8_STAGE(bufoff, gbase, voff) do { _Pragma("unroll") for (int _i = 0; _i < 2; ++_i) \
;         __builtin_amdgcn_global_load_lds((const unsigned*)((const char*)(gbase) + (voff)[_i]), (PG8_LAS unsigned*)(lds + (bufoff) + ldsw + _i * 8192), 16, 0, 0); } while (0)
; #define PG8_LDA(dst, b, h) do { _Pragma("unroll") for (int mb = 0; mb < 2; ++mb) _Pragma("unroll") for (int s = 0; s < 2; ++s) \
;         dst[mb][s] = cat8(*(const PG8_LAS bf16x8*)(lds + PG8_SA(b, h) + aoffk[s][0] + mb * 4096), *(const PG8_LAS bf16x8*)(lds + PG8_SA(b, h) + aoffk[s][1] + mb * 4096)); } while (0)
; #define PG8_WAIT_V(n) asm volatile("s_waitcnt vmcnt(" #n ")" ::: "memory")
; #define PG8_BAR __builtin_amdgcn_s_barrier()
; template <class Epi, class Sched, bool ALIGN_EPI = false, bool SP2 = false>
; __device__ __forceinline__ void gemm_phase(PG8_LAS unsigned char* lds, const Gemm g, const Sched& S, const Epi& E, const int tid) {
;     ...
;             PG8_LDA(At, 1, 1); PG8_STAGE(PG8_SB(1, 0), b3, voffB); PG8_STAGE(PG8_SB(1, 1), b3 + hstep, voffB); PG8_STAGE(PG8_SA(1, 0), a3, voffA);
;             PG8_WAIT_V(8); PG8_WAIT_L(0); PG8_BAR; PG8_MMA(1, 0, At, B0); PG8_MMA(1, 1, At, B1); PG8_BAR; PG8_SCHED;
;     ...
;         }
;         if constexpr (ALIGN_EPI) { if (wr == 0) PG8_BAR; }
	s_add_i32 s15, s15, s49
	v_lshl_add_u64 v[132:133], v[132:133], 0, s[34:35]
	s_mov_b32 m0, s15
	ds_read_b128 v[198:201], v163 offset:49152
	ds_read_b128 v[202:205], v163 offset:50176
	ds_read_b128 v[206:209], v163 offset:51200
	ds_read_b128 v[210:213], v163 offset:52224
	ds_read_b128 v[214:217], v163 offset:53248
	ds_read_b128 v[218:221], v163 offset:54272
	ds_read_b128 v[222:225], v163 offset:55296
	ds_read_b128 v[226:229], v163 offset:56320
	global_load_lds_dwordx4 v[132:133], off
	s_add_i32 m0, s15, 0x2000
	s_add_u32 s6, s6, 0x80080
	v_lshl_add_u64 v[132:133], v[148:149], 0, s[34:35]
	s_addc_u32 s7, s7, 0
	s_add_i32 s15, s16, s49
	global_load_lds_dwordx4 v[132:133], off
	v_lshl_add_u64 v[132:133], s[6:7], 0, v[136:137]
	s_mov_b32 m0, s15
	s_nop 0
	global_load_lds_dwordx4 v[132:133], off
	v_lshl_add_u64 v[132:133], s[6:7], 0, v[140:141]
	s_add_i32 m0, s15, 0x2000
	s_nop 0
	global_load_lds_dwordx4 v[132:133], off
	v_lshl_add_u64 v[132:133], v[230:231], 0, s[34:35]
	s_mov_b32 m0, s54
	s_nop 0
	global_load_lds_dwordx4 v[132:133], off
	v_lshl_add_u64 v[132:133], v[242:243], 0, s[34:35]
	s_mov_b32 m0, s55
	s_nop 0
	global_load_lds_dwordx4 v[132:133], off
	s_waitcnt vmcnt(8)
	s_waitcnt lgkmcnt(0)
	s_barrier
	s_waitcnt lgkmcnt(0)
	v_mfma_f32_16x16x32_bf16 v[62:65], v[164:167], v[198:201], v[62:65]
	v_mfma_f32_16x16x32_bf16 v[58:61], v[172:175], v[198:201], v[58:61]
	v_mfma_f32_16x16x32_bf16 v[54:57], v[164:167], v[206:209], v[54:57]
	v_mfma_f32_16x16x32_bf16 v[46:49], v[172:175], v[206:209], v[46:49]
	v_mfma_f32_16x16x32_bf16 v[38:41], v[164:167], v[214:217], v[38:41]
	v_mfma_f32_16x16x32_bf16 v[30:33], v[172:175], v[214:217], v[30:33]
	v_mfma_f32_16x16x32_bf16 v[22:25], v[164:167], v[222:225], v[22:25]
	v_mfma_f32_16x16x32_bf16 v[14:17], v[172:175], v[222:225], v[14:17]
	v_mfma_f32_16x16x32_bf16 v[62:65], v[168:171], v[202:205], v[62:65]
	v_mfma_f32_16x16x32_bf16 v[58:61], v[176:179], v[202:205], v[58:61]
	v_mfma_f32_16x16x32_bf16 v[54:57], v[168:171], v[210:213], v[54:57]
	v_mfma_f32_16x16x32_bf16 v[46:49], v[176:179], v[210:213], v[46:49]
	v_mfma_f32_16x16x32_bf16 v[38:41], v[168:171], v[218:221], v[38:41]
	v_mfma_f32_16x16x32_bf16 v[30:33], v[176:179], v[218:221], v[30:33]
	v_mfma_f32_16x16x32_bf16 v[22:25], v[168:171], v[226:229], v[22:25]
	v_mfma_f32_16x16x32_bf16 v[14:17], v[176:179], v[226:229], v[14:17]
	v_mfma_f32_16x16x32_bf16 v[50:53], v[180:183], v[198:201], v[50:53]
	v_mfma_f32_16x16x32_bf16 v[42:45], v[188:191], v[198:201], v[42:45]
	v_mfma_f32_16x16x32_bf16 v[34:37], v[180:183], v[206:209], v[34:37]
	v_mfma_f32_16x16x32_bf16 v[26:29], v[188:191], v[206:209], v[26:29]
	v_mfma_f32_16x16x32_bf16 v[18:21], v[180:183], v[214:217], v[18:21]
	v_mfma_f32_16x16x32_bf16 v[10:13], v[188:191], v[214:217], v[10:13]
	v_mfma_f32_16x16x32_bf16 v[6:9], v[180:183], v[222:225], v[6:9]
	v_mfma_f32_16x16x32_bf16 v[2:5], v[188:191], v[222:225], v[2:5]
	v_mfma_f32_16x16x32_bf16 v[50:53], v[184:187], v[202:205], v[50:53]
	v_mfma_f32_16x16x32_bf16 v[42:45], v[192:195], v[202:205], v[42:45]
	v_mfma_f32_16x16x32_bf16 v[34:37], v[184:187], v[210:213], v[34:37]
	v_mfma_f32_16x16x32_bf16 v[26:29], v[192:195], v[210:213], v[26:29]
	v_mfma_f32_16x16x32_bf16 v[18:21], v[184:187], v[218:221], v[18:21]
	v_mfma_f32_16x16x32_bf16 v[10:13], v[192:195], v[218:221], v[10:13]
	v_mfma_f32_16x16x32_bf16 v[6:9], v[184:187], v[226:229], v[6:9]
	v_mfma_f32_16x16x32_bf16 v[2:5], v[192:195], v[226:229], v[2:5]
	s_barrier
	s_add_i32 s13, s13, 2
	s_add_u32 s40, s40, 0x100
	s_addc_u32 s41, s41, 0
	s_add_u32 s11, s11, 0x100
	s_addc_u32 s12, s12, 0
	s_cmp_gt_u32 s13, 29
	s_cbranch_scc0 .LBB0_757
	s_setprio 0
	s_and_b64 vcc, exec, s[70:71]
	s_cbranch_vccz .LBB0_760
	s_barrier

; #define PG8_STAGE(bufoff, gbase, voff) do { _Pragma("unroll") for (int _i = 0; _i < 2; ++_i) \
;         __builtin_amdgcn_global_load_lds((const unsigned*)((const char*)(gbase) + (voff)[_i]), (PG8_LAS unsigned*)(lds + (bufoff) + ldsw + _i * 8192), 16, 0, 0); } while (0)
; #define PG8_LDA(dst, b, h) do { _Pragma("unroll") for (int m = 0; m < 4; ++m) _Pragma("unroll") for (int k = 0; k < 2; ++k) dst[m][k] = *(const PG8_LAS bf16x8*)(lds + PG8_SA(b, h) + aoff + m * 2048 + k * 1024); } while (0)
; #define PG8_LDB(dst, b, h) do { _Pragma("unroll") for (int n = 0; n < 2; ++n) _Pragma("unroll") for (int k = 0; k < 2; ++k) dst[n][k] = *(const PG8_LAS bf16x8*)(lds + PG8_SB(b, h) + boff + n * 2048 + k * 1024); } while (0)
; #define PG8_WAIT_V(n) asm volatile("s_waitcnt vmcnt(" #n ")" ::: "memory")
; #define PG8_WAIT_L(n) asm volatile("s_waitcnt lgkmcnt(" #n ")" ::: "memory")
; #define PG8_BAR __builtin_amdgcn_s_barrier()
; template <class Epi, class Sched, bool ALIGN_EPI = false, bool SP2 = false>
; __device__ __forceinline__ void gemm_phase(PG8_LAS unsigned char* lds, const Gemm g, const Sched& S, const Epi& E, const int tid) {
;     ...
;         const char* nA = has_next ? (const char*)g.A + (size_t)nxt.pm * tstep + (size_t)nxt.k0 * 2 : cA; const char* nB = has_next ? (const char*)g.Bt + (size_t)nxt.pn * tstep + (size_t)nxt.k0 * 2 : cB;
;         for (int t = 0; t < nt; t += 2) {
;             const bool last = (t == nt - 2);
;             const char* a1 = cA + (size_t)(t + 1) * kstep;
;             const char* a2 = last ? nA : cA + (size_t)(t + 2) * kstep; const char* b2 = last ? nB : cB + (size_t)(t + 2) * kstep;
;             const char* a3 = a2 + kstep; const char* b3 = b2 + kstep;
;             if (last && has_next) S.a_ready(nxt);
;             if constexpr (SP2) {
;             PG8_LDB(B0, 0, 0); PG8_LDB(B1, 0, 1); PG8_SCHED; PG8_LDA(At, 0, 0); PG8_STAGE(PG8_SA(1, 1), a1 + hstep, voffA);
;             PG8_WAIT_V(8); PG8_WAIT_L(0); PG8_BAR; PG8_MMA(0, 0, At, B0); PG8_MMA(0, 1, At, B1); PG8_BAR; PG8_SCHED;
;     ...
; #pragma unroll
;         for (int a = 0; a < 2; ++a)
; #pragma unroll
;             for (int b = 0; b < 2; ++b)
; #pragma unroll
;                 for (int m = 0; m < 4; ++m)
; #pragma unroll
;                     for (int n = 0; n < 2; ++n) acc[a][b][m][n] = (f32x4){0.f, 0.f, 0.f, 0.f};
;         cur = nxt; cA = nA; cB = nB; ++ui; nt = cur.nt;
.LBB0_1588:
	s_ashr_i32 s23, s22, 31
	s_lshl_b64 s[12:13], s[22:23], 20
	s_add_u32 s12, s33, s12
	s_addc_u32 s13, s19, s13
	s_ashr_i32 s17, s16, 31
	s_lshl_b64 s[42:43], s[16:17], 1
	s_add_u32 s40, s12, s42
	s_addc_u32 s41, s13, s43
	s_and_b64 s[12:13], s[28:29], exec
	s_cselect_b32 s12, s41, s47
	s_cselect_b32 s13, s40, s46
	s_ashr_i32 s21, s20, 31
	s_lshl_b64 s[48:49], s[20:21], 20
	s_add_u32 s17, s24, s48
	s_addc_u32 s21, s27, s49
	s_add_u32 s42, s17, s42
	s_addc_u32 s43, s21, s43
	s_and_b64 s[48:49], s[28:29], exec
	s_cselect_b32 s17, s43, s7
	s_cselect_b32 s21, s42, s6
	s_add_i32 s23, s64, -2
	s_add_u32 s46, s46, 0x80080
	s_addc_u32 s47, s47, 0
	s_add_u32 s39, s6, 0x100
	v_mov_b32_e32 v2, 0
	s_addc_u32 s45, s7, 0
	s_mov_b32 s6, 0
	v_mov_b32_e32 v3, v2
	v_mov_b32_e32 v4, v2
	v_mov_b32_e32 v5, v2
	v_mov_b32_e32 v6, v2
	v_mov_b32_e32 v7, v2
	v_mov_b32_e32 v8, v2
	v_mov_b32_e32 v9, v2
	v_mov_b32_e32 v14, v2
	v_mov_b32_e32 v15, v2
	v_mov_b32_e32 v16, v2
	v_mov_b32_e32 v17, v2
	v_mov_b32_e32 v22, v2
	v_mov_b32_e32 v23, v2
	v_mov_b32_e32 v24, v2
	v_mov_b32_e32 v25, v2
	v_mov_b32_e32 v30, v2
	v_mov_b32_e32 v31, v2
	v_mov_b32_e32 v32, v2
	v_mov_b32_e32 v33, v2
	v_mov_b32_e32 v38, v2
	v_mov_b32_e32 v39, v2
	v_mov_b32_e32 v40, v2
	v_mov_b32_e32 v41, v2
	v_mov_b32_e32 v46, v2
	v_mov_b32_e32 v47, v2
	v_mov_b32_e32 v48, v2
	v_mov_b32_e32 v49, v2
	v_mov_b32_e32 v54, v2
	v_mov_b32_e32 v55, v2
	v_mov_b32_e32 v56, v2
	v_mov_b32_e32 v57, v2
	v_mov_b32_e32 v10, v2
	v_mov_b32_e32 v11, v2
	v_mov_b32_e32 v12, v2
	v_mov_b32_e32 v13, v2
	v_mov_b32_e32 v18, v2
	v_mov_b32_e32 v19, v2
	v_mov_b32_e32 v20, v2
	v_mov_b32_e32 v21, v2
	v_mov_b32_e32 v26, v2
	v_mov_b32_e32 v27, v2
	v_mov_b32_e32 v28, v2
	v_mov_b32_e32 v29, v2
	v_mov_b32_e32 v34, v2
	v_mov_b32_e32 v35, v2
	v_mov_b32_e32 v36, v2
	v_mov_b32_e32 v37, v2
	v_mov_b32_e32 v42, v2
	v_mov_b32_e32 v43, v2
	v_mov_b32_e32 v44, v2
	v_mov_b32_e32 v45, v2
	v_mov_b32_e32 v50, v2
	v_mov_b32_e32 v51, v2
	v_mov_b32_e32 v52, v2
	v_mov_b32_e32 v53, v2
	v_mov_b32_e32 v58, v2
	v_mov_b32_e32 v59, v2
	v_mov_b32_e32 v60, v2
	v_mov_b32_e32 v61, v2
	v_mov_b32_e32 v62, v2
	v_mov_b32_e32 v63, v2
	v_mov_b32_e32 v64, v2
	v_mov_b32_e32 v65, v2
	v_mov_b32_e32 v66, v2
	v_mov_b32_e32 v67, v2
	v_mov_b32_e32 v68, v2
	v_mov_b32_e32 v69, v2
	v_mov_b32_e32 v70, v2
	v_mov_b32_e32 v71, v2
	v_mov_b32_e32 v72, v2
	v_mov_b32_e32 v73, v2
	v_mov_b32_e32 v78, v2
	v_mov_b32_e32 v79, v2
	v_mov_b32_e32 v80, v2
	v_mov_b32_e32 v81, v2
	v_mov_b32_e32 v86, v2
	v_mov_b32_e32 v87, v2
	v_mov_b32_e32 v88, v2
	v_mov_b32_e32 v89, v2
	v_mov_b32_e32 v94, v2
	v_mov_b32_e32 v95, v2
	v_mov_b32_e32 v96, v2
	v_mov_b32_e32 v97, v2
	v_mov_b32_e32 v102, v2
	v_mov_b32_e32 v103, v2
	v_mov_b32_e32 v104, v2
	v_mov_b32_e32 v105, v2
	v_mov_b32_e32 v110, v2
	v_mov_b32_e32 v111, v2
	v_mov_b32_e32 v112, v2
	v_mov_b32_e32 v113, v2
	v_mov_b32_e32 v118, v2
	v_mov_b32_e32 v119, v2
	v_mov_b32_e32 v120, v2
	v_mov_b32_e32 v121, v2
	v_mov_b32_e32 v74, v2
	v_mov_b32_e32 v75, v2
	v_mov_b32_e32 v76, v2
	v_mov_b32_e32 v77, v2
	v_mov_b32_e32 v82, v2
	v_mov_b32_e32 v83, v2
	v_mov_b32_e32 v84, v2
	v_mov_b32_e32 v85, v2
	v_mov_b32_e32 v90, v2
	v_mov_b32_e32 v91, v2
	v_mov_b32_e32 v92, v2
	v_mov_b32_e32 v93, v2
	v_mov_b32_e32 v98, v2
	v_mov_b32_e32 v99, v2
	v_mov_b32_e32 v100, v2
	v_mov_b32_e32 v101, v2
	v_mov_b32_e32 v106, v2
	v_mov_b32_e32 v107, v2
	v_mov_b32_e32 v108, v2
	v_mov_b32_e32 v109, v2
	v_mov_b32_e32 v114, v2
	v_mov_b32_e32 v115, v2
	v_mov_b32_e32 v116, v2
	v_mov_b32_e32 v117, v2
	v_mov_b32_e32 v122, v2
	v_mov_b32_e32 v123, v2
	v_mov_b32_e32 v124, v2
	v_mov_b32_e32 v125, v2
	v_mov_b32_e32 v126, v2
	v_mov_b32_e32 v127, v2
	v_mov_b32_e32 v128, v2
	v_mov_b32_e32 v129, v2
	s_cmp_eq_u64 s[4:5], 0
	s_cbranch_scc0 .Lsp_skip_1589
	s_setprio 1
.Lsp_skip_1589:
.LBB0_1589:
	s_add_i32 s63, s6, 2
	s_add_u32 s7, s46, 0xfff80080
	s_addc_u32 s48, s47, -1
	s_add_i32 s65, 0, 0x10000
	s_cmp_eq_u32 s23, s6
	s_cselect_b32 s49, s12, s48
	s_cselect_b32 s48, s13, s7
	s_cselect_b32 s7, s17, s45
	s_cselect_b32 s6, s21, s39
	s_add_i32 s68, 0, 0x14000
	v_add_u32_e32 v144, s65, v180
	v_add_u32_e32 v160, s68, v180
	ds_read_b128 v[132:135], v144
	ds_read_b128 v[136:139], v144 offset:1024
	ds_read_b128 v[140:143], v144 offset:2048
	ds_read_b128 v[144:147], v144 offset:3072
	ds_read_b128 v[148:151], v160
	ds_read_b128 v[152:155], v160 offset:1024
	ds_read_b128 v[156:159], v160 offset:2048
	ds_read_b128 v[160:163], v160 offset:3072
	v_lshl_add_u64 v[194:195], s[46:47], 0, v[172:173]
	s_add_i32 m0, s18, 0xc000
	ds_read_b128 v[176:179], v189
	ds_read_b128 v[190:193], v189 offset:1024
	ds_read_b128 v[198:201], v189 offset:2048
	ds_read_b128 v[202:205], v189 offset:3072
	ds_read_b128 v[206:209], v189 offset:4096
	ds_read_b128 v[210:213], v189 offset:5120
	ds_read_b128 v[214:217], v189 offset:6144
	ds_read_b128 v[218:221], v189 offset:7168
	global_load_lds_dwordx4 v[194:195], off
	v_lshl_add_u64 v[194:195], s[46:47], 0, v[174:175]
	s_add_i32 m0, s18, 0xe000
	s_nop 0
	global_load_lds_dwordx4 v[194:195], off
	s_waitcnt vmcnt(8)
	s_waitcnt lgkmcnt(0)
	s_barrier
; #define PG8_STAGE(bufoff, gbase, voff) do { _Pragma("unroll") for (int _i = 0; _i < 2; ++_i) \
;         __builtin_amdgcn_global_load_lds((const unsigned*)((const char*)(gbase) + (voff)[_i]), (PG8_LAS unsigned*)(lds + (bufoff) + ldsw + _i * 8192), 16, 0, 0); } while (0)
; #define PG8_LDA(dst, b, h) do { _Pragma("unroll") for (int m = 0; m < 4; ++m) _Pragma("unroll") for (int k = 0; k < 2; ++k) dst[m][k] = *(const PG8_LAS bf16x8*)(lds + PG8_SA(b, h) + aoff + m * 2048 + k * 1024); } while (0)
; #define PG8_LDB(dst, b, h) do { _Pragma("unroll") for (int n = 0; n < 2; ++n) _Pragma("unroll") for (int k = 0; k < 2; ++k) dst[n][k] = *(const PG8_LAS bf16x8*)(lds + PG8_SB(b, h) + boff + n * 2048 + k * 1024); } while (0)
; #define PG8_MMA(ai, bj, At, Bt) do { __builtin_amdgcn_s_setprio(1); _Pragma("unroll") for (int m = 0; m < 4; ++m) _Pragma("unroll") for (int n = 0; n < 2; ++n) _Pragma("unroll") for (int k = 0; k < 2; ++k) \
;         acc[ai][bj][m][n] = __builtin_amdgcn_mfma_f32_16x16x32_bf16(Bt[n][k], At[m][k], acc[ai][bj][m][n], 0, 0, 0); __builtin_amdgcn_s_setprio(0); } while (0)
; #define PG8_WAIT_V(n) asm volatile("s_waitcnt vmcnt(" #n ")" ::: "memory")
; #define PG8_WAIT_L(n) asm volatile("s_waitcnt lgkmcnt(" #n ")" ::: "memory")
; #define PG8_BAR __builtin_amdgcn_s_barrier()
; #define PG8_SCHED __builtin_amdgcn_sched_barrier(0)
; #define PG8_STAGE(bufoff, gbase, voff) do { _Pragma("unroll") for (int _i = 0; _i < 2; ++_i) \
;         __builtin_amdgcn_global_load_lds((const unsigned*)((const char*)(gbase) + (voff)[_i]), (PG8_LAS unsigned*)(lds + (bufoff) + ldsw + _i * 8192), 16, 0, 0); } while (0)
; #define PG8_BAR __builtin_amdgcn_s_barrier()
; template <class Epi, class Sched, bool ALIGN_EPI = false, bool SP2 = false>
; __device__ __forceinline__ void gemm_phase(PG8_LAS unsigned char* lds, const Gemm g, const Sched& S, const Epi& E, const int tid) {
;     ...
;             PG8_LDB(B0, 0, 0); PG8_LDB(B1, 0, 1); PG8_SCHED; PG8_LDA(At, 0, 0); PG8_STAGE(PG8_SA(1, 1), a1 + hstep, voffA);
;             PG8_WAIT_V(8); PG8_WAIT_L(0); PG8_BAR; PG8_MMA(0, 0, At, B0); PG8_MMA(0, 1, At, B1); PG8_BAR; PG8_SCHED;
;             PG8_LDA(At, 0, 1); PG8_STAGE(PG8_SB(0, 0), b2, voffB); PG8_STAGE(PG8_SB(0, 1), b2 + hstep, voffB); PG8_STAGE(PG8_SA(0, 0), a2, voffA);
;             PG8_WAIT_V(8); PG8_WAIT_L(0); PG8_BAR; PG8_MMA(1, 0, At, B0); PG8_MMA(1, 1, At, B1); PG8_BAR; PG8_SCHED;
	s_waitcnt lgkmcnt(0)
	v_mfma_f32_16x16x32_bf16 v[126:129], v[132:135], v[176:179], v[126:129]
	v_mfma_f32_16x16x32_bf16 v[122:125], v[140:143], v[176:179], v[122:125]
	v_mfma_f32_16x16x32_bf16 v[114:117], v[132:135], v[198:201], v[114:117]
	v_mfma_f32_16x16x32_bf16 v[106:109], v[140:143], v[198:201], v[106:109]
	v_mfma_f32_16x16x32_bf16 v[98:101], v[132:135], v[206:209], v[98:101]
	v_mfma_f32_16x16x32_bf16 v[90:93], v[140:143], v[206:209], v[90:93]
	v_mfma_f32_16x16x32_bf16 v[82:85], v[132:135], v[214:217], v[82:85]
	v_mfma_f32_16x16x32_bf16 v[74:77], v[140:143], v[214:217], v[74:77]
	v_mfma_f32_16x16x32_bf16 v[126:129], v[136:139], v[190:193], v[126:129]
	v_mfma_f32_16x16x32_bf16 v[122:125], v[144:147], v[190:193], v[122:125]
	v_mfma_f32_16x16x32_bf16 v[114:117], v[136:139], v[202:205], v[114:117]
	v_mfma_f32_16x16x32_bf16 v[106:109], v[144:147], v[202:205], v[106:109]
	v_mfma_f32_16x16x32_bf16 v[98:101], v[136:139], v[210:213], v[98:101]
	v_mfma_f32_16x16x32_bf16 v[90:93], v[144:147], v[210:213], v[90:93]
	v_mfma_f32_16x16x32_bf16 v[82:85], v[136:139], v[218:221], v[82:85]
	v_mfma_f32_16x16x32_bf16 v[74:77], v[144:147], v[218:221], v[74:77]
	v_mfma_f32_16x16x32_bf16 v[118:121], v[148:151], v[176:179], v[118:121]
	v_mfma_f32_16x16x32_bf16 v[110:113], v[156:159], v[176:179], v[110:113]
	v_mfma_f32_16x16x32_bf16 v[102:105], v[148:151], v[198:201], v[102:105]
	v_mfma_f32_16x16x32_bf16 v[94:97], v[156:159], v[198:201], v[94:97]
	v_mfma_f32_16x16x32_bf16 v[86:89], v[148:151], v[206:209], v[86:89]
	v_mfma_f32_16x16x32_bf16 v[78:81], v[156:159], v[206:209], v[78:81]
	v_mfma_f32_16x16x32_bf16 v[70:73], v[148:151], v[214:217], v[70:73]
	v_mfma_f32_16x16x32_bf16 v[66:69], v[156:159], v[214:217], v[66:69]
	v_mfma_f32_16x16x32_bf16 v[118:121], v[152:155], v[190:193], v[118:121]
	v_mfma_f32_16x16x32_bf16 v[110:113], v[160:163], v[190:193], v[110:113]
	v_mfma_f32_16x16x32_bf16 v[102:105], v[152:155], v[202:205], v[102:105]
	v_mfma_f32_16x16x32_bf16 v[94:97], v[160:163], v[202:205], v[94:97]
	v_mfma_f32_16x16x32_bf16 v[86:89], v[152:155], v[210:213], v[86:89]
	v_mfma_f32_16x16x32_bf16 v[78:81], v[160:163], v[210:213], v[78:81]
	v_mfma_f32_16x16x32_bf16 v[70:73], v[152:155], v[218:221], v[70:73]
	v_mfma_f32_16x16x32_bf16 v[66:69], v[160:163], v[218:221], v[66:69]
	s_barrier
	s_add_i32 s65, s65, s36
	v_lshl_add_u64 v[194:195], s[6:7], 0, v[166:167]
	s_mov_b32 m0, s65
	ds_read_b128 v[176:179], v189 offset:16384
	ds_read_b128 v[190:193], v189 offset:17408
	ds_read_b128 v[198:201], v189 offset:18432
	ds_read_b128 v[202:205], v189 offset:19456
	ds_read_b128 v[206:209], v189 offset:20480
	ds_read_b128 v[210:213], v189 offset:21504
	ds_read_b128 v[214:217], v189 offset:22528
	ds_read_b128 v[218:221], v189 offset:23552
	global_load_lds_dwordx4 v[194:195], off
	s_add_i32 m0, s65, 0x2000
	s_add_u32 s66, s6, 0x80000
	v_lshl_add_u64 v[222:223], s[6:7], 0, v[170:171]
	s_addc_u32 s67, s7, 0
	s_add_i32 s65, s68, s36
	global_load_lds_dwordx4 v[222:223], off
	v_lshl_add_u64 v[224:225], s[66:67], 0, v[166:167]
	s_mov_b32 m0, s65
	v_lshl_add_u64 v[226:227], s[48:49], 0, v[168:169]
	global_load_lds_dwordx4 v[224:225], off
	v_lshl_add_u64 v[224:225], s[66:67], 0, v[170:171]
	s_add_i32 m0, s65, 0x2000
	s_nop 0
	global_load_lds_dwordx4 v[224:225], off
	v_lshl_add_u64 v[224:225], s[48:49], 0, v[164:165]
	s_mov_b32 m0, s18
	s_nop 0
	global_load_lds_dwordx4 v[224:225], off
	s_mov_b32 m0, s31
	s_nop 0
	global_load_lds_dwordx4 v[226:227], off
	s_waitcnt vmcnt(8)
	s_waitcnt lgkmcnt(0)
	s_barrier
	s_waitcnt lgkmcnt(0)
	v_mfma_f32_16x16x32_bf16 v[62:65], v[132:135], v[176:179], v[62:65]
	v_mfma_f32_16x16x32_bf16 v[58:61], v[140:143], v[176:179], v[58:61]
	v_mfma_f32_16x16x32_bf16 v[50:53], v[132:135], v[198:201], v[50:53]
	v_mfma_f32_16x16x32_bf16 v[42:45], v[140:143], v[198:201], v[42:45]
	v_mfma_f32_16x16x32_bf16 v[34:37], v[132:135], v[206:209], v[34:37]
	v_mfma_f32_16x16x32_bf16 v[26:29], v[140:143], v[206:209], v[26:29]
	v_mfma_f32_16x16x32_bf16 v[18:21], v[132:135], v[214:217], v[18:21]
	v_mfma_f32_16x16x32_bf16 v[10:13], v[140:143], v[214:217], v[10:13]
	v_mfma_f32_16x16x32_bf16 v[62:65], v[136:139], v[190:193], v[62:65]
	v_mfma_f32_16x16x32_bf16 v[58:61], v[144:147], v[190:193], v[58:61]
	v_mfma_f32_16x16x32_bf16 v[50:53], v[136:139], v[202:205], v[50:53]
	v_mfma_f32_16x16x32_bf16 v[42:45], v[144:147], v[202:205], v[42:45]
	v_mfma_f32_16x16x32_bf16 v[34:37], v[136:139], v[210:213], v[34:37]
	v_mfma_f32_16x16x32_bf16 v[26:29], v[144:147], v[210:213], v[26:29]
	v_mfma_f32_16x16x32_bf16 v[18:21], v[136:139], v[218:221], v[18:21]
	v_mfma_f32_16x16x32_bf16 v[10:13], v[144:147], v[218:221], v[10:13]
	v_mfma_f32_16x16x32_bf16 v[54:57], v[148:151], v[176:179], v[54:57]
	v_mfma_f32_16x16x32_bf16 v[46:49], v[156:159], v[176:179], v[46:49]
	v_mfma_f32_16x16x32_bf16 v[38:41], v[148:151], v[198:201], v[38:41]
	v_mfma_f32_16x16x32_bf16 v[30:33], v[156:159], v[198:201], v[30:33]
	v_mfma_f32_16x16x32_bf16 v[22:25], v[148:151], v[206:209], v[22:25]
	v_mfma_f32_16x16x32_bf16 v[14:17], v[156:159], v[206:209], v[14:17]
	v_mfma_f32_16x16x32_bf16 v[6:9], v[148:151], v[214:217], v[6:9]
	v_mfma_f32_16x16x32_bf16 v[2:5], v[156:159], v[214:217], v[2:5]
	v_mfma_f32_16x16x32_bf16 v[54:57], v[152:155], v[190:193], v[54:57]
	v_mfma_f32_16x16x32_bf16 v[46:49], v[160:163], v[190:193], v[46:49]
	v_mfma_f32_16x16x32_bf16 v[38:41], v[152:155], v[202:205], v[38:41]
	v_mfma_f32_16x16x32_bf16 v[30:33], v[160:163], v[202:205], v[30:33]
	v_mfma_f32_16x16x32_bf16 v[22:25], v[152:155], v[210:213], v[22:25]
	v_mfma_f32_16x16x32_bf16 v[14:17], v[160:163], v[210:213], v[14:17]
	v_mfma_f32_16x16x32_bf16 v[6:9], v[152:155], v[218:221], v[6:9]
	v_mfma_f32_16x16x32_bf16 v[2:5], v[160:163], v[218:221], v[2:5]
	s_barrier
; #define PG8_STAGE(bufoff, gbase, voff) do { _Pragma("unroll") for (int _i = 0; _i < 2; ++_i) \
;         __builtin_amdgcn_global_load_lds((const unsigned*)((const char*)(gbase) + (voff)[_i]), (PG8_LAS unsigned*)(lds + (bufoff) + ldsw + _i * 8192), 16, 0, 0); } while (0)
; #define PG8_LDA(dst, b, h) do { _Pragma("unroll") for (int m = 0; m < 4; ++m) _Pragma("unroll") for (int k = 0; k < 2; ++k) dst[m][k] = *(const PG8_LAS bf16x8*)(lds + PG8_SA(b, h) + aoff + m * 2048 + k * 1024); } while (0)
; #define PG8_LDB(dst, b, h) do { _Pragma("unroll") for (int n = 0; n < 2; ++n) _Pragma("unroll") for (int k = 0; k < 2; ++k) dst[n][k] = *(const PG8_LAS bf16x8*)(lds + PG8_SB(b, h) + boff + n * 2048 + k * 1024); } while (0)
; #define PG8_MMA(ai, bj, At, Bt) do { __builtin_amdgcn_s_setprio(1); _Pragma("unroll") for (int m = 0; m < 4; ++m) _Pragma("unroll") for (int n = 0; n < 2; ++n) _Pragma("unroll") for (int k = 0; k < 2; ++k) \
;         acc[ai][bj][m][n] = __builtin_amdgcn_mfma_f32_16x16x32_bf16(Bt[n][k], At[m][k], acc[ai][bj][m][n], 0, 0, 0); __builtin_amdgcn_s_setprio(0); } while (0)
; #define PG8_WAIT_V(n) asm volatile("s_waitcnt vmcnt(" #n ")" ::: "memory")
; #define PG8_WAIT_L(n) asm volatile("s_waitcnt lgkmcnt(" #n ")" ::: "memory")
; #define PG8_BAR __builtin_amdgcn_s_barrier()
; #define PG8_SCHED __builtin_amdgcn_sched_barrier(0)
; #define PG8_STAGE(bufoff, gbase, voff) do { _Pragma("unroll") for (int _i = 0; _i < 2; ++_i) \
;         __builtin_amdgcn_global_load_lds((const unsigned*)((const char*)(gbase) + (voff)[_i]), (PG8_LAS unsigned*)(lds + (bufoff) + ldsw + _i * 8192), 16, 0, 0); } while (0)
; #define PG8_LDA(dst, b, h) do { _Pragma("unroll") for (int mb = 0; mb < 2; ++mb) _Pragma("unroll") for (int s = 0; s < 2; ++s) \
;         dst[mb][s] = cat8(*(const PG8_LAS bf16x8*)(lds + PG8_SA(b, h) + aoffk[s][0] + mb * 4096), *(const PG8_LAS bf16x8*)(lds + PG8_SA(b, h) + aoffk[s][1] + mb * 4096)); } while (0)
; template <class Epi, class Sched, bool ALIGN_EPI = false, bool SP2 = false>
; __device__ __forceinline__ void gemm_phase(PG8_LAS unsigned char* lds, const Gemm g, const Sched& S, const Epi& E, const int tid) {
;     ...
;             PG8_LDB(B0, 1, 0); PG8_LDB(B1, 1, 1); PG8_SCHED; PG8_LDA(At, 1, 0); PG8_STAGE(PG8_SA(0, 1), a2 + hstep, voffA);
;             PG8_WAIT_V(8); PG8_WAIT_L(0); PG8_BAR; PG8_MMA(0, 0, At, B0); PG8_MMA(0, 1, At, B1); PG8_BAR; PG8_SCHED;
	s_add_i32 s65, 0, 0x18000
	s_add_i32 s66, 0, 0x1c000
	v_add_u32_e32 v144, s65, v180
	v_add_u32_e32 v160, s66, v180
	ds_read_b128 v[132:135], v144
	ds_read_b128 v[136:139], v144 offset:1024
	ds_read_b128 v[140:143], v144 offset:2048
	ds_read_b128 v[144:147], v144 offset:3072
	ds_read_b128 v[148:151], v160
	ds_read_b128 v[152:155], v160 offset:1024
	ds_read_b128 v[156:159], v160 offset:2048
	ds_read_b128 v[160:163], v160 offset:3072
	s_add_u32 s48, s48, 0x80000
	s_addc_u32 s49, s49, 0
	s_mov_b32 m0, s37
	v_lshl_add_u64 v[228:229], s[48:49], 0, v[164:165]
	ds_read_b128 v[176:179], v189 offset:32768
	ds_read_b128 v[190:193], v189 offset:33792
	ds_read_b128 v[198:201], v189 offset:34816
	ds_read_b128 v[202:205], v189 offset:35840
	ds_read_b128 v[206:209], v189 offset:36864
	ds_read_b128 v[210:213], v189 offset:37888
	ds_read_b128 v[214:217], v189 offset:38912
	ds_read_b128 v[218:221], v189 offset:39936
	global_load_lds_dwordx4 v[228:229], off
	v_lshl_add_u64 v[228:229], s[48:49], 0, v[168:169]
	s_mov_b32 m0, s50
	s_nop 0
	global_load_lds_dwordx4 v[228:229], off
	s_waitcnt vmcnt(8)
	s_waitcnt lgkmcnt(0)
	s_barrier
	s_waitcnt lgkmcnt(0)
	v_mfma_f32_16x16x32_bf16 v[126:129], v[132:135], v[176:179], v[126:129]
	v_mfma_f32_16x16x32_bf16 v[122:125], v[140:143], v[176:179], v[122:125]
	v_mfma_f32_16x16x32_bf16 v[114:117], v[132:135], v[198:201], v[114:117]
	v_mfma_f32_16x16x32_bf16 v[106:109], v[140:143], v[198:201], v[106:109]
	v_mfma_f32_16x16x32_bf16 v[98:101], v[132:135], v[206:209], v[98:101]
	v_mfma_f32_16x16x32_bf16 v[90:93], v[140:143], v[206:209], v[90:93]
	v_mfma_f32_16x16x32_bf16 v[82:85], v[132:135], v[214:217], v[82:85]
	v_mfma_f32_16x16x32_bf16 v[74:77], v[140:143], v[214:217], v[74:77]
	v_mfma_f32_16x16x32_bf16 v[126:129], v[136:139], v[190:193], v[126:129]
	v_mfma_f32_16x16x32_bf16 v[122:125], v[144:147], v[190:193], v[122:125]
	v_mfma_f32_16x16x32_bf16 v[114:117], v[136:139], v[202:205], v[114:117]
	v_mfma_f32_16x16x32_bf16 v[106:109], v[144:147], v[202:205], v[106:109]
	v_mfma_f32_16x16x32_bf16 v[98:101], v[136:139], v[210:213], v[98:101]
	v_mfma_f32_16x16x32_bf16 v[90:93], v[144:147], v[210:213], v[90:93]
	v_mfma_f32_16x16x32_bf16 v[82:85], v[136:139], v[218:221], v[82:85]
	v_mfma_f32_16x16x32_bf16 v[74:77], v[144:147], v[218:221], v[74:77]
	v_mfma_f32_16x16x32_bf16 v[118:121], v[148:151], v[176:179], v[118:121]
	v_mfma_f32_16x16x32_bf16 v[110:113], v[156:159], v[176:179], v[110:113]
	v_mfma_f32_16x16x32_bf16 v[102:105], v[148:151], v[198:201], v[102:105]
	v_mfma_f32_16x16x32_bf16 v[94:97], v[156:159], v[198:201], v[94:97]
	v_mfma_f32_16x16x32_bf16 v[86:89], v[148:151], v[206:209], v[86:89]
	v_mfma_f32_16x16x32_bf16 v[78:81], v[156:159], v[206:209], v[78:81]
	v_mfma_f32_16x16x32_bf16 v[70:73], v[148:151], v[214:217], v[70:73]
	v_mfma_f32_16x16x32_bf16 v[66:69], v[156:159], v[214:217], v[66:69]
	v_mfma_f32_16x16x32_bf16 v[118:121], v[152:155], v[190:193], v[118:121]
	v_mfma_f32_16x16x32_bf16 v[110:113], v[160:163], v[190:193], v[110:113]
	v_mfma_f32_16x16x32_bf16 v[102:105], v[152:155], v[202:205], v[102:105]
	v_mfma_f32_16x16x32_bf16 v[94:97], v[160:163], v[202:205], v[94:97]
	v_mfma_f32_16x16x32_bf16 v[86:89], v[152:155], v[210:213], v[86:89]
	v_mfma_f32_16x16x32_bf16 v[78:81], v[160:163], v[210:213], v[78:81]
	v_mfma_f32_16x16x32_bf16 v[70:73], v[152:155], v[218:221], v[70:73]
	v_mfma_f32_16x16x32_bf16 v[66:69], v[160:163], v[218:221], v[66:69]
	s_barrier
; #define PG8_STAGE(bufoff, gbase, voff) do { _Pragma("unroll") for (int _i = 0; _i < 2; ++_i) \
;         __builtin_amdgcn_global_load_lds((const unsigned*)((const char*)(gbase) + (voff)[_i]), (PG8_LAS unsigned*)(lds + (bufoff) + ldsw + _i * 8192), 16, 0, 0); } while (0)
; #define PG8_LDA(dst, b, h) do { _Pragma("unroll") for (int m = 0; m < 4; ++m) _Pragma("unroll") for (int k = 0; k < 2; ++k) dst[m][k] = *(const PG8_LAS bf16x8*)(lds + PG8_SA(b, h) + aoff + m * 2048 + k * 1024); } while (0)
; #define PG8_MMA(ai, bj, At, Bt) do { __builtin_amdgcn_s_setprio(1); _Pragma("unroll") for (int m = 0; m < 4; ++m) _Pragma("unroll") for (int n = 0; n < 2; ++n) _Pragma("unroll") for (int k = 0; k < 2; ++k) \
;         acc[ai][bj][m][n] = __builtin_amdgcn_mfma_f32_16x16x32_bf16(Bt[n][k], At[m][k], acc[ai][bj][m][n], 0, 0, 0); __builtin_amdgcn_s_setprio(0); } while (0)
; #define PG8_WAIT_V(n) asm volatile("s_waitcnt vmcnt(" #n ")" ::: "memory")
; #define PG8_WAIT_L(n) asm volatile("s_waitcnt lgkmcnt(" #n ")" ::: "memory")
; #define PG8_BAR __builtin_amdgcn_s_barrier()
; #define PG8_SCHED __builtin_amdgcn_sched_barrier(0)
; #define PG8_STAGE(bufoff, gbase, voff) do { _Pragma("unroll") for (int _i = 0; _i < 2; ++_i) \
;         __builtin_amdgcn_global_load_lds((const unsigned*)((const char*)(gbase) + (voff)[_i]), (PG8_LAS unsigned*)(lds + (bufoff) + ldsw + _i * 8192), 16, 0, 0); } while (0)
; #define PG8_LDA(dst, b, h) do { _Pragma("unroll") for (int mb = 0; mb < 2; ++mb) _Pragma("unroll") for (int s = 0; s < 2; ++s) \
;         dst[mb][s] = cat8(*(const PG8_LAS bf16x8*)(lds + PG8_SA(b, h) + aoffk[s][0] + mb * 4096), *(const PG8_LAS bf16x8*)(lds + PG8_SA(b, h) + aoffk[s][1] + mb * 4096)); } while (0)
; #define PG8_WAIT_V(n) asm volatile("s_waitcnt vmcnt(" #n ")" ::: "memory")
; #define PG8_BAR __builtin_amdgcn_s_barrier()
; template <class Epi, class Sched, bool ALIGN_EPI = false, bool SP2 = false>
; __device__ __forceinline__ void gemm_phase(PG8_LAS unsigned char* lds, const Gemm g, const Sched& S, const Epi& E, const int tid) {
;     ...
;             PG8_LDA(At, 1, 1); PG8_STAGE(PG8_SB(1, 0), b3, voffB); PG8_STAGE(PG8_SB(1, 1), b3 + hstep, voffB); PG8_STAGE(PG8_SA(1, 0), a3, voffA);
;             PG8_WAIT_V(8); PG8_WAIT_L(0); PG8_BAR; PG8_MMA(1, 0, At, B0); PG8_MMA(1, 1, At, B1); PG8_BAR; PG8_SCHED;
;     ...
;         }
;         if constexpr (ALIGN_EPI) { if (wr == 0) PG8_BAR; }
	s_add_i32 s48, s65, s36
	v_lshl_add_u64 v[194:195], v[194:195], 0, s[34:35]
	s_mov_b32 m0, s48
	ds_read_b128 v[176:179], v189 offset:49152
	ds_read_b128 v[190:193], v189 offset:50176
	ds_read_b128 v[198:201], v189 offset:51200
	ds_read_b128 v[202:205], v189 offset:52224
	ds_read_b128 v[206:209], v189 offset:53248
	ds_read_b128 v[210:213], v189 offset:54272
	ds_read_b128 v[214:217], v189 offset:55296
	ds_read_b128 v[218:221], v189 offset:56320
	global_load_lds_dwordx4 v[194:195], off
	s_add_i32 m0, s48, 0x2000
	s_add_u32 s6, s6, 0x80080
	v_lshl_add_u64 v[194:195], v[222:223], 0, s[34:35]
	s_addc_u32 s7, s7, 0
	s_add_i32 s48, s66, s36
	global_load_lds_dwordx4 v[194:195], off
	v_lshl_add_u64 v[194:195], s[6:7], 0, v[166:167]
	s_mov_b32 m0, s48
	s_nop 0
	global_load_lds_dwordx4 v[194:195], off
	v_lshl_add_u64 v[194:195], s[6:7], 0, v[170:171]
	s_add_i32 m0, s48, 0x2000
	s_nop 0
	global_load_lds_dwordx4 v[194:195], off
	v_lshl_add_u64 v[194:195], v[224:225], 0, s[34:35]
	s_mov_b32 m0, s26
	s_nop 0
	global_load_lds_dwordx4 v[194:195], off
	v_lshl_add_u64 v[194:195], v[226:227], 0, s[34:35]
	s_mov_b32 m0, s52
	s_nop 0
	global_load_lds_dwordx4 v[194:195], off
	s_waitcnt vmcnt(8)
	s_waitcnt lgkmcnt(0)
	s_barrier
	s_waitcnt lgkmcnt(0)
	v_mfma_f32_16x16x32_bf16 v[62:65], v[132:135], v[176:179], v[62:65]
	v_mfma_f32_16x16x32_bf16 v[58:61], v[140:143], v[176:179], v[58:61]
	v_mfma_f32_16x16x32_bf16 v[50:53], v[132:135], v[198:201], v[50:53]
	v_mfma_f32_16x16x32_bf16 v[42:45], v[140:143], v[198:201], v[42:45]
	v_mfma_f32_16x16x32_bf16 v[34:37], v[132:135], v[206:209], v[34:37]
	v_mfma_f32_16x16x32_bf16 v[26:29], v[140:143], v[206:209], v[26:29]
	v_mfma_f32_16x16x32_bf16 v[18:21], v[132:135], v[214:217], v[18:21]
	v_mfma_f32_16x16x32_bf16 v[10:13], v[140:143], v[214:217], v[10:13]
	v_mfma_f32_16x16x32_bf16 v[62:65], v[136:139], v[190:193], v[62:65]
	v_mfma_f32_16x16x32_bf16 v[58:61], v[144:147], v[190:193], v[58:61]
	v_mfma_f32_16x16x32_bf16 v[50:53], v[136:139], v[202:205], v[50:53]
	v_mfma_f32_16x16x32_bf16 v[42:45], v[144:147], v[202:205], v[42:45]
	v_mfma_f32_16x16x32_bf16 v[34:37], v[136:139], v[210:213], v[34:37]
	v_mfma_f32_16x16x32_bf16 v[26:29], v[144:147], v[210:213], v[26:29]
	v_mfma_f32_16x16x32_bf16 v[18:21], v[136:139], v[218:221], v[18:21]
	v_mfma_f32_16x16x32_bf16 v[10:13], v[144:147], v[218:221], v[10:13]
	v_mfma_f32_16x16x32_bf16 v[54:57], v[148:151], v[176:179], v[54:57]
	v_mfma_f32_16x16x32_bf16 v[46:49], v[156:159], v[176:179], v[46:49]
	v_mfma_f32_16x16x32_bf16 v[38:41], v[148:151], v[198:201], v[38:41]
	v_mfma_f32_16x16x32_bf16 v[30:33], v[156:159], v[198:201], v[30:33]
	v_mfma_f32_16x16x32_bf16 v[22:25], v[148:151], v[206:209], v[22:25]
	v_mfma_f32_16x16x32_bf16 v[14:17], v[156:159], v[206:209], v[14:17]
	v_mfma_f32_16x16x32_bf16 v[6:9], v[148:151], v[214:217], v[6:9]
	v_mfma_f32_16x16x32_bf16 v[2:5], v[156:159], v[214:217], v[2:5]
	v_mfma_f32_16x16x32_bf16 v[54:57], v[152:155], v[190:193], v[54:57]
	v_mfma_f32_16x16x32_bf16 v[46:49], v[160:163], v[190:193], v[46:49]
	v_mfma_f32_16x16x32_bf16 v[38:41], v[152:155], v[202:205], v[38:41]
	v_mfma_f32_16x16x32_bf16 v[30:33], v[160:163], v[202:205], v[30:33]
	v_mfma_f32_16x16x32_bf16 v[22:25], v[152:155], v[210:213], v[22:25]
	v_mfma_f32_16x16x32_bf16 v[14:17], v[160:163], v[210:213], v[14:17]
	v_mfma_f32_16x16x32_bf16 v[6:9], v[152:155], v[218:221], v[6:9]
	v_mfma_f32_16x16x32_bf16 v[2:5], v[160:163], v[218:221], v[2:5]
	s_barrier
	s_add_u32 s46, s46, 0x100
	s_addc_u32 s47, s47, 0
	s_add_u32 s39, s39, 0x100
	s_addc_u32 s45, s45, 0
	s_cmp_ge_i32 s63, s64
	s_mov_b32 s6, s63
	s_cbranch_scc0 .LBB0_1589
	s_setprio 0
	s_and_b64 vcc, exec, s[4:5]
	s_cbranch_vccz .LBB0_1592
	s_barrier

; #define PG8_STAGE(bufoff, gbase, voff) do { _Pragma("unroll") for (int _i = 0; _i < 2; ++_i) \
;         __builtin_amdgcn_global_load_lds((const unsigned*)((const char*)(gbase) + (voff)[_i]), (PG8_LAS unsigned*)(lds + (bufoff) + ldsw + _i * 8192), 16, 0, 0); } while (0)
; #define PG8_LDA(dst, b, h) do { _Pragma("unroll") for (int m = 0; m < 4; ++m) _Pragma("unroll") for (int k = 0; k < 2; ++k) dst[m][k] = *(const PG8_LAS bf16x8*)(lds + PG8_SA(b, h) + aoff + m * 2048 + k * 1024); } while (0)
; #define PG8_LDB(dst, b, h) do { _Pragma("unroll") for (int n = 0; n < 2; ++n) _Pragma("unroll") for (int k = 0; k < 2; ++k) dst[n][k] = *(const PG8_LAS bf16x8*)(lds + PG8_SB(b, h) + boff + n * 2048 + k * 1024); } while (0)
; #define PG8_MMA(ai, bj, At, Bt) do { __builtin_amdgcn_s_setprio(1); _Pragma("unroll") for (int m = 0; m < 4; ++m) _Pragma("unroll") for (int n = 0; n < 2; ++n) _Pragma("unroll") for (int k = 0; k < 2; ++k) \
;         acc[ai][bj][m][n] = __builtin_amdgcn_mfma_f32_16x16x32_bf16(Bt[n][k], At[m][k], acc[ai][bj][m][n], 0, 0, 0); __builtin_amdgcn_s_setprio(0); } while (0)
; #define PG8_WAIT_V(n) asm volatile("s_waitcnt vmcnt(" #n ")" ::: "memory")
; #define PG8_WAIT_L(n) asm volatile("s_waitcnt lgkmcnt(" #n ")" ::: "memory")
; #define PG8_BAR __builtin_amdgcn_s_barrier()
; #define PG8_SCHED __builtin_amdgcn_sched_barrier(0)
; #define PG8_WAIT_V(n) asm volatile("s_waitcnt vmcnt(" #n ")" ::: "memory")
; template <class Epi, class Sched, int SCW, int SCX, int SCW1 = SCW>
; __device__ __forceinline__ void gemm_phase_f8(PG8_LAS unsigned char* lds, const Gemm g, const Sched& S, const Epi& E, const int tid) {
;     ...
;         for (int t = 0; t < nt; t += 2) {
;             const bool last = (t == nt - 2);
;             const char* a1 = cA + (size_t)(t + 1) * kstep;
;             const char* a2 = last ? nA : cA + (size_t)(t + 2) * kstep; const char* b2 = last ? nB : cB + (size_t)(t + 2) * kstepB;
;             const char* a3 = a2 + kstep; const char* b3 = b2 + kstepB;
;             if (last && has_next) S.a_ready(nxt);
;             PG8_LDB(B0, 0, 0); PG8_LDB(B1, 0, 1); PG8_SCHED; PG8_LDA(At, 0, 0); PG8_STAGE(PG8_SA(1, 1), a1 + hstep, voffA);
;             PG8_WAIT_V(8); PG8_WAIT_L(0); PG8_BAR; PG8_MMA(0, 0, At, B0); PG8_MMA(0, 1, At, B1); PG8_BAR; PG8_SCHED;
;     ...
;         PG8_ZERO();
;         cur = nxt; cA = nA; cB = nB; ++ui; nt = cur.nt;
.LBB0_1895:
	s_ashr_i32 s15, s14, 31
	s_lshl_b64 s[22:23], s[14:15], 19
	s_add_u32 s15, s44, s22
	s_addc_u32 s21, s45, s23
	s_ashr_i32 s17, s16, 31
	s_add_u32 s22, s15, s16
	s_addc_u32 s23, s21, s17
	s_and_b64 s[28:29], s[10:11], exec
	s_cselect_b32 s15, s23, s41
	s_cselect_b32 s63, s22, s40
	s_ashr_i32 s21, s20, 31
	s_lshl_b64 s[28:29], s[20:21], 19
	s_add_u32 s21, s46, s28
	s_addc_u32 s42, s47, s29
	s_lshl_b64 s[28:29], s[16:17], 8
	s_add_u32 s28, s21, s28
	s_addc_u32 s29, s42, s29
	s_and_b64 s[42:43], s[10:11], exec
	s_cselect_b32 s17, s29, s7
	s_cselect_b32 s21, s28, s6
	s_add_u32 s64, s6, 0x10000
	s_addc_u32 s65, s7, 0
	s_add_u32 s40, s40, 0x40080
	v_mov_b32_e32 v18, 0
	s_addc_u32 s41, s41, 0
	s_mov_b32 s66, -2
	v_mov_b32_e32 v19, v18
	v_mov_b32_e32 v20, v18
	v_mov_b32_e32 v21, v18
	v_mov_b32_e32 v22, v18
	v_mov_b32_e32 v23, v18
	v_mov_b32_e32 v24, v18
	v_mov_b32_e32 v25, v18
	v_mov_b32_e32 v26, v18
	v_mov_b32_e32 v27, v18
	v_mov_b32_e32 v28, v18
	v_mov_b32_e32 v29, v18
	v_mov_b32_e32 v30, v18
	v_mov_b32_e32 v31, v18
	v_mov_b32_e32 v32, v18
	v_mov_b32_e32 v33, v18
	v_mov_b32_e32 v50, v18
	v_mov_b32_e32 v51, v18
	v_mov_b32_e32 v52, v18
	v_mov_b32_e32 v53, v18
	v_mov_b32_e32 v54, v18
	v_mov_b32_e32 v55, v18
	v_mov_b32_e32 v56, v18
	v_mov_b32_e32 v57, v18
	v_mov_b32_e32 v58, v18
	v_mov_b32_e32 v59, v18
	v_mov_b32_e32 v60, v18
	v_mov_b32_e32 v61, v18
	v_mov_b32_e32 v62, v18
	v_mov_b32_e32 v63, v18
	v_mov_b32_e32 v64, v18
	v_mov_b32_e32 v65, v18
	v_mov_b32_e32 v2, v18
	v_mov_b32_e32 v3, v18
	v_mov_b32_e32 v4, v18
	v_mov_b32_e32 v5, v18
	v_mov_b32_e32 v6, v18
	v_mov_b32_e32 v7, v18
	v_mov_b32_e32 v8, v18
	v_mov_b32_e32 v9, v18
	v_mov_b32_e32 v10, v18
	v_mov_b32_e32 v11, v18
	v_mov_b32_e32 v12, v18
	v_mov_b32_e32 v13, v18
	v_mov_b32_e32 v14, v18
	v_mov_b32_e32 v15, v18
	v_mov_b32_e32 v16, v18
	v_mov_b32_e32 v17, v18
	v_mov_b32_e32 v34, v18
	v_mov_b32_e32 v35, v18
	v_mov_b32_e32 v36, v18
	v_mov_b32_e32 v37, v18
	v_mov_b32_e32 v38, v18
	v_mov_b32_e32 v39, v18
	v_mov_b32_e32 v40, v18
	v_mov_b32_e32 v41, v18
	v_mov_b32_e32 v42, v18
	v_mov_b32_e32 v43, v18
	v_mov_b32_e32 v44, v18
	v_mov_b32_e32 v45, v18
	v_mov_b32_e32 v46, v18
	v_mov_b32_e32 v47, v18
	v_mov_b32_e32 v48, v18
	v_mov_b32_e32 v49, v18
	v_mov_b32_e32 v82, v18
	v_mov_b32_e32 v83, v18
	v_mov_b32_e32 v84, v18
	v_mov_b32_e32 v85, v18
	v_mov_b32_e32 v86, v18
	v_mov_b32_e32 v87, v18
	v_mov_b32_e32 v88, v18
	v_mov_b32_e32 v89, v18
	v_mov_b32_e32 v90, v18
	v_mov_b32_e32 v91, v18
	v_mov_b32_e32 v92, v18
	v_mov_b32_e32 v93, v18
	v_mov_b32_e32 v94, v18
	v_mov_b32_e32 v95, v18
	v_mov_b32_e32 v96, v18
	v_mov_b32_e32 v97, v18
	v_mov_b32_e32 v114, v18
	v_mov_b32_e32 v115, v18
	v_mov_b32_e32 v116, v18
	v_mov_b32_e32 v117, v18
	v_mov_b32_e32 v118, v18
	v_mov_b32_e32 v119, v18
	v_mov_b32_e32 v120, v18
	v_mov_b32_e32 v121, v18
	v_mov_b32_e32 v122, v18
	v_mov_b32_e32 v123, v18
	v_mov_b32_e32 v124, v18
	v_mov_b32_e32 v125, v18
	v_mov_b32_e32 v126, v18
	v_mov_b32_e32 v127, v18
	v_mov_b32_e32 v128, v18
	v_mov_b32_e32 v129, v18
	v_mov_b32_e32 v66, v18
	v_mov_b32_e32 v67, v18
	v_mov_b32_e32 v68, v18
	v_mov_b32_e32 v69, v18
	v_mov_b32_e32 v70, v18
	v_mov_b32_e32 v71, v18
	v_mov_b32_e32 v72, v18
	v_mov_b32_e32 v73, v18
	v_mov_b32_e32 v74, v18
	v_mov_b32_e32 v75, v18
	v_mov_b32_e32 v76, v18
	v_mov_b32_e32 v77, v18
	v_mov_b32_e32 v78, v18
	v_mov_b32_e32 v79, v18
	v_mov_b32_e32 v80, v18
	v_mov_b32_e32 v81, v18
	v_mov_b32_e32 v98, v18
	v_mov_b32_e32 v99, v18
	v_mov_b32_e32 v100, v18
	v_mov_b32_e32 v101, v18
	v_mov_b32_e32 v102, v18
	v_mov_b32_e32 v103, v18
	v_mov_b32_e32 v104, v18
	v_mov_b32_e32 v105, v18
	v_mov_b32_e32 v106, v18
	v_mov_b32_e32 v107, v18
	v_mov_b32_e32 v108, v18
	v_mov_b32_e32 v109, v18
	v_mov_b32_e32 v110, v18
	v_mov_b32_e32 v111, v18
	v_mov_b32_e32 v112, v18
	v_mov_b32_e32 v113, v18
	s_cmp_eq_u64 s[8:9], 0
	s_cbranch_scc0 .Lsp_skip_1896
	s_setprio 1
.Lsp_skip_1896:
.LBB0_1896:
	s_add_u32 s6, s40, 0xfffc0080
	s_addc_u32 s7, s41, -1
	s_add_i32 s67, 0, 0x10000
	s_cmp_eq_u32 s66, 12
	v_add_u32_e32 v144, s67, v131
	s_cselect_b32 s43, s15, s7
	s_cselect_b32 s42, s63, s6
	v_add_u32_e32 v145, s67, v150
	ds_read_b128 v[160:163], v144
	ds_read_b128 v[164:167], v145
	v_add_u32_e32 v144, s67, v151
	s_cselect_b32 s7, s17, s65
	s_cselect_b32 s6, s21, s64
	s_add_i32 s70, 0, 0x14000
	v_add_u32_e32 v145, s67, v152
	ds_read_b128 v[168:171], v144
	ds_read_b128 v[172:175], v145
	v_add_u32_e32 v144, s70, v131
	v_add_u32_e32 v145, s70, v150
	ds_read_b128 v[176:179], v144
	ds_read_b128 v[180:183], v145
	v_add_u32_e32 v144, s70, v151
	v_add_u32_e32 v145, s70, v152
	ds_read_b128 v[184:187], v144
	ds_read_b128 v[188:191], v145
	v_lshl_add_u64 v[144:145], s[40:41], 0, v[140:141]
	s_add_i32 m0, s31, 0xc000
	ds_read_b128 v[198:201], v155
	ds_read_b128 v[206:209], v155 offset:4096
	ds_read_b128 v[202:205], v156
	ds_read_b128 v[210:213], v156 offset:4096
	ds_read_b128 v[214:217], v157
	ds_read_b128 v[222:225], v157 offset:4096
	ds_read_b128 v[218:221], v158
	ds_read_b128 v[226:229], v158 offset:4096
	global_load_lds_dwordx4 v[144:145], off
	v_lshl_add_u64 v[144:145], s[40:41], 0, v[142:143]
	s_add_i32 m0, s31, 0xe000
	s_nop 0
	global_load_lds_dwordx4 v[144:145], off
	s_waitcnt vmcnt(8)
	s_waitcnt lgkmcnt(0)
	s_barrier
; #define PG8_STAGE(bufoff, gbase, voff) do { _Pragma("unroll") for (int _i = 0; _i < 2; ++_i) \
;         __builtin_amdgcn_global_load_lds((const unsigned*)((const char*)(gbase) + (voff)[_i]), (PG8_LAS unsigned*)(lds + (bufoff) + ldsw + _i * 8192), 16, 0, 0); } while (0)
; #define PG8_LDA(dst, b, h) do { _Pragma("unroll") for (int m = 0; m < 4; ++m) _Pragma("unroll") for (int k = 0; k < 2; ++k) dst[m][k] = *(const PG8_LAS bf16x8*)(lds + PG8_SA(b, h) + aoff + m * 2048 + k * 1024); } while (0)
; #define PG8_LDB(dst, b, h) do { _Pragma("unroll") for (int n = 0; n < 2; ++n) _Pragma("unroll") for (int k = 0; k < 2; ++k) dst[n][k] = *(const PG8_LAS bf16x8*)(lds + PG8_SB(b, h) + boff + n * 2048 + k * 1024); } while (0)
; template <class Epi, class Sched, int SCW, int SCX, int SCW1 = SCW>
; __device__ __forceinline__ void gemm_phase_f8(PG8_LAS unsigned char* lds, const Gemm g, const Sched& S, const Epi& E, const int tid) {
;     ...
;         for (int t = 0; t < nt; t += 2) {
;             const bool last = (t == nt - 2);
;             const char* a1 = cA + (size_t)(t + 1) * kstep;
;             const char* a2 = last ? nA : cA + (size_t)(t + 2) * kstep; const char* b2 = last ? nB : cB + (size_t)(t + 2) * kstepB;
;             const char* a3 = a2 + kstep; const char* b3 = b2 + kstepB;
;             if (last && has_next) S.a_ready(nxt);
;             PG8_LDB(B0, 0, 0); PG8_LDB(B1, 0, 1); PG8_SCHED; PG8_LDA(At, 0, 0); PG8_STAGE(PG8_SA(1, 1), a1 + hstep, voffA);
;             PG8_WAIT_V(8); PG8_WAIT_L(0); PG8_BAR; PG8_MMA(0, 0, At, B0); PG8_MMA(0, 1, At, B1); PG8_BAR; PG8_SCHED;
;             PG8_LDA(At, 0, 1); PG8_STAGE(PG8_SB(0, 0), b2, voffB); PG8_STAGE(PG8_SB(0, 1), b2 + hstepB, voffB); PG8_STAGE(PG8_SA(0, 0), a2, voffA);
;             PG8_WAIT_V(8); PG8_WAIT_L(0); PG8_BAR; PG8_MMA(1, 0, At, B0); PG8_MMA(1, 1, At, B1); PG8_BAR; PG8_SCHED;
;             PG8_LDB(B0, 1, 0); PG8_LDB(B1, 1, 1); PG8_SCHED; PG8_LDA(At, 1, 0); PG8_STAGE(PG8_SA(0, 1), a2 + hstep, voffA);
;             PG8_WAIT_V(8); PG8_WAIT_L(0); PG8_BAR; PG8_MMA(0, 0, At, B0); PG8_MMA(0, 1, At, B1); PG8_BAR; PG8_SCHED;
;             PG8_LDA(At, 1, 1); PG8_STAGE(PG8_SB(1, 0), b3, voffB); PG8_STAGE(PG8_SB(1, 1), b3 + hstepB, voffB); PG8_STAGE(PG8_SA(1, 0), a3, voffA);
;             PG8_WAIT_V(8); PG8_WAIT_L(0); PG8_BAR; PG8_MMA(1, 0, At, B0); PG8_MMA(1, 1, At, B1); PG8_BAR; PG8_SCHED;
	s_waitcnt lgkmcnt(0)
	v_mfma_scale_f32_32x32x64_f8f6f4 v[98:113], v[160:167], v[198:205], v[98:113], v233, v232 op_sel_hi:[0,0,0]
	v_mfma_scale_f32_32x32x64_f8f6f4 v[66:81], v[160:167], v[206:213], v[66:81], v233, v232 op_sel_hi:[0,0,0]
	v_mfma_scale_f32_32x32x64_f8f6f4 v[98:113], v[168:175], v[214:221], v[98:113], v233, v232 op_sel_hi:[0,0,0]
	v_mfma_scale_f32_32x32x64_f8f6f4 v[66:81], v[168:175], v[222:229], v[66:81], v233, v232 op_sel_hi:[0,0,0]
	v_mfma_scale_f32_32x32x64_f8f6f4 v[114:129], v[176:183], v[198:205], v[114:129], v232, v232 op_sel_hi:[0,0,0]
	v_mfma_scale_f32_32x32x64_f8f6f4 v[82:97], v[176:183], v[206:213], v[82:97], v232, v232 op_sel_hi:[0,0,0]
	v_mfma_scale_f32_32x32x64_f8f6f4 v[114:129], v[184:191], v[214:221], v[114:129], v232, v232 op_sel_hi:[0,0,0]
	v_mfma_scale_f32_32x32x64_f8f6f4 v[82:97], v[184:191], v[222:229], v[82:97], v232, v232 op_sel_hi:[0,0,0]
	s_barrier
	s_add_i32 s67, s67, s48
	v_lshl_add_u64 v[144:145], s[6:7], 0, v[136:137]
	s_mov_b32 m0, s67
	ds_read_b128 v[198:201], v155 offset:16384
	ds_read_b128 v[206:209], v155 offset:20480
	ds_read_b128 v[202:205], v156 offset:16384
	ds_read_b128 v[210:213], v156 offset:20480
	ds_read_b128 v[214:217], v157 offset:16384
	ds_read_b128 v[222:225], v157 offset:20480
	ds_read_b128 v[218:221], v158 offset:16384
	ds_read_b128 v[226:229], v158 offset:20480
	global_load_lds_dwordx4 v[144:145], off
	s_add_i32 m0, s67, 0x2000
	s_add_u32 s68, s6, 0x4000
	v_lshl_add_u64 v[144:145], s[6:7], 0, v[132:133]
	s_addc_u32 s69, s7, 0
	s_add_i32 s67, s70, s48
	global_load_lds_dwordx4 v[144:145], off
	v_lshl_add_u64 v[144:145], s[68:69], 0, v[136:137]
	s_mov_b32 m0, s67
	v_lshl_add_u64 v[146:147], s[42:43], 0, v[134:135]
	global_load_lds_dwordx4 v[144:145], off
	v_lshl_add_u64 v[144:145], s[68:69], 0, v[132:133]
	s_add_i32 m0, s67, 0x2000
	s_nop 0
	global_load_lds_dwordx4 v[144:145], off
	v_lshl_add_u64 v[144:145], s[42:43], 0, v[138:139]
	s_mov_b32 m0, s31
	s_nop 0
	global_load_lds_dwordx4 v[144:145], off
	s_mov_b32 m0, s39
	s_nop 0
	global_load_lds_dwordx4 v[146:147], off
	s_waitcnt vmcnt(8)
	s_waitcnt lgkmcnt(0)
	s_barrier
	s_waitcnt lgkmcnt(0)
	v_mfma_scale_f32_32x32x64_f8f6f4 v[34:49], v[160:167], v[198:205], v[34:49], v233, v232 op_sel_hi:[0,0,0]
	v_mfma_scale_f32_32x32x64_f8f6f4 v[2:17], v[160:167], v[206:213], v[2:17], v233, v232 op_sel_hi:[0,0,0]
	v_mfma_scale_f32_32x32x64_f8f6f4 v[34:49], v[168:175], v[214:221], v[34:49], v233, v232 op_sel_hi:[0,0,0]
	v_mfma_scale_f32_32x32x64_f8f6f4 v[2:17], v[168:175], v[222:229], v[2:17], v233, v232 op_sel_hi:[0,0,0]
	v_mfma_scale_f32_32x32x64_f8f6f4 v[50:65], v[176:183], v[198:205], v[50:65], v232, v232 op_sel_hi:[0,0,0]
	v_mfma_scale_f32_32x32x64_f8f6f4 v[18:33], v[176:183], v[206:213], v[18:33], v232, v232 op_sel_hi:[0,0,0]
	v_mfma_scale_f32_32x32x64_f8f6f4 v[50:65], v[184:191], v[214:221], v[50:65], v232, v232 op_sel_hi:[0,0,0]
	v_mfma_scale_f32_32x32x64_f8f6f4 v[18:33], v[184:191], v[222:229], v[18:33], v232, v232 op_sel_hi:[0,0,0]
	s_barrier
	s_add_i32 s67, 0, 0x18000
	v_add_u32_e32 v148, s67, v131
	v_add_u32_e32 v149, s67, v150
	ds_read_b128 v[160:163], v148
	ds_read_b128 v[164:167], v149
	v_add_u32_e32 v148, s67, v151
	s_add_i32 s68, 0, 0x1c000
	v_add_u32_e32 v149, s67, v152
	ds_read_b128 v[168:171], v148
	ds_read_b128 v[172:175], v149
	v_add_u32_e32 v148, s68, v131
	v_add_u32_e32 v149, s68, v150
	ds_read_b128 v[176:179], v148
	ds_read_b128 v[180:183], v149
	v_add_u32_e32 v148, s68, v151
	v_add_u32_e32 v149, s68, v152
	ds_read_b128 v[184:187], v148
	ds_read_b128 v[188:191], v149
	s_add_u32 s42, s42, 0x40000
	s_addc_u32 s43, s43, 0
	s_mov_b32 m0, s57
	v_lshl_add_u64 v[148:149], s[42:43], 0, v[138:139]
	ds_read_b128 v[198:201], v155 offset:32768
	ds_read_b128 v[206:209], v155 offset:36864
	ds_read_b128 v[202:205], v156 offset:32768
	ds_read_b128 v[210:213], v156 offset:36864
	ds_read_b128 v[214:217], v157 offset:32768
	ds_read_b128 v[222:225], v157 offset:36864
	ds_read_b128 v[218:221], v158 offset:32768
	ds_read_b128 v[226:229], v158 offset:36864
	global_load_lds_dwordx4 v[148:149], off
	v_lshl_add_u64 v[148:149], s[42:43], 0, v[134:135]
	s_mov_b32 m0, s58
	s_nop 0
	global_load_lds_dwordx4 v[148:149], off
	s_waitcnt vmcnt(8)
	s_waitcnt lgkmcnt(0)
	s_barrier
; #define PG8_STAGE(bufoff, gbase, voff) do { _Pragma("unroll") for (int _i = 0; _i < 2; ++_i) \
;         __builtin_amdgcn_global_load_lds((const unsigned*)((const char*)(gbase) + (voff)[_i]), (PG8_LAS unsigned*)(lds + (bufoff) + ldsw + _i * 8192), 16, 0, 0); } while (0)
; #define PG8_LDA(dst, b, h) do { _Pragma("unroll") for (int m = 0; m < 4; ++m) _Pragma("unroll") for (int k = 0; k < 2; ++k) dst[m][k] = *(const PG8_LAS bf16x8*)(lds + PG8_SA(b, h) + aoff + m * 2048 + k * 1024); } while (0)
; #define PG8_WAIT_V(n) asm volatile("s_waitcnt vmcnt(" #n ")" ::: "memory")
; #define PG8_WAIT_L(n) asm volatile("s_waitcnt lgkmcnt(" #n ")" ::: "memory")
; #define PG8_BAR __builtin_amdgcn_s_barrier()
; template <class Epi, class Sched, int SCW, int SCX, int SCW1 = SCW>
; __device__ __forceinline__ void gemm_phase_f8(PG8_LAS unsigned char* lds, const Gemm g, const Sched& S, const Epi& E, const int tid) {
;     ...
;         for (int t = 0; t < nt; t += 2) {
;             const bool last = (t == nt - 2);
;             const char* a1 = cA + (size_t)(t + 1) * kstep;
;             const char* a2 = last ? nA : cA + (size_t)(t + 2) * kstep; const char* b2 = last ? nB : cB + (size_t)(t + 2) * kstepB;
;             const char* a3 = a2 + kstep; const char* b3 = b2 + kstepB;
;             if (last && has_next) S.a_ready(nxt);
;             PG8_LDB(B0, 0, 0); PG8_LDB(B1, 0, 1); PG8_SCHED; PG8_LDA(At, 0, 0); PG8_STAGE(PG8_SA(1, 1), a1 + hstep, voffA);
;             PG8_WAIT_V(8); PG8_WAIT_L(0); PG8_BAR; PG8_MMA(0, 0, At, B0); PG8_MMA(0, 1, At, B1); PG8_BAR; PG8_SCHED;
;             PG8_LDA(At, 0, 1); PG8_STAGE(PG8_SB(0, 0), b2, voffB); PG8_STAGE(PG8_SB(0, 1), b2 + hstepB, voffB); PG8_STAGE(PG8_SA(0, 0), a2, voffA);
;             PG8_WAIT_V(8); PG8_WAIT_L(0); PG8_BAR; PG8_MMA(1, 0, At, B0); PG8_MMA(1, 1, At, B1); PG8_BAR; PG8_SCHED;
;             PG8_LDB(B0, 1, 0); PG8_LDB(B1, 1, 1); PG8_SCHED; PG8_LDA(At, 1, 0); PG8_STAGE(PG8_SA(0, 1), a2 + hstep, voffA);
;             PG8_WAIT_V(8); PG8_WAIT_L(0); PG8_BAR; PG8_MMA(0, 0, At, B0); PG8_MMA(0, 1, At, B1); PG8_BAR; PG8_SCHED;
;             PG8_LDA(At, 1, 1); PG8_STAGE(PG8_SB(1, 0), b3, voffB); PG8_STAGE(PG8_SB(1, 1), b3 + hstepB, voffB); PG8_STAGE(PG8_SA(1, 0), a3, voffA);
;             PG8_WAIT_V(8); PG8_WAIT_L(0); PG8_BAR; PG8_MMA(1, 0, At, B0); PG8_MMA(1, 1, At, B1); PG8_BAR; PG8_SCHED;
;         }
;         if (wr == 0) PG8_BAR;
	s_waitcnt lgkmcnt(0)
	v_mfma_scale_f32_32x32x64_f8f6f4 v[98:113], v[160:167], v[198:205], v[98:113], v233, v232 op_sel_hi:[0,0,0]
	v_mfma_scale_f32_32x32x64_f8f6f4 v[66:81], v[160:167], v[206:213], v[66:81], v233, v232 op_sel_hi:[0,0,0]
	v_mfma_scale_f32_32x32x64_f8f6f4 v[98:113], v[168:175], v[214:221], v[98:113], v233, v232 op_sel_hi:[0,0,0]
	v_mfma_scale_f32_32x32x64_f8f6f4 v[66:81], v[168:175], v[222:229], v[66:81], v233, v232 op_sel_hi:[0,0,0]
	v_mfma_scale_f32_32x32x64_f8f6f4 v[114:129], v[176:183], v[198:205], v[114:129], v232, v232 op_sel_hi:[0,0,0]
	v_mfma_scale_f32_32x32x64_f8f6f4 v[82:97], v[176:183], v[206:213], v[82:97], v232, v232 op_sel_hi:[0,0,0]
	v_mfma_scale_f32_32x32x64_f8f6f4 v[114:129], v[184:191], v[214:221], v[114:129], v232, v232 op_sel_hi:[0,0,0]
	v_mfma_scale_f32_32x32x64_f8f6f4 v[82:97], v[184:191], v[222:229], v[82:97], v232, v232 op_sel_hi:[0,0,0]
	s_barrier
	s_add_u32 s42, s6, 0x8000
	s_addc_u32 s43, s7, 0
	s_add_i32 s67, s67, s48
	v_lshl_add_u64 v[148:149], s[42:43], 0, v[136:137]
	s_mov_b32 m0, s67
	ds_read_b128 v[198:201], v155 offset:49152
	ds_read_b128 v[206:209], v155 offset:53248
	ds_read_b128 v[202:205], v156 offset:49152
	ds_read_b128 v[210:213], v156 offset:53248
	ds_read_b128 v[214:217], v157 offset:49152
	ds_read_b128 v[222:225], v157 offset:53248
	ds_read_b128 v[218:221], v158 offset:49152
	ds_read_b128 v[226:229], v158 offset:53248
	global_load_lds_dwordx4 v[148:149], off
	s_add_i32 m0, s67, 0x2000
	s_add_u32 s6, s6, 0xc000
	v_lshl_add_u64 v[148:149], s[42:43], 0, v[132:133]
	s_addc_u32 s7, s7, 0
	s_add_i32 s42, s68, s48
	global_load_lds_dwordx4 v[148:149], off
	v_lshl_add_u64 v[148:149], s[6:7], 0, v[136:137]
	s_mov_b32 m0, s42
	v_lshl_add_u64 v[144:145], v[144:145], 0, s[34:35]
	global_load_lds_dwordx4 v[148:149], off
	v_lshl_add_u64 v[148:149], s[6:7], 0, v[132:133]
	s_add_i32 m0, s42, 0x2000
	s_nop 0
	global_load_lds_dwordx4 v[148:149], off
	s_mov_b32 m0, s59
	s_nop 0
	global_load_lds_dwordx4 v[144:145], off
	v_lshl_add_u64 v[144:145], v[146:147], 0, s[34:35]
	s_mov_b32 m0, s60
	s_nop 0
	global_load_lds_dwordx4 v[144:145], off
	s_waitcnt vmcnt(8)
	s_waitcnt lgkmcnt(0)
	s_barrier
	s_waitcnt lgkmcnt(0)
	v_mfma_scale_f32_32x32x64_f8f6f4 v[34:49], v[160:167], v[198:205], v[34:49], v233, v232 op_sel_hi:[0,0,0]
	v_mfma_scale_f32_32x32x64_f8f6f4 v[2:17], v[160:167], v[206:213], v[2:17], v233, v232 op_sel_hi:[0,0,0]
	v_mfma_scale_f32_32x32x64_f8f6f4 v[34:49], v[168:175], v[214:221], v[34:49], v233, v232 op_sel_hi:[0,0,0]
	v_mfma_scale_f32_32x32x64_f8f6f4 v[2:17], v[168:175], v[222:229], v[2:17], v233, v232 op_sel_hi:[0,0,0]
	v_mfma_scale_f32_32x32x64_f8f6f4 v[50:65], v[176:183], v[198:205], v[50:65], v232, v232 op_sel_hi:[0,0,0]
	v_mfma_scale_f32_32x32x64_f8f6f4 v[18:33], v[176:183], v[206:213], v[18:33], v232, v232 op_sel_hi:[0,0,0]
	v_mfma_scale_f32_32x32x64_f8f6f4 v[50:65], v[184:191], v[214:221], v[50:65], v232, v232 op_sel_hi:[0,0,0]
	v_mfma_scale_f32_32x32x64_f8f6f4 v[18:33], v[184:191], v[222:229], v[18:33], v232, v232 op_sel_hi:[0,0,0]
	s_barrier
	s_add_i32 s66, s66, 2
	s_add_u32 s64, s64, 0x10000
	s_addc_u32 s65, s65, 0
	s_add_u32 s40, s40, 0x100
	s_addc_u32 s41, s41, 0
	s_cmp_gt_u32 s66, 13
	s_cbranch_scc0 .LBB0_1896
	s_setprio 0
	s_and_b64 vcc, exec, s[8:9]
	s_cbranch_vccz .LBB0_1899
	s_barrier

; #define PG8_STAGE(bufoff, gbase, voff) do { _Pragma("unroll") for (int _i = 0; _i < 2; ++_i) \
;         __builtin_amdgcn_global_load_lds((const unsigned*)((const char*)(gbase) + (voff)[_i]), (PG8_LAS unsigned*)(lds + (bufoff) + ldsw + _i * 8192), 16, 0, 0); } while (0)
; #define PG8_LDA(dst, b, h) do { _Pragma("unroll") for (int m = 0; m < 4; ++m) _Pragma("unroll") for (int k = 0; k < 2; ++k) dst[m][k] = *(const PG8_LAS bf16x8*)(lds + PG8_SA(b, h) + aoff + m * 2048 + k * 1024); } while (0)
; #define PG8_WAIT_V(n) asm volatile("s_waitcnt vmcnt(" #n ")" ::: "memory")
; #define PG8_WAIT_L(n) asm volatile("s_waitcnt lgkmcnt(" #n ")" ::: "memory")
; template <class Epi, class Sched, int SCW, int SCX, int SCW1 = SCW>
; __device__ __forceinline__ void gemm_phase_f8(PG8_LAS unsigned char* lds, const Gemm g, const Sched& S, const Epi& E, const int tid) {
;     ...
;         for (int t = 0; t < nt; t += 2) {
;             const bool last = (t == nt - 2);
;             const char* a1 = cA + (size_t)(t + 1) * kstep;
;             const char* a2 = last ? nA : cA + (size_t)(t + 2) * kstep; const char* b2 = last ? nB : cB + (size_t)(t + 2) * kstepB;
;             const char* a3 = a2 + kstep; const char* b3 = b2 + kstepB;
;             if (last && has_next) S.a_ready(nxt);
;             PG8_LDB(B0, 0, 0); PG8_LDB(B1, 0, 1); PG8_SCHED; PG8_LDA(At, 0, 0); PG8_STAGE(PG8_SA(1, 1), a1 + hstep, voffA);
;             PG8_WAIT_V(8); PG8_WAIT_L(0); PG8_BAR; PG8_MMA(0, 0, At, B0); PG8_MMA(0, 1, At, B1); PG8_BAR; PG8_SCHED;
;             PG8_LDA(At, 0, 1); PG8_STAGE(PG8_SB(0, 0), b2, voffB); PG8_STAGE(PG8_SB(0, 1), b2 + hstepB, voffB); PG8_STAGE(PG8_SA(0, 0), a2, voffA);
;             PG8_WAIT_V(8); PG8_WAIT_L(0); PG8_BAR; PG8_MMA(1, 0, At, B0); PG8_MMA(1, 1, At, B1); PG8_BAR; PG8_SCHED;
;             PG8_LDB(B0, 1, 0); PG8_LDB(B1, 1, 1); PG8_SCHED; PG8_LDA(At, 1, 0); PG8_STAGE(PG8_SA(0, 1), a2 + hstep, voffA);
;             PG8_WAIT_V(8); PG8_WAIT_L(0); PG8_BAR; PG8_MMA(0, 0, At, B0); PG8_MMA(0, 1, At, B1); PG8_BAR; PG8_SCHED;
;             PG8_LDA(At, 1, 1); PG8_STAGE(PG8_SB(1, 0), b3, voffB); PG8_STAGE(PG8_SB(1, 1), b3 + hstepB, voffB); PG8_STAGE(PG8_SA(1, 0), a3, voffA);
;             PG8_WAIT_V(8); PG8_WAIT_L(0); PG8_BAR; PG8_MMA(1, 0, At, B0); PG8_MMA(1, 1, At, B1); PG8_BAR; PG8_SCHED;
;     ...
;         PG8_ZERO();
;         cur = nxt; cA = nA; cB = nB; ++ui; nt = cur.nt;
.LBB0_1999:
	s_add_i32 s12, s24, -2
	s_add_u32 s13, s6, 0x10000
	s_addc_u32 s17, s7, 0
	s_add_u32 s28, s28, 0xc000
	v_mov_b32_e32 v2, 0
	s_addc_u32 s29, s29, 0
	s_mov_b32 s6, 0
	v_mov_b32_e32 v3, v2
	v_mov_b32_e32 v4, v2
	v_mov_b32_e32 v5, v2
	v_mov_b32_e32 v6, v2
	v_mov_b32_e32 v7, v2
	v_mov_b32_e32 v8, v2
	v_mov_b32_e32 v9, v2
	v_mov_b32_e32 v10, v2
	v_mov_b32_e32 v11, v2
	v_mov_b32_e32 v12, v2
	v_mov_b32_e32 v13, v2
	v_mov_b32_e32 v14, v2
	v_mov_b32_e32 v15, v2
	v_mov_b32_e32 v16, v2
	v_mov_b32_e32 v17, v2
	v_mov_b32_e32 v34, v2
	v_mov_b32_e32 v35, v2
	v_mov_b32_e32 v36, v2
	v_mov_b32_e32 v37, v2
	v_mov_b32_e32 v38, v2
	v_mov_b32_e32 v39, v2
	v_mov_b32_e32 v40, v2
	v_mov_b32_e32 v41, v2
	v_mov_b32_e32 v42, v2
	v_mov_b32_e32 v43, v2
	v_mov_b32_e32 v44, v2
	v_mov_b32_e32 v45, v2
	v_mov_b32_e32 v46, v2
	v_mov_b32_e32 v47, v2
	v_mov_b32_e32 v48, v2
	v_mov_b32_e32 v49, v2
	v_mov_b32_e32 v18, v2
	v_mov_b32_e32 v19, v2
	v_mov_b32_e32 v20, v2
	v_mov_b32_e32 v21, v2
	v_mov_b32_e32 v22, v2
	v_mov_b32_e32 v23, v2
	v_mov_b32_e32 v24, v2
	v_mov_b32_e32 v25, v2
	v_mov_b32_e32 v26, v2
	v_mov_b32_e32 v27, v2
	v_mov_b32_e32 v28, v2
	v_mov_b32_e32 v29, v2
	v_mov_b32_e32 v30, v2
	v_mov_b32_e32 v31, v2
	v_mov_b32_e32 v32, v2
	v_mov_b32_e32 v33, v2
	v_mov_b32_e32 v50, v2
	v_mov_b32_e32 v51, v2
	v_mov_b32_e32 v52, v2
	v_mov_b32_e32 v53, v2
	v_mov_b32_e32 v54, v2
	v_mov_b32_e32 v55, v2
	v_mov_b32_e32 v56, v2
	v_mov_b32_e32 v57, v2
	v_mov_b32_e32 v58, v2
	v_mov_b32_e32 v59, v2
	v_mov_b32_e32 v60, v2
	v_mov_b32_e32 v61, v2
	v_mov_b32_e32 v62, v2
	v_mov_b32_e32 v63, v2
	v_mov_b32_e32 v64, v2
	v_mov_b32_e32 v65, v2
	v_mov_b32_e32 v66, v2
	v_mov_b32_e32 v67, v2
	v_mov_b32_e32 v68, v2
	v_mov_b32_e32 v69, v2
	v_mov_b32_e32 v70, v2
	v_mov_b32_e32 v71, v2
	v_mov_b32_e32 v72, v2
	v_mov_b32_e32 v73, v2
	v_mov_b32_e32 v74, v2
	v_mov_b32_e32 v75, v2
	v_mov_b32_e32 v76, v2
	v_mov_b32_e32 v77, v2
	v_mov_b32_e32 v78, v2
	v_mov_b32_e32 v79, v2
	v_mov_b32_e32 v80, v2
	v_mov_b32_e32 v81, v2
	v_mov_b32_e32 v98, v2
	v_mov_b32_e32 v99, v2
	v_mov_b32_e32 v100, v2
	v_mov_b32_e32 v101, v2
	v_mov_b32_e32 v102, v2
	v_mov_b32_e32 v103, v2
	v_mov_b32_e32 v104, v2
	v_mov_b32_e32 v105, v2
	v_mov_b32_e32 v106, v2
	v_mov_b32_e32 v107, v2
	v_mov_b32_e32 v108, v2
	v_mov_b32_e32 v109, v2
	v_mov_b32_e32 v110, v2
	v_mov_b32_e32 v111, v2
	v_mov_b32_e32 v112, v2
	v_mov_b32_e32 v113, v2
	v_mov_b32_e32 v82, v2
	v_mov_b32_e32 v83, v2
	v_mov_b32_e32 v84, v2
	v_mov_b32_e32 v85, v2
	v_mov_b32_e32 v86, v2
	v_mov_b32_e32 v87, v2
	v_mov_b32_e32 v88, v2
	v_mov_b32_e32 v89, v2
	v_mov_b32_e32 v90, v2
	v_mov_b32_e32 v91, v2
	v_mov_b32_e32 v92, v2
	v_mov_b32_e32 v93, v2
	v_mov_b32_e32 v94, v2
	v_mov_b32_e32 v95, v2
	v_mov_b32_e32 v96, v2
	v_mov_b32_e32 v97, v2
	v_mov_b32_e32 v114, v2
	v_mov_b32_e32 v115, v2
	v_mov_b32_e32 v116, v2
	v_mov_b32_e32 v117, v2
	v_mov_b32_e32 v118, v2
	v_mov_b32_e32 v119, v2
	v_mov_b32_e32 v120, v2
	v_mov_b32_e32 v121, v2
	v_mov_b32_e32 v122, v2
	v_mov_b32_e32 v123, v2
	v_mov_b32_e32 v124, v2
	v_mov_b32_e32 v125, v2
	v_mov_b32_e32 v126, v2
	v_mov_b32_e32 v127, v2
	v_mov_b32_e32 v128, v2
	v_mov_b32_e32 v129, v2
	s_cmp_eq_u64 s[8:9], 0
	s_cbranch_scc0 .Lsp_skip_2000
	s_setprio 1
.Lsp_skip_2000:
.LBB0_2000:
	s_add_i32 s63, s6, 2
	s_add_u32 s7, s28, 0x4000
	s_addc_u32 s30, s29, 0
	s_add_i32 s66, 0, 0x10000
	s_cmp_eq_u32 s12, s6
	v_add_u32_e32 v153, s66, v131
	v_add_u32_e32 v158, s66, v144
	s_cselect_b32 s31, s21, s30
	s_cselect_b32 s30, s20, s7
	ds_read_b128 v[154:157], v153
	ds_read_b128 v[158:161], v158
	v_add_u32_e32 v153, s66, v145
	v_add_u32_e32 v166, s66, v146
	s_cselect_b32 s7, s23, s17
	s_cselect_b32 s6, s22, s13
	s_add_i32 s87, 0, 0x14000
	ds_read_b128 v[162:165], v153
	ds_read_b128 v[166:169], v166
	v_add_u32_e32 v153, s87, v131
	v_add_u32_e32 v174, s87, v144
	ds_read_b128 v[170:173], v153
	ds_read_b128 v[174:177], v174
	v_add_u32_e32 v153, s87, v145
	v_add_u32_e32 v182, s87, v146
	ds_read_b128 v[178:181], v153
	ds_read_b128 v[182:185], v182
	v_lshl_add_u64 v[194:195], s[28:29], 0, v[140:141]
	s_add_i32 m0, s51, 0xc000
	ds_read_b128 v[186:189], v149
	ds_read_b128 v[198:201], v149 offset:4096
	ds_read_b128 v[190:193], v150
	ds_read_b128 v[202:205], v150 offset:4096
	ds_read_b128 v[206:209], v151
	ds_read_b128 v[214:217], v151 offset:4096
	ds_read_b128 v[210:213], v152
	ds_read_b128 v[218:221], v152 offset:4096
	global_load_lds_dwordx4 v[194:195], off
	v_lshl_add_u64 v[194:195], s[28:29], 0, v[142:143]
	s_add_i32 m0, s51, 0xe000
	s_nop 0
	global_load_lds_dwordx4 v[194:195], off
	s_waitcnt vmcnt(8)
	s_waitcnt lgkmcnt(0)
	s_barrier
	s_waitcnt lgkmcnt(0)
	v_mfma_scale_f32_32x32x64_f8f6f4 v[114:129], v[154:161], v[186:193], v[114:129], v233, v234 op_sel_hi:[0,0,0]
	v_mfma_scale_f32_32x32x64_f8f6f4 v[82:97], v[154:161], v[198:205], v[82:97], v233, v234 op_sel_hi:[0,0,0]
	v_mfma_scale_f32_32x32x64_f8f6f4 v[114:129], v[162:169], v[206:213], v[114:129], v233, v234 op_sel_hi:[0,0,0]
	v_mfma_scale_f32_32x32x64_f8f6f4 v[82:97], v[162:169], v[214:221], v[82:97], v233, v234 op_sel_hi:[0,0,0]
	v_mfma_scale_f32_32x32x64_f8f6f4 v[98:113], v[170:177], v[186:193], v[98:113], v233, v234 op_sel_hi:[0,0,0]
	v_mfma_scale_f32_32x32x64_f8f6f4 v[66:81], v[170:177], v[198:205], v[66:81], v233, v234 op_sel_hi:[0,0,0]
	v_mfma_scale_f32_32x32x64_f8f6f4 v[98:113], v[178:185], v[206:213], v[98:113], v233, v234 op_sel_hi:[0,0,0]
	v_mfma_scale_f32_32x32x64_f8f6f4 v[66:81], v[178:185], v[214:221], v[66:81], v233, v234 op_sel_hi:[0,0,0]
	s_barrier
; #define PG8_STAGE(bufoff, gbase, voff) do { _Pragma("unroll") for (int _i = 0; _i < 2; ++_i) \
;         __builtin_amdgcn_global_load_lds((const unsigned*)((const char*)(gbase) + (voff)[_i]), (PG8_LAS unsigned*)(lds + (bufoff) + ldsw + _i * 8192), 16, 0, 0); } while (0)
; #define PG8_LDA(dst, b, h) do { _Pragma("unroll") for (int m = 0; m < 4; ++m) _Pragma("unroll") for (int k = 0; k < 2; ++k) dst[m][k] = *(const PG8_LAS bf16x8*)(lds + PG8_SA(b, h) + aoff + m * 2048 + k * 1024); } while (0)
; #define PG8_LDB(dst, b, h) do { _Pragma("unroll") for (int n = 0; n < 2; ++n) _Pragma("unroll") for (int k = 0; k < 2; ++k) dst[n][k] = *(const PG8_LAS bf16x8*)(lds + PG8_SB(b, h) + boff + n * 2048 + k * 1024); } while (0)
; template <class Epi, class Sched, int SCW, int SCX, int SCW1 = SCW>
; __device__ __forceinline__ void gemm_phase_f8(PG8_LAS unsigned char* lds, const Gemm g, const Sched& S, const Epi& E, const int tid) {
;     ...
;         for (int t = 0; t < nt; t += 2) {
;             const bool last = (t == nt - 2);
;             const char* a1 = cA + (size_t)(t + 1) * kstep;
;             const char* a2 = last ? nA : cA + (size_t)(t + 2) * kstep; const char* b2 = last ? nB : cB + (size_t)(t + 2) * kstepB;
;             const char* a3 = a2 + kstep; const char* b3 = b2 + kstepB;
;             if (last && has_next) S.a_ready(nxt);
;             PG8_LDB(B0, 0, 0); PG8_LDB(B1, 0, 1); PG8_SCHED; PG8_LDA(At, 0, 0); PG8_STAGE(PG8_SA(1, 1), a1 + hstep, voffA);
;             PG8_WAIT_V(8); PG8_WAIT_L(0); PG8_BAR; PG8_MMA(0, 0, At, B0); PG8_MMA(0, 1, At, B1); PG8_BAR; PG8_SCHED;
;             PG8_LDA(At, 0, 1); PG8_STAGE(PG8_SB(0, 0), b2, voffB); PG8_STAGE(PG8_SB(0, 1), b2 + hstepB, voffB); PG8_STAGE(PG8_SA(0, 0), a2, voffA);
;             PG8_WAIT_V(8); PG8_WAIT_L(0); PG8_BAR; PG8_MMA(1, 0, At, B0); PG8_MMA(1, 1, At, B1); PG8_BAR; PG8_SCHED;
;             PG8_LDB(B0, 1, 0); PG8_LDB(B1, 1, 1); PG8_SCHED; PG8_LDA(At, 1, 0); PG8_STAGE(PG8_SA(0, 1), a2 + hstep, voffA);
;             PG8_WAIT_V(8); PG8_WAIT_L(0); PG8_BAR; PG8_MMA(0, 0, At, B0); PG8_MMA(0, 1, At, B1); PG8_BAR; PG8_SCHED;
;             PG8_LDA(At, 1, 1); PG8_STAGE(PG8_SB(1, 0), b3, voffB); PG8_STAGE(PG8_SB(1, 1), b3 + hstepB, voffB); PG8_STAGE(PG8_SA(1, 0), a3, voffA);
;             PG8_WAIT_V(8); PG8_WAIT_L(0); PG8_BAR; PG8_MMA(1, 0, At, B0); PG8_MMA(1, 1, At, B1); PG8_BAR; PG8_SCHED;
;         }
	s_add_i32 s66, s66, s50
	v_lshl_add_u64 v[194:195], s[6:7], 0, v[134:135]
	s_mov_b32 m0, s66
	ds_read_b128 v[186:189], v149 offset:16384
	ds_read_b128 v[198:201], v149 offset:20480
	ds_read_b128 v[190:193], v150 offset:16384
	ds_read_b128 v[202:205], v150 offset:20480
	ds_read_b128 v[206:209], v151 offset:16384
	ds_read_b128 v[214:217], v151 offset:20480
	ds_read_b128 v[210:213], v152 offset:16384
	ds_read_b128 v[218:221], v152 offset:20480
	global_load_lds_dwordx4 v[194:195], off
	s_add_i32 m0, s66, 0x2000
	s_add_u32 s88, s6, 0x4000
	v_lshl_add_u64 v[194:195], s[6:7], 0, v[138:139]
	s_addc_u32 s89, s7, 0
	s_add_i32 s66, s87, s50
	global_load_lds_dwordx4 v[194:195], off
	v_lshl_add_u64 v[194:195], s[88:89], 0, v[134:135]
	s_mov_b32 m0, s66
	v_lshl_add_u64 v[222:223], s[30:31], 0, v[136:137]
	global_load_lds_dwordx4 v[194:195], off
	v_lshl_add_u64 v[194:195], s[88:89], 0, v[138:139]
	s_add_i32 m0, s66, 0x2000
	s_nop 0
	global_load_lds_dwordx4 v[194:195], off
	v_lshl_add_u64 v[194:195], s[30:31], 0, v[132:133]
	s_mov_b32 m0, s51
	s_nop 0
	global_load_lds_dwordx4 v[194:195], off
	s_mov_b32 m0, s52
	s_nop 0
	global_load_lds_dwordx4 v[222:223], off
	s_waitcnt vmcnt(8)
	s_waitcnt lgkmcnt(0)
	s_barrier
	s_waitcnt lgkmcnt(0)
	v_mfma_scale_f32_32x32x64_f8f6f4 v[50:65], v[154:161], v[186:193], v[50:65], v233, v234 op_sel_hi:[0,0,0]
	v_mfma_scale_f32_32x32x64_f8f6f4 v[18:33], v[154:161], v[198:205], v[18:33], v233, v234 op_sel_hi:[0,0,0]
	v_mfma_scale_f32_32x32x64_f8f6f4 v[50:65], v[162:169], v[206:213], v[50:65], v233, v234 op_sel_hi:[0,0,0]
	v_mfma_scale_f32_32x32x64_f8f6f4 v[18:33], v[162:169], v[214:221], v[18:33], v233, v234 op_sel_hi:[0,0,0]
	v_mfma_scale_f32_32x32x64_f8f6f4 v[34:49], v[170:177], v[186:193], v[34:49], v233, v234 op_sel_hi:[0,0,0]
	v_mfma_scale_f32_32x32x64_f8f6f4 v[2:17], v[170:177], v[198:205], v[2:17], v233, v234 op_sel_hi:[0,0,0]
	v_mfma_scale_f32_32x32x64_f8f6f4 v[34:49], v[178:185], v[206:213], v[34:49], v233, v234 op_sel_hi:[0,0,0]
	v_mfma_scale_f32_32x32x64_f8f6f4 v[2:17], v[178:185], v[214:221], v[2:17], v233, v234 op_sel_hi:[0,0,0]
	s_barrier
	s_add_i32 s66, 0, 0x18000
	v_add_u32_e32 v153, s66, v131
	v_add_u32_e32 v158, s66, v144
	ds_read_b128 v[154:157], v153
	ds_read_b128 v[158:161], v158
	v_add_u32_e32 v153, s66, v145
	v_add_u32_e32 v166, s66, v146
	s_add_i32 s87, 0, 0x1c000
	ds_read_b128 v[162:165], v153
	ds_read_b128 v[166:169], v166
	v_add_u32_e32 v153, s87, v131
	v_add_u32_e32 v174, s87, v144
	ds_read_b128 v[170:173], v153
	ds_read_b128 v[174:177], v174
	v_add_u32_e32 v153, s87, v145
	v_add_u32_e32 v182, s87, v146
	ds_read_b128 v[178:181], v153
	ds_read_b128 v[182:185], v182
	s_add_u32 s30, s30, 0x4000
	s_addc_u32 s31, s31, 0
	s_mov_b32 m0, s53
	v_lshl_add_u64 v[224:225], s[30:31], 0, v[132:133]
	ds_read_b128 v[186:189], v149 offset:32768
	ds_read_b128 v[198:201], v149 offset:36864
	ds_read_b128 v[190:193], v150 offset:32768
	ds_read_b128 v[202:205], v150 offset:36864
	ds_read_b128 v[206:209], v151 offset:32768
	ds_read_b128 v[214:217], v151 offset:36864
	ds_read_b128 v[210:213], v152 offset:32768
	ds_read_b128 v[218:221], v152 offset:36864
	global_load_lds_dwordx4 v[224:225], off
	v_lshl_add_u64 v[224:225], s[30:31], 0, v[136:137]
	s_mov_b32 m0, s54
	s_nop 0
	global_load_lds_dwordx4 v[224:225], off
	s_waitcnt vmcnt(8)
	s_waitcnt lgkmcnt(0)
	s_barrier
	s_waitcnt lgkmcnt(0)
	v_mfma_scale_f32_32x32x64_f8f6f4 v[114:129], v[154:161], v[186:193], v[114:129], v233, v234 op_sel_hi:[0,0,0]
	v_mfma_scale_f32_32x32x64_f8f6f4 v[82:97], v[154:161], v[198:205], v[82:97], v233, v234 op_sel_hi:[0,0,0]
	v_mfma_scale_f32_32x32x64_f8f6f4 v[114:129], v[162:169], v[206:213], v[114:129], v233, v234 op_sel_hi:[0,0,0]
	v_mfma_scale_f32_32x32x64_f8f6f4 v[82:97], v[162:169], v[214:221], v[82:97], v233, v234 op_sel_hi:[0,0,0]
	v_mfma_scale_f32_32x32x64_f8f6f4 v[98:113], v[170:177], v[186:193], v[98:113], v233, v234 op_sel_hi:[0,0,0]
	v_mfma_scale_f32_32x32x64_f8f6f4 v[66:81], v[170:177], v[198:205], v[66:81], v233, v234 op_sel_hi:[0,0,0]
	v_mfma_scale_f32_32x32x64_f8f6f4 v[98:113], v[178:185], v[206:213], v[98:113], v233, v234 op_sel_hi:[0,0,0]
	v_mfma_scale_f32_32x32x64_f8f6f4 v[66:81], v[178:185], v[214:221], v[66:81], v233, v234 op_sel_hi:[0,0,0]
	s_barrier
	s_add_u32 s30, s6, 0x8000
	s_addc_u32 s31, s7, 0
	s_add_i32 s66, s66, s50
	v_lshl_add_u64 v[224:225], s[30:31], 0, v[134:135]
	s_mov_b32 m0, s66
	ds_read_b128 v[186:189], v149 offset:49152
	ds_read_b128 v[198:201], v149 offset:53248
	ds_read_b128 v[190:193], v150 offset:49152
	ds_read_b128 v[202:205], v150 offset:53248
	ds_read_b128 v[206:209], v151 offset:49152
	ds_read_b128 v[214:217], v151 offset:53248
	ds_read_b128 v[210:213], v152 offset:49152
	ds_read_b128 v[218:221], v152 offset:53248
	global_load_lds_dwordx4 v[224:225], off
	s_add_i32 m0, s66, 0x2000
	s_add_u32 s6, s6, 0xc000
	v_lshl_add_u64 v[224:225], s[30:31], 0, v[138:139]
	s_addc_u32 s7, s7, 0
	s_add_i32 s30, s87, s50
	global_load_lds_dwordx4 v[224:225], off
	v_lshl_add_u64 v[224:225], s[6:7], 0, v[134:135]
	s_mov_b32 m0, s30
	v_lshl_add_u64 v[194:195], v[194:195], 0, s[100:101]
	global_load_lds_dwordx4 v[224:225], off
	v_lshl_add_u64 v[224:225], s[6:7], 0, v[138:139]
	s_add_i32 m0, s30, 0x2000
	s_nop 0
	global_load_lds_dwordx4 v[224:225], off
	s_mov_b32 m0, s59
	s_nop 0
	global_load_lds_dwordx4 v[194:195], off
	v_lshl_add_u64 v[194:195], v[222:223], 0, s[100:101]
	s_mov_b32 m0, s60
	s_nop 0
	global_load_lds_dwordx4 v[194:195], off
	s_waitcnt vmcnt(8)
	s_waitcnt lgkmcnt(0)
	s_barrier
	s_waitcnt lgkmcnt(0)
	v_mfma_scale_f32_32x32x64_f8f6f4 v[50:65], v[154:161], v[186:193], v[50:65], v233, v234 op_sel_hi:[0,0,0]
	v_mfma_scale_f32_32x32x64_f8f6f4 v[18:33], v[154:161], v[198:205], v[18:33], v233, v234 op_sel_hi:[0,0,0]
	v_mfma_scale_f32_32x32x64_f8f6f4 v[50:65], v[162:169], v[206:213], v[50:65], v233, v234 op_sel_hi:[0,0,0]
	v_mfma_scale_f32_32x32x64_f8f6f4 v[18:33], v[162:169], v[214:221], v[18:33], v233, v234 op_sel_hi:[0,0,0]
	v_mfma_scale_f32_32x32x64_f8f6f4 v[34:49], v[170:177], v[186:193], v[34:49], v233, v234 op_sel_hi:[0,0,0]
	v_mfma_scale_f32_32x32x64_f8f6f4 v[2:17], v[170:177], v[198:205], v[2:17], v233, v234 op_sel_hi:[0,0,0]
	v_mfma_scale_f32_32x32x64_f8f6f4 v[34:49], v[178:185], v[206:213], v[34:49], v233, v234 op_sel_hi:[0,0,0]
	v_mfma_scale_f32_32x32x64_f8f6f4 v[2:17], v[178:185], v[214:221], v[2:17], v233, v234 op_sel_hi:[0,0,0]
	s_barrier
	s_add_u32 s13, s13, 0x10000
	s_addc_u32 s17, s17, 0
	s_add_u32 s28, s28, 0x10000
	s_addc_u32 s29, s29, 0
	s_cmp_ge_i32 s63, s24
	s_mov_b32 s6, s63
	s_cbranch_scc0 .LBB0_2000
	s_setprio 0
	s_and_b64 vcc, exec, s[8:9]
	s_cbranch_vccz .LBB0_2003
	s_barrier

; #define PG8_STAGE(bufoff, gbase, voff) do { _Pragma("unroll") for (int _i = 0; _i < 2; ++_i) \
;         __builtin_amdgcn_global_load_lds((const unsigned*)((const char*)(gbase) + (voff)[_i]), (PG8_LAS unsigned*)(lds + (bufoff) + ldsw + _i * 8192), 16, 0, 0); } while (0)
; #define PG8_LDA(dst, b, h) do { _Pragma("unroll") for (int m = 0; m < 4; ++m) _Pragma("unroll") for (int k = 0; k < 2; ++k) dst[m][k] = *(const PG8_LAS bf16x8*)(lds + PG8_SA(b, h) + aoff + m * 2048 + k * 1024); } while (0)
; #define PG8_LDB(dst, b, h) do { _Pragma("unroll") for (int n = 0; n < 2; ++n) _Pragma("unroll") for (int k = 0; k < 2; ++k) dst[n][k] = *(const PG8_LAS bf16x8*)(lds + PG8_SB(b, h) + boff + n * 2048 + k * 1024); } while (0)
; #define PG8_WAIT_V(n) asm volatile("s_waitcnt vmcnt(" #n ")" ::: "memory")
; #define PG8_WAIT_L(n) asm volatile("s_waitcnt lgkmcnt(" #n ")" ::: "memory")
; #define PG8_BAR __builtin_amdgcn_s_barrier()
; #define PG8_SCHED __builtin_amdgcn_sched_barrier(0)
; template <class Epi, class Sched, bool ALIGN_EPI = false, bool SP2 = false>
; __device__ __forceinline__ void gemm_phase(PG8_LAS unsigned char* lds, const Gemm g, const Sched& S, const Epi& E, const int tid) {
;     ...
;         for (int t = 0; t < nt; t += 2) {
;             const bool last = (t == nt - 2);
;             const char* a1 = cA + (size_t)(t + 1) * kstep;
;             const char* a2 = last ? nA : cA + (size_t)(t + 2) * kstep; const char* b2 = last ? nB : cB + (size_t)(t + 2) * kstep;
;             const char* a3 = a2 + kstep; const char* b3 = b2 + kstep;
;             if (last && has_next) S.a_ready(nxt);
;             if constexpr (SP2) {
;             PG8_LDB(B0, 0, 0); PG8_LDB(B1, 0, 1); PG8_SCHED; PG8_LDA(At, 0, 0); PG8_STAGE(PG8_SA(1, 1), a1 + hstep, voffA);
;             PG8_WAIT_V(8); PG8_WAIT_L(0); PG8_BAR; PG8_MMA(0, 0, At, B0); PG8_MMA(0, 1, At, B1); PG8_BAR; PG8_SCHED;
;             PG8_LDA(At, 0, 1); PG8_STAGE(PG8_SB(0, 0), b2, voffB); PG8_STAGE(PG8_SB(0, 1), b2 + hstep, voffB); PG8_STAGE(PG8_SA(0, 0), a2, voffA);
;     ...
; #pragma unroll
;         for (int a = 0; a < 2; ++a)
; #pragma unroll
;             for (int b = 0; b < 2; ++b)
; #pragma unroll
;                 for (int m = 0; m < 4; ++m)
; #pragma unroll
;                     for (int n = 0; n < 2; ++n) acc[a][b][m][n] = (f32x4){0.f, 0.f, 0.f, 0.f};
;         cur = nxt; cA = nA; cB = nB; ++ui; nt = cur.nt;
.LBB0_2281:
	s_ashr_i32 s47, s46, 31
	s_lshl_b64 s[12:13], s[46:47], 20
	s_add_u32 s50, s58, s12
	s_addc_u32 s51, s59, s13
	s_and_b64 s[12:13], s[48:49], exec
	s_cselect_b32 s5, s51, s55
	s_cselect_b32 s12, s50, s54
	s_ashr_i32 s31, s30, 31
	s_lshl_b64 s[18:19], s[30:31], 20
	s_add_u32 s52, s60, s18
	s_addc_u32 s53, s61, s19
	s_and_b64 s[18:19], s[48:49], exec
	s_cselect_b32 s13, s53, s7
	s_cselect_b32 s15, s52, s6
	s_add_u32 s54, s54, 0x80080
	s_addc_u32 s55, s55, 0
	s_add_u32 s18, s6, 0x100
	s_waitcnt vmcnt(0)
	v_mov_b32_e32 v6, 0
	s_addc_u32 s19, s7, 0
	s_mov_b32 s24, -2
	v_mov_b32_e32 v7, v6
	v_mov_b32_e32 v8, v6
	v_mov_b32_e32 v9, v6
	v_mov_b32_e32 v14, v6
	v_mov_b32_e32 v15, v6
	v_mov_b32_e32 v16, v6
	v_mov_b32_e32 v17, v6
	v_mov_b32_e32 v22, v6
	v_mov_b32_e32 v23, v6
	v_mov_b32_e32 v24, v6
	v_mov_b32_e32 v25, v6
	v_mov_b32_e32 v30, v6
	v_mov_b32_e32 v31, v6
	v_mov_b32_e32 v32, v6
	v_mov_b32_e32 v33, v6
	v_mov_b32_e32 v38, v6
	v_mov_b32_e32 v39, v6
	v_mov_b32_e32 v40, v6
	v_mov_b32_e32 v41, v6
	v_mov_b32_e32 v46, v6
	v_mov_b32_e32 v47, v6
	v_mov_b32_e32 v48, v6
	v_mov_b32_e32 v49, v6
	v_mov_b32_e32 v54, v6
	v_mov_b32_e32 v55, v6
	v_mov_b32_e32 v56, v6
	v_mov_b32_e32 v57, v6
	v_mov_b32_e32 v62, v6
	v_mov_b32_e32 v63, v6
	v_mov_b32_e32 v64, v6
	v_mov_b32_e32 v65, v6
	v_mov_b32_e32 v2, v6
	v_mov_b32_e32 v3, v6
	v_mov_b32_e32 v4, v6
	v_mov_b32_e32 v5, v6
	v_mov_b32_e32 v10, v6
	v_mov_b32_e32 v11, v6
	v_mov_b32_e32 v12, v6
	v_mov_b32_e32 v13, v6
	v_mov_b32_e32 v18, v6
	v_mov_b32_e32 v19, v6
	v_mov_b32_e32 v20, v6
	v_mov_b32_e32 v21, v6
	v_mov_b32_e32 v26, v6
	v_mov_b32_e32 v27, v6
	v_mov_b32_e32 v28, v6
	v_mov_b32_e32 v29, v6
	v_mov_b32_e32 v34, v6
	v_mov_b32_e32 v35, v6
	v_mov_b32_e32 v36, v6
	v_mov_b32_e32 v37, v6
	v_mov_b32_e32 v42, v6
	v_mov_b32_e32 v43, v6
	v_mov_b32_e32 v44, v6
	v_mov_b32_e32 v45, v6
	v_mov_b32_e32 v50, v6
	v_mov_b32_e32 v51, v6
	v_mov_b32_e32 v52, v6
	v_mov_b32_e32 v53, v6
	v_mov_b32_e32 v58, v6
	v_mov_b32_e32 v59, v6
	v_mov_b32_e32 v60, v6
	v_mov_b32_e32 v61, v6
	v_mov_b32_e32 v70, v6
	v_mov_b32_e32 v71, v6
	v_mov_b32_e32 v72, v6
	v_mov_b32_e32 v73, v6
	v_mov_b32_e32 v78, v6
	v_mov_b32_e32 v79, v6
	v_mov_b32_e32 v80, v6
	v_mov_b32_e32 v81, v6
	v_mov_b32_e32 v86, v6
	v_mov_b32_e32 v87, v6
	v_mov_b32_e32 v88, v6
	v_mov_b32_e32 v89, v6
	v_mov_b32_e32 v94, v6
	v_mov_b32_e32 v95, v6
	v_mov_b32_e32 v96, v6
	v_mov_b32_e32 v97, v6
	v_mov_b32_e32 v102, v6
	v_mov_b32_e32 v103, v6
	v_mov_b32_e32 v104, v6
	v_mov_b32_e32 v105, v6
	v_mov_b32_e32 v110, v6
	v_mov_b32_e32 v111, v6
	v_mov_b32_e32 v112, v6
	v_mov_b32_e32 v113, v6
	v_mov_b32_e32 v118, v6
	v_mov_b32_e32 v119, v6
	v_mov_b32_e32 v120, v6
	v_mov_b32_e32 v121, v6
	v_mov_b32_e32 v126, v6
	v_mov_b32_e32 v127, v6
	v_mov_b32_e32 v128, v6
	v_mov_b32_e32 v129, v6
	v_mov_b32_e32 v66, v6
	v_mov_b32_e32 v67, v6
	v_mov_b32_e32 v68, v6
	v_mov_b32_e32 v69, v6
	v_mov_b32_e32 v74, v6
	v_mov_b32_e32 v75, v6
	v_mov_b32_e32 v76, v6
	v_mov_b32_e32 v77, v6
	v_mov_b32_e32 v82, v6
	v_mov_b32_e32 v83, v6
	v_mov_b32_e32 v84, v6
	v_mov_b32_e32 v85, v6
	v_mov_b32_e32 v90, v6
	v_mov_b32_e32 v91, v6
	v_mov_b32_e32 v92, v6
	v_mov_b32_e32 v93, v6
	v_mov_b32_e32 v98, v6
	v_mov_b32_e32 v99, v6
	v_mov_b32_e32 v100, v6
	v_mov_b32_e32 v101, v6
	v_mov_b32_e32 v106, v6
	v_mov_b32_e32 v107, v6
	v_mov_b32_e32 v108, v6
	v_mov_b32_e32 v109, v6
	v_mov_b32_e32 v114, v6
	v_mov_b32_e32 v115, v6
	v_mov_b32_e32 v116, v6
	v_mov_b32_e32 v117, v6
	v_mov_b32_e32 v122, v6
	v_mov_b32_e32 v123, v6
	v_mov_b32_e32 v124, v6
	v_mov_b32_e32 v125, v6
	s_cmp_eq_u64 s[10:11], 0
	s_cbranch_scc0 .Lsp_skip_2282
	s_setprio 1
.Lsp_skip_2282:
.LBB0_2282:
	s_add_u32 s6, s54, 0xfff80080
	s_addc_u32 s7, s55, -1
	s_add_i32 s26, 0, 0x10000
	s_cmp_eq_u32 s24, 28
	s_cselect_b32 s57, s5, s7
	s_cselect_b32 s56, s12, s6
	v_add_u32_e32 v131, s26, v156
	s_cselect_b32 s7, s13, s19
	s_cselect_b32 s6, s15, s18
	s_add_i32 s31, 0, 0x14000
	ds_read_b128 v[172:175], v131
	ds_read_b128 v[176:179], v131 offset:1024
	ds_read_b128 v[180:183], v131 offset:2048
	ds_read_b128 v[184:187], v131 offset:3072
	v_add_u32_e32 v131, s31, v156
	ds_read_b128 v[188:191], v131
	ds_read_b128 v[192:195], v131 offset:1024
	ds_read_b128 v[198:201], v131 offset:2048
	ds_read_b128 v[202:205], v131 offset:3072
	v_lshl_add_u64 v[132:133], s[54:55], 0, v[148:149]
	s_add_i32 m0, s65, 0xc000
	ds_read_b128 v[206:209], v170
	ds_read_b128 v[210:213], v170 offset:1024
	ds_read_b128 v[214:217], v170 offset:2048
	ds_read_b128 v[218:221], v170 offset:3072
	ds_read_b128 v[222:225], v170 offset:4096
	ds_read_b128 v[226:229], v170 offset:5120
	ds_read_b128 v[244:247], v170 offset:6144
	ds_read_b128 v[248:251], v170 offset:7168
	global_load_lds_dwordx4 v[132:133], off
	v_lshl_add_u64 v[132:133], s[54:55], 0, v[150:151]
	s_add_i32 m0, s65, 0xe000
	s_nop 0
	global_load_lds_dwordx4 v[132:133], off
	s_waitcnt vmcnt(8)
	s_waitcnt lgkmcnt(0)
	s_barrier
; #define PG8_STAGE(bufoff, gbase, voff) do { _Pragma("unroll") for (int _i = 0; _i < 2; ++_i) \
;         __builtin_amdgcn_global_load_lds((const unsigned*)((const char*)(gbase) + (voff)[_i]), (PG8_LAS unsigned*)(lds + (bufoff) + ldsw + _i * 8192), 16, 0, 0); } while (0)
; #define PG8_LDA(dst, b, h) do { _Pragma("unroll") for (int m = 0; m < 4; ++m) _Pragma("unroll") for (int k = 0; k < 2; ++k) dst[m][k] = *(const PG8_LAS bf16x8*)(lds + PG8_SA(b, h) + aoff + m * 2048 + k * 1024); } while (0)
; #define PG8_LDB(dst, b, h) do { _Pragma("unroll") for (int n = 0; n < 2; ++n) _Pragma("unroll") for (int k = 0; k < 2; ++k) dst[n][k] = *(const PG8_LAS bf16x8*)(lds + PG8_SB(b, h) + boff + n * 2048 + k * 1024); } while (0)
; #define PG8_MMA(ai, bj, At, Bt) do { __builtin_amdgcn_s_setprio(1); _Pragma("unroll") for (int m = 0; m < 4; ++m) _Pragma("unroll") for (int n = 0; n < 2; ++n) _Pragma("unroll") for (int k = 0; k < 2; ++k) \
;         acc[ai][bj][m][n] = __builtin_amdgcn_mfma_f32_16x16x32_bf16(Bt[n][k], At[m][k], acc[ai][bj][m][n], 0, 0, 0); __builtin_amdgcn_s_setprio(0); } while (0)
; #define PG8_WAIT_V(n) asm volatile("s_waitcnt vmcnt(" #n ")" ::: "memory")
; #define PG8_BAR __builtin_amdgcn_s_barrier()
; template <class Epi, class Sched, bool ALIGN_EPI = false, bool SP2 = false>
; __device__ __forceinline__ void gemm_phase(PG8_LAS unsigned char* lds, const Gemm g, const Sched& S, const Epi& E, const int tid) {
;     ...
;         for (int t = 0; t < nt; t += 2) {
;             const bool last = (t == nt - 2);
;             const char* a1 = cA + (size_t)(t + 1) * kstep;
;             const char* a2 = last ? nA : cA + (size_t)(t + 2) * kstep; const char* b2 = last ? nB : cB + (size_t)(t + 2) * kstep;
;             const char* a3 = a2 + kstep; const char* b3 = b2 + kstep;
;             if (last && has_next) S.a_ready(nxt);
;             if constexpr (SP2) {
;             PG8_LDB(B0, 0, 0); PG8_LDB(B1, 0, 1); PG8_SCHED; PG8_LDA(At, 0, 0); PG8_STAGE(PG8_SA(1, 1), a1 + hstep, voffA);
;             PG8_WAIT_V(8); PG8_WAIT_L(0); PG8_BAR; PG8_MMA(0, 0, At, B0); PG8_MMA(0, 1, At, B1); PG8_BAR; PG8_SCHED;
;             PG8_LDA(At, 0, 1); PG8_STAGE(PG8_SB(0, 0), b2, voffB); PG8_STAGE(PG8_SB(0, 1), b2 + hstep, voffB); PG8_STAGE(PG8_SA(0, 0), a2, voffA);
;             PG8_WAIT_V(8); PG8_WAIT_L(0); PG8_BAR; PG8_MMA(1, 0, At, B0); PG8_MMA(1, 1, At, B1); PG8_BAR; PG8_SCHED;
	s_waitcnt lgkmcnt(0)
	v_mfma_f32_16x16x32_bf16 v[122:125], v[172:175], v[206:209], v[122:125]
	v_mfma_f32_16x16x32_bf16 v[114:117], v[180:183], v[206:209], v[114:117]
	v_mfma_f32_16x16x32_bf16 v[106:109], v[172:175], v[214:217], v[106:109]
	v_mfma_f32_16x16x32_bf16 v[98:101], v[180:183], v[214:217], v[98:101]
	v_mfma_f32_16x16x32_bf16 v[90:93], v[172:175], v[222:225], v[90:93]
	v_mfma_f32_16x16x32_bf16 v[82:85], v[180:183], v[222:225], v[82:85]
	v_mfma_f32_16x16x32_bf16 v[74:77], v[172:175], v[244:247], v[74:77]
	v_mfma_f32_16x16x32_bf16 v[66:69], v[180:183], v[244:247], v[66:69]
	v_mfma_f32_16x16x32_bf16 v[122:125], v[176:179], v[210:213], v[122:125]
	v_mfma_f32_16x16x32_bf16 v[114:117], v[184:187], v[210:213], v[114:117]
	v_mfma_f32_16x16x32_bf16 v[106:109], v[176:179], v[218:221], v[106:109]
	v_mfma_f32_16x16x32_bf16 v[98:101], v[184:187], v[218:221], v[98:101]
	v_mfma_f32_16x16x32_bf16 v[90:93], v[176:179], v[226:229], v[90:93]
	v_mfma_f32_16x16x32_bf16 v[82:85], v[184:187], v[226:229], v[82:85]
	v_mfma_f32_16x16x32_bf16 v[74:77], v[176:179], v[248:251], v[74:77]
	v_mfma_f32_16x16x32_bf16 v[66:69], v[184:187], v[248:251], v[66:69]
	v_mfma_f32_16x16x32_bf16 v[126:129], v[188:191], v[206:209], v[126:129]
	v_mfma_f32_16x16x32_bf16 v[118:121], v[198:201], v[206:209], v[118:121]
	v_mfma_f32_16x16x32_bf16 v[110:113], v[188:191], v[214:217], v[110:113]
	v_mfma_f32_16x16x32_bf16 v[102:105], v[198:201], v[214:217], v[102:105]
	v_mfma_f32_16x16x32_bf16 v[94:97], v[188:191], v[222:225], v[94:97]
	v_mfma_f32_16x16x32_bf16 v[86:89], v[198:201], v[222:225], v[86:89]
	v_mfma_f32_16x16x32_bf16 v[78:81], v[188:191], v[244:247], v[78:81]
	v_mfma_f32_16x16x32_bf16 v[70:73], v[198:201], v[244:247], v[70:73]
	v_mfma_f32_16x16x32_bf16 v[126:129], v[192:195], v[210:213], v[126:129]
	v_mfma_f32_16x16x32_bf16 v[118:121], v[202:205], v[210:213], v[118:121]
	v_mfma_f32_16x16x32_bf16 v[110:113], v[192:195], v[218:221], v[110:113]
	v_mfma_f32_16x16x32_bf16 v[102:105], v[202:205], v[218:221], v[102:105]
	v_mfma_f32_16x16x32_bf16 v[94:97], v[192:195], v[226:229], v[94:97]
	v_mfma_f32_16x16x32_bf16 v[86:89], v[202:205], v[226:229], v[86:89]
	v_mfma_f32_16x16x32_bf16 v[78:81], v[192:195], v[248:251], v[78:81]
	v_mfma_f32_16x16x32_bf16 v[70:73], v[202:205], v[248:251], v[70:73]
	s_barrier
	s_add_i32 s26, s26, s64
	v_lshl_add_u64 v[132:133], s[6:7], 0, v[136:137]
	s_mov_b32 m0, s26
	ds_read_b128 v[206:209], v170 offset:16384
	ds_read_b128 v[210:213], v170 offset:17408
	ds_read_b128 v[214:217], v170 offset:18432
	ds_read_b128 v[218:221], v170 offset:19456
	ds_read_b128 v[222:225], v170 offset:20480
	ds_read_b128 v[226:229], v170 offset:21504
	ds_read_b128 v[244:247], v170 offset:22528
	ds_read_b128 v[248:251], v170 offset:23552
	global_load_lds_dwordx4 v[132:133], off
	s_add_i32 m0, s26, 0x2000
	s_add_u32 s36, s6, 0x80000
	v_lshl_add_u64 v[152:153], s[6:7], 0, v[140:141]
	s_addc_u32 s37, s7, 0
	s_add_i32 s26, s31, s64
	global_load_lds_dwordx4 v[152:153], off
	v_lshl_add_u64 v[230:231], s[36:37], 0, v[136:137]
	s_mov_b32 m0, s26
	v_lshl_add_u64 v[242:243], s[56:57], 0, v[138:139]
	global_load_lds_dwordx4 v[230:231], off
	v_lshl_add_u64 v[230:231], s[36:37], 0, v[140:141]
	s_add_i32 m0, s26, 0x2000
	s_nop 0
	global_load_lds_dwordx4 v[230:231], off
	v_lshl_add_u64 v[230:231], s[56:57], 0, v[134:135]
	s_mov_b32 m0, s65
	s_nop 0
	global_load_lds_dwordx4 v[230:231], off
	s_mov_b32 m0, s68
	s_nop 0
	global_load_lds_dwordx4 v[242:243], off
	s_waitcnt vmcnt(8)
	s_waitcnt lgkmcnt(0)
	s_barrier
	s_waitcnt lgkmcnt(0)
	v_mfma_f32_16x16x32_bf16 v[58:61], v[172:175], v[206:209], v[58:61]
	v_mfma_f32_16x16x32_bf16 v[50:53], v[180:183], v[206:209], v[50:53]
	v_mfma_f32_16x16x32_bf16 v[42:45], v[172:175], v[214:217], v[42:45]
	v_mfma_f32_16x16x32_bf16 v[34:37], v[180:183], v[214:217], v[34:37]
	v_mfma_f32_16x16x32_bf16 v[26:29], v[172:175], v[222:225], v[26:29]
	v_mfma_f32_16x16x32_bf16 v[18:21], v[180:183], v[222:225], v[18:21]
	v_mfma_f32_16x16x32_bf16 v[10:13], v[172:175], v[244:247], v[10:13]
	v_mfma_f32_16x16x32_bf16 v[2:5], v[180:183], v[244:247], v[2:5]
	v_mfma_f32_16x16x32_bf16 v[58:61], v[176:179], v[210:213], v[58:61]
	v_mfma_f32_16x16x32_bf16 v[50:53], v[184:187], v[210:213], v[50:53]
	v_mfma_f32_16x16x32_bf16 v[42:45], v[176:179], v[218:221], v[42:45]
	v_mfma_f32_16x16x32_bf16 v[34:37], v[184:187], v[218:221], v[34:37]
	v_mfma_f32_16x16x32_bf16 v[26:29], v[176:179], v[226:229], v[26:29]
	v_mfma_f32_16x16x32_bf16 v[18:21], v[184:187], v[226:229], v[18:21]
	v_mfma_f32_16x16x32_bf16 v[10:13], v[176:179], v[248:251], v[10:13]
	v_mfma_f32_16x16x32_bf16 v[2:5], v[184:187], v[248:251], v[2:5]
	v_mfma_f32_16x16x32_bf16 v[62:65], v[188:191], v[206:209], v[62:65]
	v_mfma_f32_16x16x32_bf16 v[54:57], v[198:201], v[206:209], v[54:57]
	v_mfma_f32_16x16x32_bf16 v[46:49], v[188:191], v[214:217], v[46:49]
	v_mfma_f32_16x16x32_bf16 v[38:41], v[198:201], v[214:217], v[38:41]
	v_mfma_f32_16x16x32_bf16 v[30:33], v[188:191], v[222:225], v[30:33]
	v_mfma_f32_16x16x32_bf16 v[22:25], v[198:201], v[222:225], v[22:25]
	v_mfma_f32_16x16x32_bf16 v[14:17], v[188:191], v[244:247], v[14:17]
	v_mfma_f32_16x16x32_bf16 v[6:9], v[198:201], v[244:247], v[6:9]
	v_mfma_f32_16x16x32_bf16 v[62:65], v[192:195], v[210:213], v[62:65]
	v_mfma_f32_16x16x32_bf16 v[54:57], v[202:205], v[210:213], v[54:57]
	v_mfma_f32_16x16x32_bf16 v[46:49], v[192:195], v[218:221], v[46:49]
	v_mfma_f32_16x16x32_bf16 v[38:41], v[202:205], v[218:221], v[38:41]
	v_mfma_f32_16x16x32_bf16 v[30:33], v[192:195], v[226:229], v[30:33]
	v_mfma_f32_16x16x32_bf16 v[22:25], v[202:205], v[226:229], v[22:25]
	v_mfma_f32_16x16x32_bf16 v[14:17], v[192:195], v[248:251], v[14:17]
	v_mfma_f32_16x16x32_bf16 v[6:9], v[202:205], v[248:251], v[6:9]
	s_barrier
; #define PG8_STAGE(bufoff, gbase, voff) do { _Pragma("unroll") for (int _i = 0; _i < 2; ++_i) \
;         __builtin_amdgcn_global_load_lds((const unsigned*)((const char*)(gbase) + (voff)[_i]), (PG8_LAS unsigned*)(lds + (bufoff) + ldsw + _i * 8192), 16, 0, 0); } while (0)
; #define PG8_LDA(dst, b, h) do { _Pragma("unroll") for (int m = 0; m < 4; ++m) _Pragma("unroll") for (int k = 0; k < 2; ++k) dst[m][k] = *(const PG8_LAS bf16x8*)(lds + PG8_SA(b, h) + aoff + m * 2048 + k * 1024); } while (0)
; #define PG8_LDB(dst, b, h) do { _Pragma("unroll") for (int n = 0; n < 2; ++n) _Pragma("unroll") for (int k = 0; k < 2; ++k) dst[n][k] = *(const PG8_LAS bf16x8*)(lds + PG8_SB(b, h) + boff + n * 2048 + k * 1024); } while (0)
; #define PG8_MMA(ai, bj, At, Bt) do { __builtin_amdgcn_s_setprio(1); _Pragma("unroll") for (int m = 0; m < 4; ++m) _Pragma("unroll") for (int n = 0; n < 2; ++n) _Pragma("unroll") for (int k = 0; k < 2; ++k) \
;         acc[ai][bj][m][n] = __builtin_amdgcn_mfma_f32_16x16x32_bf16(Bt[n][k], At[m][k], acc[ai][bj][m][n], 0, 0, 0); __builtin_amdgcn_s_setprio(0); } while (0)
; #define PG8_WAIT_V(n) asm volatile("s_waitcnt vmcnt(" #n ")" ::: "memory")
; #define PG8_WAIT_L(n) asm volatile("s_waitcnt lgkmcnt(" #n ")" ::: "memory")
; #define PG8_BAR __builtin_amdgcn_s_barrier()
; #define PG8_SCHED __builtin_amdgcn_sched_barrier(0)
; #define PG8_STAGE(bufoff, gbase, voff) do { _Pragma("unroll") for (int _i = 0; _i < 2; ++_i) \
;         __builtin_amdgcn_global_load_lds((const unsigned*)((const char*)(gbase) + (voff)[_i]), (PG8_LAS unsigned*)(lds + (bufoff) + ldsw + _i * 8192), 16, 0, 0); } while (0)
; #define PG8_LDA(dst, b, h) do { _Pragma("unroll") for (int mb = 0; mb < 2; ++mb) _Pragma("unroll") for (int s = 0; s < 2; ++s) \
;         dst[mb][s] = cat8(*(const PG8_LAS bf16x8*)(lds + PG8_SA(b, h) + aoffk[s][0] + mb * 4096), *(const PG8_LAS bf16x8*)(lds + PG8_SA(b, h) + aoffk[s][1] + mb * 4096)); } while (0)
; template <class Epi, class Sched, bool ALIGN_EPI = false, bool SP2 = false>
; __device__ __forceinline__ void gemm_phase(PG8_LAS unsigned char* lds, const Gemm g, const Sched& S, const Epi& E, const int tid) {
;     ...
;             PG8_LDB(B0, 1, 0); PG8_LDB(B1, 1, 1); PG8_SCHED; PG8_LDA(At, 1, 0); PG8_STAGE(PG8_SA(0, 1), a2 + hstep, voffA);
;             PG8_WAIT_V(8); PG8_WAIT_L(0); PG8_BAR; PG8_MMA(0, 0, At, B0); PG8_MMA(0, 1, At, B1); PG8_BAR; PG8_SCHED;
	s_add_i32 s26, 0, 0x18000
	v_add_u32_e32 v131, s26, v156
	s_add_i32 s31, 0, 0x1c000
	ds_read_b128 v[172:175], v131
	ds_read_b128 v[176:179], v131 offset:1024
	ds_read_b128 v[180:183], v131 offset:2048
	ds_read_b128 v[184:187], v131 offset:3072
	v_add_u32_e32 v131, s31, v156
	ds_read_b128 v[188:191], v131
	ds_read_b128 v[192:195], v131 offset:1024
	ds_read_b128 v[198:201], v131 offset:2048
	ds_read_b128 v[202:205], v131 offset:3072
	s_add_u32 s36, s56, 0x80000
	s_addc_u32 s37, s57, 0
	s_mov_b32 m0, s69
	v_lshl_add_u64 v[158:159], s[36:37], 0, v[134:135]
	ds_read_b128 v[206:209], v170 offset:32768
	ds_read_b128 v[210:213], v170 offset:33792
	ds_read_b128 v[214:217], v170 offset:34816
	ds_read_b128 v[218:221], v170 offset:35840
	ds_read_b128 v[222:225], v170 offset:36864
	ds_read_b128 v[226:229], v170 offset:37888
	ds_read_b128 v[244:247], v170 offset:38912
	ds_read_b128 v[248:251], v170 offset:39936
	global_load_lds_dwordx4 v[158:159], off
	v_lshl_add_u64 v[158:159], s[36:37], 0, v[138:139]
	s_mov_b32 m0, s70
	s_nop 0
	global_load_lds_dwordx4 v[158:159], off
	s_waitcnt vmcnt(8)
	s_waitcnt lgkmcnt(0)
	s_barrier
	s_waitcnt lgkmcnt(0)
	v_mfma_f32_16x16x32_bf16 v[122:125], v[172:175], v[206:209], v[122:125]
	v_mfma_f32_16x16x32_bf16 v[114:117], v[180:183], v[206:209], v[114:117]
	v_mfma_f32_16x16x32_bf16 v[106:109], v[172:175], v[214:217], v[106:109]
	v_mfma_f32_16x16x32_bf16 v[98:101], v[180:183], v[214:217], v[98:101]
	v_mfma_f32_16x16x32_bf16 v[90:93], v[172:175], v[222:225], v[90:93]
	v_mfma_f32_16x16x32_bf16 v[82:85], v[180:183], v[222:225], v[82:85]
	v_mfma_f32_16x16x32_bf16 v[74:77], v[172:175], v[244:247], v[74:77]
	v_mfma_f32_16x16x32_bf16 v[66:69], v[180:183], v[244:247], v[66:69]
	v_mfma_f32_16x16x32_bf16 v[122:125], v[176:179], v[210:213], v[122:125]
	v_mfma_f32_16x16x32_bf16 v[114:117], v[184:187], v[210:213], v[114:117]
	v_mfma_f32_16x16x32_bf16 v[106:109], v[176:179], v[218:221], v[106:109]
	v_mfma_f32_16x16x32_bf16 v[98:101], v[184:187], v[218:221], v[98:101]
	v_mfma_f32_16x16x32_bf16 v[90:93], v[176:179], v[226:229], v[90:93]
	v_mfma_f32_16x16x32_bf16 v[82:85], v[184:187], v[226:229], v[82:85]
	v_mfma_f32_16x16x32_bf16 v[74:77], v[176:179], v[248:251], v[74:77]
	v_mfma_f32_16x16x32_bf16 v[66:69], v[184:187], v[248:251], v[66:69]
	v_mfma_f32_16x16x32_bf16 v[126:129], v[188:191], v[206:209], v[126:129]
	v_mfma_f32_16x16x32_bf16 v[118:121], v[198:201], v[206:209], v[118:121]
	v_mfma_f32_16x16x32_bf16 v[110:113], v[188:191], v[214:217], v[110:113]
	v_mfma_f32_16x16x32_bf16 v[102:105], v[198:201], v[214:217], v[102:105]
	v_mfma_f32_16x16x32_bf16 v[94:97], v[188:191], v[222:225], v[94:97]
	v_mfma_f32_16x16x32_bf16 v[86:89], v[198:201], v[222:225], v[86:89]
	v_mfma_f32_16x16x32_bf16 v[78:81], v[188:191], v[244:247], v[78:81]
	v_mfma_f32_16x16x32_bf16 v[70:73], v[198:201], v[244:247], v[70:73]
	v_mfma_f32_16x16x32_bf16 v[126:129], v[192:195], v[210:213], v[126:129]
	v_mfma_f32_16x16x32_bf16 v[118:121], v[202:205], v[210:213], v[118:121]
	v_mfma_f32_16x16x32_bf16 v[110:113], v[192:195], v[218:221], v[110:113]
	v_mfma_f32_16x16x32_bf16 v[102:105], v[202:205], v[218:221], v[102:105]
	v_mfma_f32_16x16x32_bf16 v[94:97], v[192:195], v[226:229], v[94:97]
	v_mfma_f32_16x16x32_bf16 v[86:89], v[202:205], v[226:229], v[86:89]
	v_mfma_f32_16x16x32_bf16 v[78:81], v[192:195], v[248:251], v[78:81]
	v_mfma_f32_16x16x32_bf16 v[70:73], v[202:205], v[248:251], v[70:73]
	s_barrier
; #define PG8_STAGE(bufoff, gbase, voff) do { _Pragma("unroll") for (int _i = 0; _i < 2; ++_i) \
;         __builtin_amdgcn_global_load_lds((const unsigned*)((const char*)(gbase) + (voff)[_i]), (PG8_LAS unsigned*)(lds + (bufoff) + ldsw + _i * 8192), 16, 0, 0); } while (0)
; #define PG8_LDA(dst, b, h) do { _Pragma("unroll") for (int m = 0; m < 4; ++m) _Pragma("unroll") for (int k = 0; k < 2; ++k) dst[m][k] = *(const PG8_LAS bf16x8*)(lds + PG8_SA(b, h) + aoff + m * 2048 + k * 1024); } while (0)
; #define PG8_MMA(ai, bj, At, Bt) do { __builtin_amdgcn_s_setprio(1); _Pragma("unroll") for (int m = 0; m < 4; ++m) _Pragma("unroll") for (int n = 0; n < 2; ++n) _Pragma("unroll") for (int k = 0; k < 2; ++k) \
;         acc[ai][bj][m][n] = __builtin_amdgcn_mfma_f32_16x16x32_bf16(Bt[n][k], At[m][k], acc[ai][bj][m][n], 0, 0, 0); __builtin_amdgcn_s_setprio(0); } while (0)
; #define PG8_WAIT_V(n) asm volatile("s_waitcnt vmcnt(" #n ")" ::: "memory")
; #define PG8_WAIT_L(n) asm volatile("s_waitcnt lgkmcnt(" #n ")" ::: "memory")
; #define PG8_BAR __builtin_amdgcn_s_barrier()
; #define PG8_SCHED __builtin_amdgcn_sched_barrier(0)
; #define PG8_STAGE(bufoff, gbase, voff) do { _Pragma("unroll") for (int _i = 0; _i < 2; ++_i) \
;         __builtin_amdgcn_global_load_lds((const unsigned*)((const char*)(gbase) + (voff)[_i]), (PG8_LAS unsigned*)(lds + (bufoff) + ldsw + _i * 8192), 16, 0, 0); } while (0)
; #define PG8_LDA(dst, b, h) do { _Pragma("unroll") for (int mb = 0; mb < 2; ++mb) _Pragma("unroll") for (int s = 0; s < 2; ++s) \
;         dst[mb][s] = cat8(*(const PG8_LAS bf16x8*)(lds + PG8_SA(b, h) + aoffk[s][0] + mb * 4096), *(const PG8_LAS bf16x8*)(lds + PG8_SA(b, h) + aoffk[s][1] + mb * 4096)); } while (0)
; #define PG8_WAIT_V(n) asm volatile("s_waitcnt vmcnt(" #n ")" ::: "memory")
; #define PG8_BAR __builtin_amdgcn_s_barrier()
; template <class Epi, class Sched, bool ALIGN_EPI = false, bool SP2 = false>
; __device__ __forceinline__ void gemm_phase(PG8_LAS unsigned char* lds, const Gemm g, const Sched& S, const Epi& E, const int tid) {
;     ...
;             PG8_LDA(At, 1, 1); PG8_STAGE(PG8_SB(1, 0), b3, voffB); PG8_STAGE(PG8_SB(1, 1), b3 + hstep, voffB); PG8_STAGE(PG8_SA(1, 0), a3, voffA);
;             PG8_WAIT_V(8); PG8_WAIT_L(0); PG8_BAR; PG8_MMA(1, 0, At, B0); PG8_MMA(1, 1, At, B1); PG8_BAR; PG8_SCHED;
;     ...
;         if constexpr (ALIGN_EPI) { if (wr == 0) PG8_BAR; }
	s_add_i32 s26, s26, s64
	v_lshl_add_u64 v[132:133], v[132:133], 0, s[34:35]
	s_mov_b32 m0, s26
	ds_read_b128 v[206:209], v170 offset:49152
	ds_read_b128 v[210:213], v170 offset:50176
	ds_read_b128 v[214:217], v170 offset:51200
	ds_read_b128 v[218:221], v170 offset:52224
	ds_read_b128 v[222:225], v170 offset:53248
	ds_read_b128 v[226:229], v170 offset:54272
	ds_read_b128 v[244:247], v170 offset:55296
	ds_read_b128 v[248:251], v170 offset:56320
	global_load_lds_dwordx4 v[132:133], off
	s_add_i32 m0, s26, 0x2000
	s_add_u32 s6, s6, 0x80080
	v_lshl_add_u64 v[132:133], v[152:153], 0, s[34:35]
	s_addc_u32 s7, s7, 0
	s_add_i32 s26, s31, s64
	global_load_lds_dwordx4 v[132:133], off
	v_lshl_add_u64 v[132:133], s[6:7], 0, v[136:137]
	s_mov_b32 m0, s26
	s_nop 0
	global_load_lds_dwordx4 v[132:133], off
	v_lshl_add_u64 v[132:133], s[6:7], 0, v[140:141]
	s_add_i32 m0, s26, 0x2000
	s_nop 0
	global_load_lds_dwordx4 v[132:133], off
	v_lshl_add_u64 v[132:133], v[230:231], 0, s[34:35]
	s_mov_b32 m0, s72
	s_nop 0
	global_load_lds_dwordx4 v[132:133], off
	v_lshl_add_u64 v[132:133], v[242:243], 0, s[34:35]
	s_mov_b32 m0, s73
	s_nop 0
	global_load_lds_dwordx4 v[132:133], off
	s_waitcnt vmcnt(8)
	s_waitcnt lgkmcnt(0)
	s_barrier
	s_waitcnt lgkmcnt(0)
	v_mfma_f32_16x16x32_bf16 v[58:61], v[172:175], v[206:209], v[58:61]
	v_mfma_f32_16x16x32_bf16 v[50:53], v[180:183], v[206:209], v[50:53]
	v_mfma_f32_16x16x32_bf16 v[42:45], v[172:175], v[214:217], v[42:45]
	v_mfma_f32_16x16x32_bf16 v[34:37], v[180:183], v[214:217], v[34:37]
	v_mfma_f32_16x16x32_bf16 v[26:29], v[172:175], v[222:225], v[26:29]
	v_mfma_f32_16x16x32_bf16 v[18:21], v[180:183], v[222:225], v[18:21]
	v_mfma_f32_16x16x32_bf16 v[10:13], v[172:175], v[244:247], v[10:13]
	v_mfma_f32_16x16x32_bf16 v[2:5], v[180:183], v[244:247], v[2:5]
	v_mfma_f32_16x16x32_bf16 v[58:61], v[176:179], v[210:213], v[58:61]
	v_mfma_f32_16x16x32_bf16 v[50:53], v[184:187], v[210:213], v[50:53]
	v_mfma_f32_16x16x32_bf16 v[42:45], v[176:179], v[218:221], v[42:45]
	v_mfma_f32_16x16x32_bf16 v[34:37], v[184:187], v[218:221], v[34:37]
	v_mfma_f32_16x16x32_bf16 v[26:29], v[176:179], v[226:229], v[26:29]
	v_mfma_f32_16x16x32_bf16 v[18:21], v[184:187], v[226:229], v[18:21]
	v_mfma_f32_16x16x32_bf16 v[10:13], v[176:179], v[248:251], v[10:13]
	v_mfma_f32_16x16x32_bf16 v[2:5], v[184:187], v[248:251], v[2:5]
	v_mfma_f32_16x16x32_bf16 v[62:65], v[188:191], v[206:209], v[62:65]
	v_mfma_f32_16x16x32_bf16 v[54:57], v[198:201], v[206:209], v[54:57]
	v_mfma_f32_16x16x32_bf16 v[46:49], v[188:191], v[214:217], v[46:49]
	v_mfma_f32_16x16x32_bf16 v[38:41], v[198:201], v[214:217], v[38:41]
	v_mfma_f32_16x16x32_bf16 v[30:33], v[188:191], v[222:225], v[30:33]
	v_mfma_f32_16x16x32_bf16 v[22:25], v[198:201], v[222:225], v[22:25]
	v_mfma_f32_16x16x32_bf16 v[14:17], v[188:191], v[244:247], v[14:17]
	v_mfma_f32_16x16x32_bf16 v[6:9], v[198:201], v[244:247], v[6:9]
	v_mfma_f32_16x16x32_bf16 v[62:65], v[192:195], v[210:213], v[62:65]
	v_mfma_f32_16x16x32_bf16 v[54:57], v[202:205], v[210:213], v[54:57]
	v_mfma_f32_16x16x32_bf16 v[46:49], v[192:195], v[218:221], v[46:49]
	v_mfma_f32_16x16x32_bf16 v[38:41], v[202:205], v[218:221], v[38:41]
	v_mfma_f32_16x16x32_bf16 v[30:33], v[192:195], v[226:229], v[30:33]
	v_mfma_f32_16x16x32_bf16 v[22:25], v[202:205], v[226:229], v[22:25]
	v_mfma_f32_16x16x32_bf16 v[14:17], v[192:195], v[248:251], v[14:17]
	v_mfma_f32_16x16x32_bf16 v[6:9], v[202:205], v[248:251], v[6:9]
	s_barrier
	s_add_i32 s24, s24, 2
	s_add_u32 s54, s54, 0x100
	s_addc_u32 s55, s55, 0
	s_add_u32 s18, s18, 0x100
	s_addc_u32 s19, s19, 0
	s_cmp_gt_u32 s24, 29
	s_cbranch_scc0 .LBB0_2282
	s_setprio 0
	s_and_b64 vcc, exec, s[10:11]
	s_cbranch_vccz .LBB0_2285
	s_barrier

; #define PG8_STAGE(bufoff, gbase, voff) do { _Pragma("unroll") for (int _i = 0; _i < 2; ++_i) \
;         __builtin_amdgcn_global_load_lds((const unsigned*)((const char*)(gbase) + (voff)[_i]), (PG8_LAS unsigned*)(lds + (bufoff) + ldsw + _i * 8192), 16, 0, 0); } while (0)
; #define PG8_LDA(dst, b, h) do { _Pragma("unroll") for (int m = 0; m < 4; ++m) _Pragma("unroll") for (int k = 0; k < 2; ++k) dst[m][k] = *(const PG8_LAS bf16x8*)(lds + PG8_SA(b, h) + aoff + m * 2048 + k * 1024); } while (0)
; #define PG8_LDB(dst, b, h) do { _Pragma("unroll") for (int n = 0; n < 2; ++n) _Pragma("unroll") for (int k = 0; k < 2; ++k) dst[n][k] = *(const PG8_LAS bf16x8*)(lds + PG8_SB(b, h) + boff + n * 2048 + k * 1024); } while (0)
; #define PG8_WAIT_V(n) asm volatile("s_waitcnt vmcnt(" #n ")" ::: "memory")
; #define PG8_WAIT_L(n) asm volatile("s_waitcnt lgkmcnt(" #n ")" ::: "memory")
; #define PG8_BAR __builtin_amdgcn_s_barrier()
; #define PG8_SCHED __builtin_amdgcn_sched_barrier(0)
; template <class Epi, class Sched, bool ALIGN_EPI = false, bool SP2 = false>
; __device__ __forceinline__ void gemm_phase(PG8_LAS unsigned char* lds, const Gemm g, const Sched& S, const Epi& E, const int tid) {
;     ...
;         for (int t = 0; t < nt; t += 2) {
;             const bool last = (t == nt - 2);
;             const char* a1 = cA + (size_t)(t + 1) * kstep;
;             const char* a2 = last ? nA : cA + (size_t)(t + 2) * kstep; const char* b2 = last ? nB : cB + (size_t)(t + 2) * kstep;
;             const char* a3 = a2 + kstep; const char* b3 = b2 + kstep;
;             if (last && has_next) S.a_ready(nxt);
;             if constexpr (SP2) {
;             PG8_LDB(B0, 0, 0); PG8_LDB(B1, 0, 1); PG8_SCHED; PG8_LDA(At, 0, 0); PG8_STAGE(PG8_SA(1, 1), a1 + hstep, voffA);
;             PG8_WAIT_V(8); PG8_WAIT_L(0); PG8_BAR; PG8_MMA(0, 0, At, B0); PG8_MMA(0, 1, At, B1); PG8_BAR; PG8_SCHED;
;             PG8_LDA(At, 0, 1); PG8_STAGE(PG8_SB(0, 0), b2, voffB); PG8_STAGE(PG8_SB(0, 1), b2 + hstep, voffB); PG8_STAGE(PG8_SA(0, 0), a2, voffA);
;     ...
; #pragma unroll
;         for (int a = 0; a < 2; ++a)
; #pragma unroll
;             for (int b = 0; b < 2; ++b)
; #pragma unroll
;                 for (int m = 0; m < 4; ++m)
; #pragma unroll
;                     for (int n = 0; n < 2; ++n) acc[a][b][m][n] = (f32x4){0.f, 0.f, 0.f, 0.f};
;         cur = nxt; cA = nA; cB = nB; ++ui; nt = cur.nt;
.LBB0_2524:
	s_add_i32 s12, s2, -2
	s_add_u32 s13, s6, 0x100
	v_mov_b32_e32 v2, 0
	s_addc_u32 s15, s7, 0
	s_mov_b32 s18, 0
	v_mov_b32_e32 v3, v2
	v_mov_b32_e32 v4, v2
	v_mov_b32_e32 v5, v2
	v_mov_b32_e32 v6, v2
	v_mov_b32_e32 v7, v2
	v_mov_b32_e32 v8, v2
	v_mov_b32_e32 v9, v2
	v_mov_b32_e32 v14, v2
	v_mov_b32_e32 v15, v2
	v_mov_b32_e32 v16, v2
	v_mov_b32_e32 v17, v2
	v_mov_b32_e32 v22, v2
	v_mov_b32_e32 v23, v2
	v_mov_b32_e32 v24, v2
	v_mov_b32_e32 v25, v2
	v_mov_b32_e32 v30, v2
	v_mov_b32_e32 v31, v2
	v_mov_b32_e32 v32, v2
	v_mov_b32_e32 v33, v2
	v_mov_b32_e32 v38, v2
	v_mov_b32_e32 v39, v2
	v_mov_b32_e32 v40, v2
	v_mov_b32_e32 v41, v2
	v_mov_b32_e32 v46, v2
	v_mov_b32_e32 v47, v2
	v_mov_b32_e32 v48, v2
	v_mov_b32_e32 v49, v2
	v_mov_b32_e32 v54, v2
	v_mov_b32_e32 v55, v2
	v_mov_b32_e32 v56, v2
	v_mov_b32_e32 v57, v2
	v_mov_b32_e32 v10, v2
	v_mov_b32_e32 v11, v2
	v_mov_b32_e32 v12, v2
	v_mov_b32_e32 v13, v2
	v_mov_b32_e32 v18, v2
	v_mov_b32_e32 v19, v2
	v_mov_b32_e32 v20, v2
	v_mov_b32_e32 v21, v2
	v_mov_b32_e32 v26, v2
	v_mov_b32_e32 v27, v2
	v_mov_b32_e32 v28, v2
	v_mov_b32_e32 v29, v2
	v_mov_b32_e32 v34, v2
	v_mov_b32_e32 v35, v2
	v_mov_b32_e32 v36, v2
	v_mov_b32_e32 v37, v2
	v_mov_b32_e32 v42, v2
	v_mov_b32_e32 v43, v2
	v_mov_b32_e32 v44, v2
	v_mov_b32_e32 v45, v2
	v_mov_b32_e32 v50, v2
	v_mov_b32_e32 v51, v2
	v_mov_b32_e32 v52, v2
	v_mov_b32_e32 v53, v2
	v_mov_b32_e32 v58, v2
	v_mov_b32_e32 v59, v2
	v_mov_b32_e32 v60, v2
	v_mov_b32_e32 v61, v2
	v_mov_b32_e32 v62, v2
	v_mov_b32_e32 v63, v2
	v_mov_b32_e32 v64, v2
	v_mov_b32_e32 v65, v2
	v_mov_b32_e32 v66, v2
	v_mov_b32_e32 v67, v2
	v_mov_b32_e32 v68, v2
	v_mov_b32_e32 v69, v2
	v_mov_b32_e32 v70, v2
	v_mov_b32_e32 v71, v2
	v_mov_b32_e32 v72, v2
	v_mov_b32_e32 v73, v2
	v_mov_b32_e32 v78, v2
	v_mov_b32_e32 v79, v2
	v_mov_b32_e32 v80, v2
	v_mov_b32_e32 v81, v2
	v_mov_b32_e32 v86, v2
	v_mov_b32_e32 v87, v2
	v_mov_b32_e32 v88, v2
	v_mov_b32_e32 v89, v2
	v_mov_b32_e32 v94, v2
	v_mov_b32_e32 v95, v2
	v_mov_b32_e32 v96, v2
	v_mov_b32_e32 v97, v2
	v_mov_b32_e32 v102, v2
	v_mov_b32_e32 v103, v2
	v_mov_b32_e32 v104, v2
	v_mov_b32_e32 v105, v2
	v_mov_b32_e32 v110, v2
	v_mov_b32_e32 v111, v2
	v_mov_b32_e32 v112, v2
	v_mov_b32_e32 v113, v2
	v_mov_b32_e32 v118, v2
	v_mov_b32_e32 v119, v2
	v_mov_b32_e32 v120, v2
	v_mov_b32_e32 v121, v2
	v_mov_b32_e32 v74, v2
	v_mov_b32_e32 v75, v2
	v_mov_b32_e32 v76, v2
	v_mov_b32_e32 v77, v2
	v_mov_b32_e32 v82, v2
	v_mov_b32_e32 v83, v2
	v_mov_b32_e32 v84, v2
	v_mov_b32_e32 v85, v2
	v_mov_b32_e32 v90, v2
	v_mov_b32_e32 v91, v2
	v_mov_b32_e32 v92, v2
	v_mov_b32_e32 v93, v2
	v_mov_b32_e32 v98, v2
	v_mov_b32_e32 v99, v2
	v_mov_b32_e32 v100, v2
	v_mov_b32_e32 v101, v2
	v_mov_b32_e32 v106, v2
	v_mov_b32_e32 v107, v2
	v_mov_b32_e32 v108, v2
	v_mov_b32_e32 v109, v2
	v_mov_b32_e32 v114, v2
	v_mov_b32_e32 v115, v2
	v_mov_b32_e32 v116, v2
	v_mov_b32_e32 v117, v2
	v_mov_b32_e32 v122, v2
	v_mov_b32_e32 v123, v2
	v_mov_b32_e32 v124, v2
	v_mov_b32_e32 v125, v2
	v_mov_b32_e32 v126, v2
	v_mov_b32_e32 v127, v2
	v_mov_b32_e32 v128, v2
	v_mov_b32_e32 v129, v2
	s_cmp_eq_u64 s[10:11], 0
	s_cbranch_scc0 .Lsp_skip_2525
	s_setprio 1
.Lsp_skip_2525:
.LBB0_2525:
	s_add_i32 s19, s18, 2
	s_add_u32 s6, s22, 0x100
	s_addc_u32 s7, s23, 0
	s_add_i32 s26, 0, 0x10000
	s_cmp_eq_u32 s12, s18
	s_cselect_b32 s31, s17, s7
	s_cselect_b32 s30, s16, s6
	s_cselect_b32 s29, s21, s15
	s_cselect_b32 s28, s20, s13
	s_add_i32 s18, 0, 0x14000
	v_add_u32_e32 v144, s26, v162
	v_add_u32_e32 v160, s18, v162
	ds_read_b128 v[132:135], v144
	ds_read_b128 v[136:139], v144 offset:1024
	ds_read_b128 v[140:143], v144 offset:2048
	ds_read_b128 v[144:147], v144 offset:3072
	ds_read_b128 v[172:175], v160
	ds_read_b128 v[176:179], v160 offset:1024
	ds_read_b128 v[180:183], v160 offset:2048
	ds_read_b128 v[184:187], v160 offset:3072
	v_lshl_add_u64 v[160:161], s[22:23], 0, v[156:157]
	s_add_i32 m0, s44, 0xc000
	ds_read_b128 v[188:191], v171
	ds_read_b128 v[192:195], v171 offset:1024
	ds_read_b128 v[198:201], v171 offset:2048
	ds_read_b128 v[202:205], v171 offset:3072
	ds_read_b128 v[206:209], v171 offset:4096
	ds_read_b128 v[210:213], v171 offset:5120
	ds_read_b128 v[214:217], v171 offset:6144
	ds_read_b128 v[218:221], v171 offset:7168
	global_load_lds_dwordx4 v[160:161], off
	v_lshl_add_u64 v[160:161], s[22:23], 0, v[158:159]
	s_add_i32 m0, s44, 0xe000
	s_nop 0
	global_load_lds_dwordx4 v[160:161], off
	s_waitcnt vmcnt(8)
	s_waitcnt lgkmcnt(0)
	s_barrier
	s_waitcnt lgkmcnt(0)
	v_mfma_f32_16x16x32_bf16 v[126:129], v[132:135], v[188:191], v[126:129]
	v_mfma_f32_16x16x32_bf16 v[122:125], v[140:143], v[188:191], v[122:125]
	v_mfma_f32_16x16x32_bf16 v[114:117], v[132:135], v[198:201], v[114:117]
	v_mfma_f32_16x16x32_bf16 v[106:109], v[140:143], v[198:201], v[106:109]
	v_mfma_f32_16x16x32_bf16 v[98:101], v[132:135], v[206:209], v[98:101]
	v_mfma_f32_16x16x32_bf16 v[90:93], v[140:143], v[206:209], v[90:93]
	v_mfma_f32_16x16x32_bf16 v[82:85], v[132:135], v[214:217], v[82:85]
	v_mfma_f32_16x16x32_bf16 v[74:77], v[140:143], v[214:217], v[74:77]
	v_mfma_f32_16x16x32_bf16 v[126:129], v[136:139], v[192:195], v[126:129]
	v_mfma_f32_16x16x32_bf16 v[122:125], v[144:147], v[192:195], v[122:125]
	v_mfma_f32_16x16x32_bf16 v[114:117], v[136:139], v[202:205], v[114:117]
	v_mfma_f32_16x16x32_bf16 v[106:109], v[144:147], v[202:205], v[106:109]
	v_mfma_f32_16x16x32_bf16 v[98:101], v[136:139], v[210:213], v[98:101]
	v_mfma_f32_16x16x32_bf16 v[90:93], v[144:147], v[210:213], v[90:93]
	v_mfma_f32_16x16x32_bf16 v[82:85], v[136:139], v[218:221], v[82:85]
	v_mfma_f32_16x16x32_bf16 v[74:77], v[144:147], v[218:221], v[74:77]
	v_mfma_f32_16x16x32_bf16 v[118:121], v[172:175], v[188:191], v[118:121]
	v_mfma_f32_16x16x32_bf16 v[110:113], v[180:183], v[188:191], v[110:113]
	v_mfma_f32_16x16x32_bf16 v[102:105], v[172:175], v[198:201], v[102:105]
	v_mfma_f32_16x16x32_bf16 v[94:97], v[180:183], v[198:201], v[94:97]
	v_mfma_f32_16x16x32_bf16 v[86:89], v[172:175], v[206:209], v[86:89]
	v_mfma_f32_16x16x32_bf16 v[78:81], v[180:183], v[206:209], v[78:81]
	v_mfma_f32_16x16x32_bf16 v[70:73], v[172:175], v[214:217], v[70:73]
	v_mfma_f32_16x16x32_bf16 v[66:69], v[180:183], v[214:217], v[66:69]
	v_mfma_f32_16x16x32_bf16 v[118:121], v[176:179], v[192:195], v[118:121]
	v_mfma_f32_16x16x32_bf16 v[110:113], v[184:187], v[192:195], v[110:113]
	v_mfma_f32_16x16x32_bf16 v[102:105], v[176:179], v[202:205], v[102:105]
	v_mfma_f32_16x16x32_bf16 v[94:97], v[184:187], v[202:205], v[94:97]
	v_mfma_f32_16x16x32_bf16 v[86:89], v[176:179], v[210:213], v[86:89]
	v_mfma_f32_16x16x32_bf16 v[78:81], v[184:187], v[210:213], v[78:81]
	v_mfma_f32_16x16x32_bf16 v[70:73], v[176:179], v[218:221], v[70:73]
	v_mfma_f32_16x16x32_bf16 v[66:69], v[184:187], v[218:221], v[66:69]
	s_barrier
; #define PG8_STAGE(bufoff, gbase, voff) do { _Pragma("unroll") for (int _i = 0; _i < 2; ++_i) \
;         __builtin_amdgcn_global_load_lds((const unsigned*)((const char*)(gbase) + (voff)[_i]), (PG8_LAS unsigned*)(lds + (bufoff) + ldsw + _i * 8192), 16, 0, 0); } while (0)
; #define PG8_LDA(dst, b, h) do { _Pragma("unroll") for (int m = 0; m < 4; ++m) _Pragma("unroll") for (int k = 0; k < 2; ++k) dst[m][k] = *(const PG8_LAS bf16x8*)(lds + PG8_SA(b, h) + aoff + m * 2048 + k * 1024); } while (0)
; #define PG8_LDB(dst, b, h) do { _Pragma("unroll") for (int n = 0; n < 2; ++n) _Pragma("unroll") for (int k = 0; k < 2; ++k) dst[n][k] = *(const PG8_LAS bf16x8*)(lds + PG8_SB(b, h) + boff + n * 2048 + k * 1024); } while (0)
; #define PG8_MMA(ai, bj, At, Bt) do { __builtin_amdgcn_s_setprio(1); _Pragma("unroll") for (int m = 0; m < 4; ++m) _Pragma("unroll") for (int n = 0; n < 2; ++n) _Pragma("unroll") for (int k = 0; k < 2; ++k) \
;         acc[ai][bj][m][n] = __builtin_amdgcn_mfma_f32_16x16x32_bf16(Bt[n][k], At[m][k], acc[ai][bj][m][n], 0, 0, 0); __builtin_amdgcn_s_setprio(0); } while (0)
; #define PG8_WAIT_V(n) asm volatile("s_waitcnt vmcnt(" #n ")" ::: "memory")
; #define PG8_WAIT_L(n) asm volatile("s_waitcnt lgkmcnt(" #n ")" ::: "memory")
; #define PG8_BAR __builtin_amdgcn_s_barrier()
; #define PG8_SCHED __builtin_amdgcn_sched_barrier(0)
; #define PG8_STAGE(bufoff, gbase, voff) do { _Pragma("unroll") for (int _i = 0; _i < 2; ++_i) \
;         __builtin_amdgcn_global_load_lds((const unsigned*)((const char*)(gbase) + (voff)[_i]), (PG8_LAS unsigned*)(lds + (bufoff) + ldsw + _i * 8192), 16, 0, 0); } while (0)
; #define PG8_WAIT_V(n) asm volatile("s_waitcnt vmcnt(" #n ")" ::: "memory")
; #define PG8_WAIT_L(n) asm volatile("s_waitcnt lgkmcnt(" #n ")" ::: "memory")
; template <class Epi, class Sched, bool ALIGN_EPI = false, bool SP2 = false>
; __device__ __forceinline__ void gemm_phase(PG8_LAS unsigned char* lds, const Gemm g, const Sched& S, const Epi& E, const int tid) {
;     ...
;             PG8_WAIT_V(8); PG8_WAIT_L(0); PG8_BAR; PG8_MMA(1, 0, At, B0); PG8_MMA(1, 1, At, B1); PG8_BAR; PG8_SCHED;
;             PG8_LDB(B0, 1, 0); PG8_LDB(B1, 1, 1); PG8_SCHED; PG8_LDA(At, 1, 0); PG8_STAGE(PG8_SA(0, 1), a2 + hstep, voffA);
;             PG8_WAIT_V(8); PG8_WAIT_L(0); PG8_BAR; PG8_MMA(0, 0, At, B0); PG8_MMA(0, 1, At, B1); PG8_BAR; PG8_SCHED;
	s_add_i32 s22, s26, s43
	v_lshl_add_u64 v[160:161], s[28:29], 0, v[150:151]
	s_mov_b32 m0, s22
	ds_read_b128 v[188:191], v171 offset:16384
	ds_read_b128 v[192:195], v171 offset:17408
	ds_read_b128 v[198:201], v171 offset:18432
	ds_read_b128 v[202:205], v171 offset:19456
	ds_read_b128 v[206:209], v171 offset:20480
	ds_read_b128 v[210:213], v171 offset:21504
	ds_read_b128 v[214:217], v171 offset:22528
	ds_read_b128 v[218:221], v171 offset:23552
	global_load_lds_dwordx4 v[160:161], off
	s_add_i32 m0, s22, 0x2000
	s_add_u32 s22, s28, 0x160000
	v_lshl_add_u64 v[222:223], s[28:29], 0, v[154:155]
	s_addc_u32 s23, s29, 0
	s_add_i32 s18, s18, s43
	global_load_lds_dwordx4 v[222:223], off
	v_lshl_add_u64 v[224:225], s[22:23], 0, v[150:151]
	s_mov_b32 m0, s18
	v_lshl_add_u64 v[226:227], s[30:31], 0, v[152:153]
	global_load_lds_dwordx4 v[224:225], off
	v_lshl_add_u64 v[224:225], s[22:23], 0, v[154:155]
	s_add_i32 m0, s18, 0x2000
	s_nop 0
	global_load_lds_dwordx4 v[224:225], off
	v_lshl_add_u64 v[224:225], s[30:31], 0, v[148:149]
	s_mov_b32 m0, s44
	s_nop 0
	global_load_lds_dwordx4 v[224:225], off
	s_mov_b32 m0, s45
	s_nop 0
	global_load_lds_dwordx4 v[226:227], off
	s_waitcnt vmcnt(8)
	s_waitcnt lgkmcnt(0)
	s_barrier
	s_waitcnt lgkmcnt(0)
	v_mfma_f32_16x16x32_bf16 v[62:65], v[132:135], v[188:191], v[62:65]
	v_mfma_f32_16x16x32_bf16 v[58:61], v[140:143], v[188:191], v[58:61]
	v_mfma_f32_16x16x32_bf16 v[50:53], v[132:135], v[198:201], v[50:53]
	v_mfma_f32_16x16x32_bf16 v[42:45], v[140:143], v[198:201], v[42:45]
	v_mfma_f32_16x16x32_bf16 v[34:37], v[132:135], v[206:209], v[34:37]
	v_mfma_f32_16x16x32_bf16 v[26:29], v[140:143], v[206:209], v[26:29]
	v_mfma_f32_16x16x32_bf16 v[18:21], v[132:135], v[214:217], v[18:21]
	v_mfma_f32_16x16x32_bf16 v[10:13], v[140:143], v[214:217], v[10:13]
	v_mfma_f32_16x16x32_bf16 v[62:65], v[136:139], v[192:195], v[62:65]
	v_mfma_f32_16x16x32_bf16 v[58:61], v[144:147], v[192:195], v[58:61]
	v_mfma_f32_16x16x32_bf16 v[50:53], v[136:139], v[202:205], v[50:53]
	v_mfma_f32_16x16x32_bf16 v[42:45], v[144:147], v[202:205], v[42:45]
	v_mfma_f32_16x16x32_bf16 v[34:37], v[136:139], v[210:213], v[34:37]
	v_mfma_f32_16x16x32_bf16 v[26:29], v[144:147], v[210:213], v[26:29]
	v_mfma_f32_16x16x32_bf16 v[18:21], v[136:139], v[218:221], v[18:21]
	v_mfma_f32_16x16x32_bf16 v[10:13], v[144:147], v[218:221], v[10:13]
	v_mfma_f32_16x16x32_bf16 v[54:57], v[172:175], v[188:191], v[54:57]
	v_mfma_f32_16x16x32_bf16 v[46:49], v[180:183], v[188:191], v[46:49]
	v_mfma_f32_16x16x32_bf16 v[38:41], v[172:175], v[198:201], v[38:41]
	v_mfma_f32_16x16x32_bf16 v[30:33], v[180:183], v[198:201], v[30:33]
	v_mfma_f32_16x16x32_bf16 v[22:25], v[172:175], v[206:209], v[22:25]
	v_mfma_f32_16x16x32_bf16 v[14:17], v[180:183], v[206:209], v[14:17]
	v_mfma_f32_16x16x32_bf16 v[6:9], v[172:175], v[214:217], v[6:9]
	v_mfma_f32_16x16x32_bf16 v[2:5], v[180:183], v[214:217], v[2:5]
	v_mfma_f32_16x16x32_bf16 v[54:57], v[176:179], v[192:195], v[54:57]
	v_mfma_f32_16x16x32_bf16 v[46:49], v[184:187], v[192:195], v[46:49]
	v_mfma_f32_16x16x32_bf16 v[38:41], v[176:179], v[202:205], v[38:41]
	v_mfma_f32_16x16x32_bf16 v[30:33], v[184:187], v[202:205], v[30:33]
	v_mfma_f32_16x16x32_bf16 v[22:25], v[176:179], v[210:213], v[22:25]
	v_mfma_f32_16x16x32_bf16 v[14:17], v[184:187], v[210:213], v[14:17]
	v_mfma_f32_16x16x32_bf16 v[6:9], v[176:179], v[218:221], v[6:9]
	v_mfma_f32_16x16x32_bf16 v[2:5], v[184:187], v[218:221], v[2:5]
	s_barrier
	s_add_i32 s18, 0, 0x18000
	s_add_i32 s26, 0, 0x1c000
	v_add_u32_e32 v144, s18, v162
	v_add_u32_e32 v184, s26, v162
	ds_read_b128 v[132:135], v144
	ds_read_b128 v[136:139], v144 offset:1024
	ds_read_b128 v[140:143], v144 offset:2048
	ds_read_b128 v[144:147], v144 offset:3072
	ds_read_b128 v[172:175], v184
	ds_read_b128 v[176:179], v184 offset:1024
	ds_read_b128 v[180:183], v184 offset:2048
	ds_read_b128 v[184:187], v184 offset:3072
	s_add_u32 s22, s30, 0x160000
	s_addc_u32 s23, s31, 0
	s_mov_b32 m0, s46
	v_lshl_add_u64 v[228:229], s[22:23], 0, v[148:149]
	ds_read_b128 v[188:191], v171 offset:32768
	ds_read_b128 v[192:195], v171 offset:33792
	ds_read_b128 v[198:201], v171 offset:34816
	ds_read_b128 v[202:205], v171 offset:35840
	ds_read_b128 v[206:209], v171 offset:36864
	ds_read_b128 v[210:213], v171 offset:37888
	ds_read_b128 v[214:217], v171 offset:38912
	ds_read_b128 v[218:221], v171 offset:39936
	global_load_lds_dwordx4 v[228:229], off
	v_lshl_add_u64 v[228:229], s[22:23], 0, v[152:153]
	s_mov_b32 m0, s47
	s_nop 0
	global_load_lds_dwordx4 v[228:229], off
	s_waitcnt vmcnt(8)
	s_waitcnt lgkmcnt(0)
	s_barrier
; #define PG8_STAGE(bufoff, gbase, voff) do { _Pragma("unroll") for (int _i = 0; _i < 2; ++_i) \
;         __builtin_amdgcn_global_load_lds((const unsigned*)((const char*)(gbase) + (voff)[_i]), (PG8_LAS unsigned*)(lds + (bufoff) + ldsw + _i * 8192), 16, 0, 0); } while (0)
; #define PG8_LDA(dst, b, h) do { _Pragma("unroll") for (int m = 0; m < 4; ++m) _Pragma("unroll") for (int k = 0; k < 2; ++k) dst[m][k] = *(const PG8_LAS bf16x8*)(lds + PG8_SA(b, h) + aoff + m * 2048 + k * 1024); } while (0)
; #define PG8_MMA(ai, bj, At, Bt) do { __builtin_amdgcn_s_setprio(1); _Pragma("unroll") for (int m = 0; m < 4; ++m) _Pragma("unroll") for (int n = 0; n < 2; ++n) _Pragma("unroll") for (int k = 0; k < 2; ++k) \
;         acc[ai][bj][m][n] = __builtin_amdgcn_mfma_f32_16x16x32_bf16(Bt[n][k], At[m][k], acc[ai][bj][m][n], 0, 0, 0); __builtin_amdgcn_s_setprio(0); } while (0)
; #define PG8_WAIT_V(n) asm volatile("s_waitcnt vmcnt(" #n ")" ::: "memory")
; #define PG8_WAIT_L(n) asm volatile("s_waitcnt lgkmcnt(" #n ")" ::: "memory")
; #define PG8_BAR __builtin_amdgcn_s_barrier()
; #define PG8_SCHED __builtin_amdgcn_sched_barrier(0)
; #define PG8_STAGE(bufoff, gbase, voff) do { _Pragma("unroll") for (int _i = 0; _i < 2; ++_i) \
;         __builtin_amdgcn_global_load_lds((const unsigned*)((const char*)(gbase) + (voff)[_i]), (PG8_LAS unsigned*)(lds + (bufoff) + ldsw + _i * 8192), 16, 0, 0); } while (0)
; #define PG8_LDA(dst, b, h) do { _Pragma("unroll") for (int mb = 0; mb < 2; ++mb) _Pragma("unroll") for (int s = 0; s < 2; ++s) \
;         dst[mb][s] = cat8(*(const PG8_LAS bf16x8*)(lds + PG8_SA(b, h) + aoffk[s][0] + mb * 4096), *(const PG8_LAS bf16x8*)(lds + PG8_SA(b, h) + aoffk[s][1] + mb * 4096)); } while (0)
; template <class Epi, class Sched, bool ALIGN_EPI = false, bool SP2 = false>
; __device__ __forceinline__ void gemm_phase(PG8_LAS unsigned char* lds, const Gemm g, const Sched& S, const Epi& E, const int tid) {
;     ...
;             PG8_WAIT_V(8); PG8_WAIT_L(0); PG8_BAR; PG8_MMA(0, 0, At, B0); PG8_MMA(0, 1, At, B1); PG8_BAR; PG8_SCHED;
;             PG8_LDA(At, 1, 1); PG8_STAGE(PG8_SB(1, 0), b3, voffB); PG8_STAGE(PG8_SB(1, 1), b3 + hstep, voffB); PG8_STAGE(PG8_SA(1, 0), a3, voffA);
;             PG8_WAIT_V(8); PG8_WAIT_L(0); PG8_BAR; PG8_MMA(1, 0, At, B0); PG8_MMA(1, 1, At, B1); PG8_BAR; PG8_SCHED;
;     ...
;         if constexpr (ALIGN_EPI) { if (wr == 0) PG8_BAR; }
	s_waitcnt lgkmcnt(0)
	v_mfma_f32_16x16x32_bf16 v[126:129], v[132:135], v[188:191], v[126:129]
	v_mfma_f32_16x16x32_bf16 v[122:125], v[140:143], v[188:191], v[122:125]
	v_mfma_f32_16x16x32_bf16 v[114:117], v[132:135], v[198:201], v[114:117]
	v_mfma_f32_16x16x32_bf16 v[106:109], v[140:143], v[198:201], v[106:109]
	v_mfma_f32_16x16x32_bf16 v[98:101], v[132:135], v[206:209], v[98:101]
	v_mfma_f32_16x16x32_bf16 v[90:93], v[140:143], v[206:209], v[90:93]
	v_mfma_f32_16x16x32_bf16 v[82:85], v[132:135], v[214:217], v[82:85]
	v_mfma_f32_16x16x32_bf16 v[74:77], v[140:143], v[214:217], v[74:77]
	v_mfma_f32_16x16x32_bf16 v[126:129], v[136:139], v[192:195], v[126:129]
	v_mfma_f32_16x16x32_bf16 v[122:125], v[144:147], v[192:195], v[122:125]
	v_mfma_f32_16x16x32_bf16 v[114:117], v[136:139], v[202:205], v[114:117]
	v_mfma_f32_16x16x32_bf16 v[106:109], v[144:147], v[202:205], v[106:109]
	v_mfma_f32_16x16x32_bf16 v[98:101], v[136:139], v[210:213], v[98:101]
	v_mfma_f32_16x16x32_bf16 v[90:93], v[144:147], v[210:213], v[90:93]
	v_mfma_f32_16x16x32_bf16 v[82:85], v[136:139], v[218:221], v[82:85]
	v_mfma_f32_16x16x32_bf16 v[74:77], v[144:147], v[218:221], v[74:77]
	v_mfma_f32_16x16x32_bf16 v[118:121], v[172:175], v[188:191], v[118:121]
	v_mfma_f32_16x16x32_bf16 v[110:113], v[180:183], v[188:191], v[110:113]
	v_mfma_f32_16x16x32_bf16 v[102:105], v[172:175], v[198:201], v[102:105]
	v_mfma_f32_16x16x32_bf16 v[94:97], v[180:183], v[198:201], v[94:97]
	v_mfma_f32_16x16x32_bf16 v[86:89], v[172:175], v[206:209], v[86:89]
	v_mfma_f32_16x16x32_bf16 v[78:81], v[180:183], v[206:209], v[78:81]
	v_mfma_f32_16x16x32_bf16 v[70:73], v[172:175], v[214:217], v[70:73]
	v_mfma_f32_16x16x32_bf16 v[66:69], v[180:183], v[214:217], v[66:69]
	v_mfma_f32_16x16x32_bf16 v[118:121], v[176:179], v[192:195], v[118:121]
	v_mfma_f32_16x16x32_bf16 v[110:113], v[184:187], v[192:195], v[110:113]
	v_mfma_f32_16x16x32_bf16 v[102:105], v[176:179], v[202:205], v[102:105]
	v_mfma_f32_16x16x32_bf16 v[94:97], v[184:187], v[202:205], v[94:97]
	v_mfma_f32_16x16x32_bf16 v[86:89], v[176:179], v[210:213], v[86:89]
	v_mfma_f32_16x16x32_bf16 v[78:81], v[184:187], v[210:213], v[78:81]
	v_mfma_f32_16x16x32_bf16 v[70:73], v[176:179], v[218:221], v[70:73]
	v_mfma_f32_16x16x32_bf16 v[66:69], v[184:187], v[218:221], v[66:69]
	s_barrier
	s_add_i32 s18, s18, s43
	v_lshl_add_u64 v[160:161], v[160:161], 0, s[34:35]
	s_mov_b32 m0, s18
	ds_read_b128 v[188:191], v171 offset:49152
	ds_read_b128 v[192:195], v171 offset:50176
	ds_read_b128 v[198:201], v171 offset:51200
	ds_read_b128 v[202:205], v171 offset:52224
	ds_read_b128 v[206:209], v171 offset:53248
	ds_read_b128 v[210:213], v171 offset:54272
	ds_read_b128 v[214:217], v171 offset:55296
	ds_read_b128 v[218:221], v171 offset:56320
	global_load_lds_dwordx4 v[160:161], off
	s_add_i32 m0, s18, 0x2000
	s_add_u32 s22, s28, 0x160080
	v_lshl_add_u64 v[160:161], v[222:223], 0, s[34:35]
	s_addc_u32 s23, s29, 0
	s_add_i32 s18, s26, s43
	global_load_lds_dwordx4 v[160:161], off
	v_lshl_add_u64 v[160:161], s[22:23], 0, v[150:151]
	s_mov_b32 m0, s18
	s_nop 0
	global_load_lds_dwordx4 v[160:161], off
	v_lshl_add_u64 v[160:161], s[22:23], 0, v[154:155]
	s_add_i32 m0, s18, 0x2000
	s_nop 0
	global_load_lds_dwordx4 v[160:161], off
	v_lshl_add_u64 v[160:161], v[224:225], 0, s[34:35]
	s_mov_b32 m0, s48
	s_nop 0
	global_load_lds_dwordx4 v[160:161], off
	v_lshl_add_u64 v[160:161], v[226:227], 0, s[34:35]
	s_mov_b32 m0, s49
	s_nop 0
	global_load_lds_dwordx4 v[160:161], off
	s_waitcnt vmcnt(8)
	s_waitcnt lgkmcnt(0)
	s_barrier
	s_waitcnt lgkmcnt(0)
	v_mfma_f32_16x16x32_bf16 v[62:65], v[132:135], v[188:191], v[62:65]
	v_mfma_f32_16x16x32_bf16 v[58:61], v[140:143], v[188:191], v[58:61]
	v_mfma_f32_16x16x32_bf16 v[50:53], v[132:135], v[198:201], v[50:53]
	v_mfma_f32_16x16x32_bf16 v[42:45], v[140:143], v[198:201], v[42:45]
	v_mfma_f32_16x16x32_bf16 v[34:37], v[132:135], v[206:209], v[34:37]
	v_mfma_f32_16x16x32_bf16 v[26:29], v[140:143], v[206:209], v[26:29]
	v_mfma_f32_16x16x32_bf16 v[18:21], v[132:135], v[214:217], v[18:21]
	v_mfma_f32_16x16x32_bf16 v[10:13], v[140:143], v[214:217], v[10:13]
	v_mfma_f32_16x16x32_bf16 v[62:65], v[136:139], v[192:195], v[62:65]
	v_mfma_f32_16x16x32_bf16 v[58:61], v[144:147], v[192:195], v[58:61]
	v_mfma_f32_16x16x32_bf16 v[50:53], v[136:139], v[202:205], v[50:53]
	v_mfma_f32_16x16x32_bf16 v[42:45], v[144:147], v[202:205], v[42:45]
	v_mfma_f32_16x16x32_bf16 v[34:37], v[136:139], v[210:213], v[34:37]
	v_mfma_f32_16x16x32_bf16 v[26:29], v[144:147], v[210:213], v[26:29]
	v_mfma_f32_16x16x32_bf16 v[18:21], v[136:139], v[218:221], v[18:21]
	v_mfma_f32_16x16x32_bf16 v[10:13], v[144:147], v[218:221], v[10:13]
	v_mfma_f32_16x16x32_bf16 v[54:57], v[172:175], v[188:191], v[54:57]
	v_mfma_f32_16x16x32_bf16 v[46:49], v[180:183], v[188:191], v[46:49]
	v_mfma_f32_16x16x32_bf16 v[38:41], v[172:175], v[198:201], v[38:41]
	v_mfma_f32_16x16x32_bf16 v[30:33], v[180:183], v[198:201], v[30:33]
	v_mfma_f32_16x16x32_bf16 v[22:25], v[172:175], v[206:209], v[22:25]
	v_mfma_f32_16x16x32_bf16 v[14:17], v[180:183], v[206:209], v[14:17]
	v_mfma_f32_16x16x32_bf16 v[6:9], v[172:175], v[214:217], v[6:9]
	v_mfma_f32_16x16x32_bf16 v[2:5], v[180:183], v[214:217], v[2:5]
	v_mfma_f32_16x16x32_bf16 v[54:57], v[176:179], v[192:195], v[54:57]
	v_mfma_f32_16x16x32_bf16 v[46:49], v[184:187], v[192:195], v[46:49]
	v_mfma_f32_16x16x32_bf16 v[38:41], v[176:179], v[202:205], v[38:41]
	v_mfma_f32_16x16x32_bf16 v[30:33], v[184:187], v[202:205], v[30:33]
	v_mfma_f32_16x16x32_bf16 v[22:25], v[176:179], v[210:213], v[22:25]
	v_mfma_f32_16x16x32_bf16 v[14:17], v[184:187], v[210:213], v[14:17]
	v_mfma_f32_16x16x32_bf16 v[6:9], v[176:179], v[218:221], v[6:9]
	v_mfma_f32_16x16x32_bf16 v[2:5], v[184:187], v[218:221], v[2:5]
	s_barrier
	s_add_u32 s13, s13, 0x100
	s_addc_u32 s15, s15, 0
	s_cmp_ge_i32 s19, s2
	s_mov_b64 s[22:23], s[6:7]
	s_mov_b32 s18, s19
	s_cbranch_scc0 .LBB0_2525
	s_setprio 0
	s_and_b64 vcc, exec, s[10:11]
	s_cbranch_vccz .LBB0_2528
	s_barrier
